# prep32 B3 rewritten as 8 static per-wave variants: lin fragments register-resident, 5-deep ring of prefetched weight/bias slots with counted vmcnt waits (L2 latency no longer exposed per tile); S2 rea
# speedup vs baseline: 1.0035x; 1.0035x over previous
.LBB0_260:
	v_or_b32_e32 v0, s76, v180
	s_movk_i32 s2, 0x600
	v_mad_i64_i32 v[154:155], s[0:1], v0, s95, 0
	v_mad_i64_i32 v[156:157], s[0:1], v0, s2, 0
	v_or_b32_e32 v0, 16, v0
	v_mad_i64_i32 v[158:159], s[0:1], v0, s95, 0
	v_mad_i64_i32 v[160:161], s[0:1], v0, s2, 0
	s_mov_b32 s31, 0
	v_mov_b32_e32 v162, v230
	s_waitcnt lgkmcnt(0)
	s_barrier
	v_readlane_b32 s2, v251, 12
	v_readlane_b32 s10, v253, 60
	v_mbcnt_lo_u32_b32 v98, -1, 0
	v_mbcnt_hi_u32_b32 v98, -1, v98
	s_lshr_b32 s2, s2, 6
	s_mul_i32 s7, s10, 0x78000
	s_add_u32 s0, s36, 0x55484800
	s_addc_u32 s1, s37, 0
	s_add_u32 s0, s0, s7
	s_addc_u32 s1, s1, 0
	v_and_b32_e32 v99, 15, v98
	v_lshrrev_b32_e32 v100, 4, v98
	v_lshlrev_b32_e32 v159, 4, v100
	v_lshl_add_u32 v153, v99, 8, v159
	v_mul_u32_u24_e32 v0, 0x210, v99
	s_mov_b32 s7, 0x17600
	v_add3_u32 v0, v0, v159, s7
	v_mul_u32_u24_e32 v154, 0x300, v99
	v_lshlrev_b32_e32 v102, 3, v100
	s_mov_b32 s7, 0x1b800
	v_add3_u32 v154, v154, v102, s7
	v_or_b32_e32 v103, s76, v99
	v_mul_u32_u24_e32 v155, 0x600, v103
	v_add_u32_e32 v155, v155, v159
	v_add_u32_e32 v156, 0x6000, v155
	v_mul_u32_u24_e32 v157, 0x300, v103
	v_add_u32_e32 v157, v157, v102
	v_add_u32_e32 v158, 0x3000, v157
	s_cmp_eq_u32 s2, 1
	s_cbranch_scc1 .Lb3w_1
	s_cmp_eq_u32 s2, 2
	s_cbranch_scc1 .Lb3w_2
	s_cmp_eq_u32 s2, 3
	s_cbranch_scc1 .Lb3w_3
	s_cmp_eq_u32 s2, 4
	s_cbranch_scc1 .Lb3w_4
	s_cmp_eq_u32 s2, 5
	s_cbranch_scc1 .Lb3w_5
	s_cmp_eq_u32 s2, 6
	s_cbranch_scc1 .Lb3w_6
	s_cmp_eq_u32 s2, 7
	s_cbranch_scc1 .Lb3w_7
	ds_read_b128 v[2:5], v0 offset:0
	ds_read_b128 v[6:9], v0 offset:64
	ds_read_b128 v[10:13], v0 offset:8448
	ds_read_b128 v[14:17], v0 offset:8512
	s_add_u32 s16, s0, 0x0
	s_addc_u32 s17, s1, 0
	global_load_dwordx4 v[18:21], v153, s[16:17] offset:0
	global_load_dwordx4 v[22:25], v153, s[16:17] offset:64
	s_add_u32 s18, s68, 0x0
	s_addc_u32 s19, s69, 0
	global_load_dwordx4 v[38:41], v159, s[18:19]
	s_add_u32 s16, s0, 0x1000
	s_addc_u32 s17, s1, 0
	global_load_dwordx4 v[42:45], v153, s[16:17] offset:0
	global_load_dwordx4 v[46:49], v153, s[16:17] offset:64
	s_add_u32 s18, s68, 0x40
	s_addc_u32 s19, s69, 0
	global_load_dwordx4 v[50:53], v159, s[18:19]
	s_add_u32 s16, s0, 0x2000
	s_addc_u32 s17, s1, 0
	global_load_dwordx4 v[54:57], v153, s[16:17] offset:0
	global_load_dwordx4 v[58:61], v153, s[16:17] offset:64
	s_add_u32 s18, s68, 0x80
	s_addc_u32 s19, s69, 0
	global_load_dwordx4 v[62:65], v159, s[18:19]
	s_add_u32 s16, s0, 0x3000
	s_addc_u32 s17, s1, 0
	global_load_dwordx4 v[66:69], v153, s[16:17] offset:0
	global_load_dwordx4 v[70:73], v153, s[16:17] offset:64
	s_add_u32 s18, s68, 0xc0
	s_addc_u32 s19, s69, 0
	global_load_dwordx4 v[74:77], v159, s[18:19]
	s_add_u32 s16, s0, 0x4000
	s_addc_u32 s17, s1, 0
	global_load_dwordx4 v[78:81], v153, s[16:17] offset:0
	global_load_dwordx4 v[82:85], v153, s[16:17] offset:64
	s_add_u32 s18, s68, 0x100
	s_addc_u32 s19, s69, 0
	global_load_dwordx4 v[86:89], v159, s[18:19]
	s_waitcnt vmcnt(12) lgkmcnt(0)
	v_mfma_f32_16x16x32_bf16 v[26:29], v[18:21], v[2:5], 0
	v_mfma_f32_16x16x32_bf16 v[26:29], v[22:25], v[6:9], v[26:29]
	v_mfma_f32_16x16x32_bf16 v[30:33], v[18:21], v[10:13], 0
	v_mfma_f32_16x16x32_bf16 v[30:33], v[22:25], v[14:17], v[30:33]
	s_add_u32 s20, s56, 0x0
	s_addc_u32 s21, s57, 0
	s_nop 7
	v_pk_add_f32 v[26:27], v[26:27], v[38:39]
	v_pk_add_f32 v[28:29], v[28:29], v[40:41]
	v_pk_add_f32 v[30:31], v[30:31], v[38:39]
	v_pk_add_f32 v[32:33], v[32:33], v[40:41]
	s_add_u32 s16, s0, 0x5000
	s_addc_u32 s17, s1, 0
	global_load_dwordx4 v[18:21], v153, s[16:17] offset:0
	global_load_dwordx4 v[22:25], v153, s[16:17] offset:64
	s_add_u32 s18, s68, 0x140
	s_addc_u32 s19, s69, 0
	global_load_dwordx4 v[38:41], v159, s[18:19]
	v_mul_f32_e32 v168, 0xbfb8aa3b, v26
	v_mul_f32_e32 v169, 0xbfb8aa3b, v27
	v_mul_f32_e32 v170, 0xbfb8aa3b, v28
	v_mul_f32_e32 v171, 0xbfb8aa3b, v29
	v_exp_f32_e32 v168, v168
	v_exp_f32_e32 v169, v169
	v_exp_f32_e32 v170, v170
	v_exp_f32_e32 v171, v171
	v_add_f32_e32 v168, 1.0, v168
	v_add_f32_e32 v169, 1.0, v169
	v_add_f32_e32 v170, 1.0, v170
	v_add_f32_e32 v171, 1.0, v171
	v_rcp_f32_e32 v168, v168
	v_rcp_f32_e32 v169, v169
	v_rcp_f32_e32 v170, v170
	v_rcp_f32_e32 v171, v171
	v_mul_f32_e32 v168, 0xbf1b4598, v168
	v_mul_f32_e32 v169, 0xbf1b4598, v169
	v_mul_f32_e32 v170, 0xbf1b4598, v170
	v_mul_f32_e32 v171, 0xbf1b4598, v171
	global_store_dwordx4 v155, v[168:171], s[20:21]
	v_mul_f32_e32 v176, 0xbfb8aa3b, v30
	v_mul_f32_e32 v177, 0xbfb8aa3b, v31
	v_mul_f32_e32 v178, 0xbfb8aa3b, v32
	v_mul_f32_e32 v179, 0xbfb8aa3b, v33
	v_exp_f32_e32 v176, v176
	v_exp_f32_e32 v177, v177
	v_exp_f32_e32 v178, v178
	v_exp_f32_e32 v179, v179
	v_add_f32_e32 v176, 1.0, v176
	v_add_f32_e32 v177, 1.0, v177
	v_add_f32_e32 v178, 1.0, v178
	v_add_f32_e32 v179, 1.0, v179
	v_rcp_f32_e32 v176, v176
	v_rcp_f32_e32 v177, v177
	v_rcp_f32_e32 v178, v178
	v_rcp_f32_e32 v179, v179
	v_mul_f32_e32 v176, 0xbf1b4598, v176
	v_mul_f32_e32 v177, 0xbf1b4598, v177
	v_mul_f32_e32 v178, 0xbf1b4598, v178
	v_mul_f32_e32 v179, 0xbf1b4598, v179
	global_store_dwordx4 v156, v[176:179], s[20:21]
	s_waitcnt vmcnt(14)
	v_mfma_f32_16x16x32_bf16 v[26:29], v[42:45], v[2:5], 0
	v_mfma_f32_16x16x32_bf16 v[26:29], v[46:49], v[6:9], v[26:29]
	v_mfma_f32_16x16x32_bf16 v[30:33], v[42:45], v[10:13], 0
	v_mfma_f32_16x16x32_bf16 v[30:33], v[46:49], v[14:17], v[30:33]
	s_add_u32 s20, s56, 0x40
	s_addc_u32 s21, s57, 0
	s_nop 7
	v_pk_add_f32 v[26:27], v[26:27], v[50:51]
	v_pk_add_f32 v[28:29], v[28:29], v[52:53]
	v_pk_add_f32 v[30:31], v[30:31], v[50:51]
	v_pk_add_f32 v[32:33], v[32:33], v[52:53]
	s_add_u32 s16, s0, 0x6000
	s_addc_u32 s17, s1, 0
	global_load_dwordx4 v[42:45], v153, s[16:17] offset:0
	global_load_dwordx4 v[46:49], v153, s[16:17] offset:64
	s_add_u32 s18, s68, 0x180
	s_addc_u32 s19, s69, 0
	global_load_dwordx4 v[50:53], v159, s[18:19]
	v_mul_f32_e32 v168, 0xbfb8aa3b, v26
	v_mul_f32_e32 v169, 0xbfb8aa3b, v27
	v_mul_f32_e32 v170, 0xbfb8aa3b, v28
	v_mul_f32_e32 v171, 0xbfb8aa3b, v29
	v_exp_f32_e32 v168, v168
	v_exp_f32_e32 v169, v169
	v_exp_f32_e32 v170, v170
	v_exp_f32_e32 v171, v171
	v_add_f32_e32 v168, 1.0, v168
	v_add_f32_e32 v169, 1.0, v169
	v_add_f32_e32 v170, 1.0, v170
	v_add_f32_e32 v171, 1.0, v171
	v_rcp_f32_e32 v168, v168
	v_rcp_f32_e32 v169, v169
	v_rcp_f32_e32 v170, v170
	v_rcp_f32_e32 v171, v171
	v_mul_f32_e32 v168, 0xbf1b4598, v168
	v_mul_f32_e32 v169, 0xbf1b4598, v169
	v_mul_f32_e32 v170, 0xbf1b4598, v170
	v_mul_f32_e32 v171, 0xbf1b4598, v171
	global_store_dwordx4 v155, v[168:171], s[20:21]
	v_mul_f32_e32 v176, 0xbfb8aa3b, v30
	v_mul_f32_e32 v177, 0xbfb8aa3b, v31
	v_mul_f32_e32 v178, 0xbfb8aa3b, v32
	v_mul_f32_e32 v179, 0xbfb8aa3b, v33
	v_exp_f32_e32 v176, v176
	v_exp_f32_e32 v177, v177
	v_exp_f32_e32 v178, v178
	v_exp_f32_e32 v179, v179
	v_add_f32_e32 v176, 1.0, v176
	v_add_f32_e32 v177, 1.0, v177
	v_add_f32_e32 v178, 1.0, v178
	v_add_f32_e32 v179, 1.0, v179
	v_rcp_f32_e32 v176, v176
	v_rcp_f32_e32 v177, v177
	v_rcp_f32_e32 v178, v178
	v_rcp_f32_e32 v179, v179
	v_mul_f32_e32 v176, 0xbf1b4598, v176
	v_mul_f32_e32 v177, 0xbf1b4598, v177
	v_mul_f32_e32 v178, 0xbf1b4598, v178
	v_mul_f32_e32 v179, 0xbf1b4598, v179
	global_store_dwordx4 v156, v[176:179], s[20:21]
	s_waitcnt vmcnt(16)
	v_mfma_f32_16x16x32_bf16 v[26:29], v[54:57], v[2:5], 0
	v_mfma_f32_16x16x32_bf16 v[26:29], v[58:61], v[6:9], v[26:29]
	v_mfma_f32_16x16x32_bf16 v[30:33], v[54:57], v[10:13], 0
	v_mfma_f32_16x16x32_bf16 v[30:33], v[58:61], v[14:17], v[30:33]
	s_add_u32 s20, s56, 0x80
	s_addc_u32 s21, s57, 0
	s_nop 7
	v_pk_add_f32 v[26:27], v[26:27], v[62:63]
	v_pk_add_f32 v[28:29], v[28:29], v[64:65]
	v_pk_add_f32 v[30:31], v[30:31], v[62:63]
	v_pk_add_f32 v[32:33], v[32:33], v[64:65]
	s_add_u32 s16, s0, 0x7000
	s_addc_u32 s17, s1, 0
	global_load_dwordx4 v[54:57], v153, s[16:17] offset:0
	global_load_dwordx4 v[58:61], v153, s[16:17] offset:64
	s_add_u32 s18, s68, 0x1c0
	s_addc_u32 s19, s69, 0
	global_load_dwordx4 v[62:65], v159, s[18:19]
	v_mul_f32_e32 v168, 0xbfb8aa3b, v26
	v_mul_f32_e32 v169, 0xbfb8aa3b, v27
	v_mul_f32_e32 v170, 0xbfb8aa3b, v28
	v_mul_f32_e32 v171, 0xbfb8aa3b, v29
	v_exp_f32_e32 v168, v168
	v_exp_f32_e32 v169, v169
	v_exp_f32_e32 v170, v170
	v_exp_f32_e32 v171, v171
	v_add_f32_e32 v168, 1.0, v168
	v_add_f32_e32 v169, 1.0, v169
	v_add_f32_e32 v170, 1.0, v170
	v_add_f32_e32 v171, 1.0, v171
	v_rcp_f32_e32 v168, v168
	v_rcp_f32_e32 v169, v169
	v_rcp_f32_e32 v170, v170
	v_rcp_f32_e32 v171, v171
	v_mul_f32_e32 v168, 0xbf1b4598, v168
	v_mul_f32_e32 v169, 0xbf1b4598, v169
	v_mul_f32_e32 v170, 0xbf1b4598, v170
	v_mul_f32_e32 v171, 0xbf1b4598, v171
	global_store_dwordx4 v155, v[168:171], s[20:21]
	v_mul_f32_e32 v176, 0xbfb8aa3b, v30
	v_mul_f32_e32 v177, 0xbfb8aa3b, v31
	v_mul_f32_e32 v178, 0xbfb8aa3b, v32
	v_mul_f32_e32 v179, 0xbfb8aa3b, v33
	v_exp_f32_e32 v176, v176
	v_exp_f32_e32 v177, v177
	v_exp_f32_e32 v178, v178
	v_exp_f32_e32 v179, v179
	v_add_f32_e32 v176, 1.0, v176
	v_add_f32_e32 v177, 1.0, v177
	v_add_f32_e32 v178, 1.0, v178
	v_add_f32_e32 v179, 1.0, v179
	v_rcp_f32_e32 v176, v176
	v_rcp_f32_e32 v177, v177
	v_rcp_f32_e32 v178, v178
	v_rcp_f32_e32 v179, v179
	v_mul_f32_e32 v176, 0xbf1b4598, v176
	v_mul_f32_e32 v177, 0xbf1b4598, v177
	v_mul_f32_e32 v178, 0xbf1b4598, v178
	v_mul_f32_e32 v179, 0xbf1b4598, v179
	global_store_dwordx4 v156, v[176:179], s[20:21]
	s_waitcnt vmcnt(18)
	v_mfma_f32_16x16x32_bf16 v[26:29], v[66:69], v[2:5], 0
	v_mfma_f32_16x16x32_bf16 v[26:29], v[70:73], v[6:9], v[26:29]
	v_mfma_f32_16x16x32_bf16 v[30:33], v[66:69], v[10:13], 0
	v_mfma_f32_16x16x32_bf16 v[30:33], v[70:73], v[14:17], v[30:33]
	s_add_u32 s20, s56, 0xc0
	s_addc_u32 s21, s57, 0
	s_nop 7
	v_pk_add_f32 v[26:27], v[26:27], v[74:75]
	v_pk_add_f32 v[28:29], v[28:29], v[76:77]
	v_pk_add_f32 v[30:31], v[30:31], v[74:75]
	v_pk_add_f32 v[32:33], v[32:33], v[76:77]
	s_add_u32 s16, s0, 0x8000
	s_addc_u32 s17, s1, 0
	global_load_dwordx4 v[66:69], v153, s[16:17] offset:0
	global_load_dwordx4 v[70:73], v153, s[16:17] offset:64
	s_add_u32 s18, s68, 0x200
	s_addc_u32 s19, s69, 0
	global_load_dwordx4 v[74:77], v159, s[18:19]
	v_mul_f32_e32 v168, 0xbfb8aa3b, v26
	v_mul_f32_e32 v169, 0xbfb8aa3b, v27
	v_mul_f32_e32 v170, 0xbfb8aa3b, v28
	v_mul_f32_e32 v171, 0xbfb8aa3b, v29
	v_exp_f32_e32 v168, v168
	v_exp_f32_e32 v169, v169
	v_exp_f32_e32 v170, v170
	v_exp_f32_e32 v171, v171
	v_add_f32_e32 v168, 1.0, v168
	v_add_f32_e32 v169, 1.0, v169
	v_add_f32_e32 v170, 1.0, v170
	v_add_f32_e32 v171, 1.0, v171
	v_rcp_f32_e32 v168, v168
	v_rcp_f32_e32 v169, v169
	v_rcp_f32_e32 v170, v170
	v_rcp_f32_e32 v171, v171
	v_mul_f32_e32 v168, 0xbf1b4598, v168
	v_mul_f32_e32 v169, 0xbf1b4598, v169
	v_mul_f32_e32 v170, 0xbf1b4598, v170
	v_mul_f32_e32 v171, 0xbf1b4598, v171
	global_store_dwordx4 v155, v[168:171], s[20:21]
	v_mul_f32_e32 v176, 0xbfb8aa3b, v30
	v_mul_f32_e32 v177, 0xbfb8aa3b, v31
	v_mul_f32_e32 v178, 0xbfb8aa3b, v32
	v_mul_f32_e32 v179, 0xbfb8aa3b, v33
	v_exp_f32_e32 v176, v176
	v_exp_f32_e32 v177, v177
	v_exp_f32_e32 v178, v178
	v_exp_f32_e32 v179, v179
	v_add_f32_e32 v176, 1.0, v176
	v_add_f32_e32 v177, 1.0, v177
	v_add_f32_e32 v178, 1.0, v178
	v_add_f32_e32 v179, 1.0, v179
	v_rcp_f32_e32 v176, v176
	v_rcp_f32_e32 v177, v177
	v_rcp_f32_e32 v178, v178
	v_rcp_f32_e32 v179, v179
	v_mul_f32_e32 v176, 0xbf1b4598, v176
	v_mul_f32_e32 v177, 0xbf1b4598, v177
	v_mul_f32_e32 v178, 0xbf1b4598, v178
	v_mul_f32_e32 v179, 0xbf1b4598, v179
	global_store_dwordx4 v156, v[176:179], s[20:21]
	s_waitcnt vmcnt(20)
	v_mfma_f32_16x16x32_bf16 v[26:29], v[78:81], v[2:5], 0
	v_mfma_f32_16x16x32_bf16 v[26:29], v[82:85], v[6:9], v[26:29]
	v_mfma_f32_16x16x32_bf16 v[30:33], v[78:81], v[10:13], 0
	v_mfma_f32_16x16x32_bf16 v[30:33], v[82:85], v[14:17], v[30:33]
	s_add_u32 s20, s56, 0x100
	s_addc_u32 s21, s57, 0
	s_nop 7
	v_pk_add_f32 v[26:27], v[26:27], v[86:87]
	v_pk_add_f32 v[28:29], v[28:29], v[88:89]
	v_pk_add_f32 v[30:31], v[30:31], v[86:87]
	v_pk_add_f32 v[32:33], v[32:33], v[88:89]
	s_add_u32 s16, s0, 0x9000
	s_addc_u32 s17, s1, 0
	global_load_dwordx4 v[78:81], v153, s[16:17] offset:0
	global_load_dwordx4 v[82:85], v153, s[16:17] offset:64
	s_add_u32 s18, s68, 0x240
	s_addc_u32 s19, s69, 0
	global_load_dwordx4 v[86:89], v159, s[18:19]
	v_mul_f32_e32 v168, 0xbfb8aa3b, v26
	v_mul_f32_e32 v169, 0xbfb8aa3b, v27
	v_mul_f32_e32 v170, 0xbfb8aa3b, v28
	v_mul_f32_e32 v171, 0xbfb8aa3b, v29
	v_exp_f32_e32 v168, v168
	v_exp_f32_e32 v169, v169
	v_exp_f32_e32 v170, v170
	v_exp_f32_e32 v171, v171
	v_add_f32_e32 v168, 1.0, v168
	v_add_f32_e32 v169, 1.0, v169
	v_add_f32_e32 v170, 1.0, v170
	v_add_f32_e32 v171, 1.0, v171
	v_rcp_f32_e32 v168, v168
	v_rcp_f32_e32 v169, v169
	v_rcp_f32_e32 v170, v170
	v_rcp_f32_e32 v171, v171
	v_mul_f32_e32 v168, 0xbf1b4598, v168
	v_mul_f32_e32 v169, 0xbf1b4598, v169
	v_mul_f32_e32 v170, 0xbf1b4598, v170
	v_mul_f32_e32 v171, 0xbf1b4598, v171
	global_store_dwordx4 v155, v[168:171], s[20:21]
	v_mul_f32_e32 v176, 0xbfb8aa3b, v30
	v_mul_f32_e32 v177, 0xbfb8aa3b, v31
	v_mul_f32_e32 v178, 0xbfb8aa3b, v32
	v_mul_f32_e32 v179, 0xbfb8aa3b, v33
	v_exp_f32_e32 v176, v176
	v_exp_f32_e32 v177, v177
	v_exp_f32_e32 v178, v178
	v_exp_f32_e32 v179, v179
	v_add_f32_e32 v176, 1.0, v176
	v_add_f32_e32 v177, 1.0, v177
	v_add_f32_e32 v178, 1.0, v178
	v_add_f32_e32 v179, 1.0, v179
	v_rcp_f32_e32 v176, v176
	v_rcp_f32_e32 v177, v177
	v_rcp_f32_e32 v178, v178
	v_rcp_f32_e32 v179, v179
	v_mul_f32_e32 v176, 0xbf1b4598, v176
	v_mul_f32_e32 v177, 0xbf1b4598, v177
	v_mul_f32_e32 v178, 0xbf1b4598, v178
	v_mul_f32_e32 v179, 0xbf1b4598, v179
	global_store_dwordx4 v156, v[176:179], s[20:21]
	s_waitcnt vmcnt(22)
	v_mfma_f32_16x16x32_bf16 v[26:29], v[18:21], v[2:5], 0
	v_mfma_f32_16x16x32_bf16 v[26:29], v[22:25], v[6:9], v[26:29]
	v_mfma_f32_16x16x32_bf16 v[30:33], v[18:21], v[10:13], 0
	v_mfma_f32_16x16x32_bf16 v[30:33], v[22:25], v[14:17], v[30:33]
	s_add_u32 s20, s56, 0x140
	s_addc_u32 s21, s57, 0
	s_nop 7
	v_pk_add_f32 v[26:27], v[26:27], v[38:39]
	v_pk_add_f32 v[28:29], v[28:29], v[40:41]
	v_pk_add_f32 v[30:31], v[30:31], v[38:39]
	v_pk_add_f32 v[32:33], v[32:33], v[40:41]
	s_add_u32 s16, s0, 0xa000
	s_addc_u32 s17, s1, 0
	global_load_dwordx4 v[18:21], v153, s[16:17] offset:0
	global_load_dwordx4 v[22:25], v153, s[16:17] offset:64
	s_add_u32 s18, s68, 0x280
	s_addc_u32 s19, s69, 0
	global_load_dwordx4 v[38:41], v159, s[18:19]
	v_mul_f32_e32 v168, 0xbfb8aa3b, v26
	v_mul_f32_e32 v169, 0xbfb8aa3b, v27
	v_mul_f32_e32 v170, 0xbfb8aa3b, v28
	v_mul_f32_e32 v171, 0xbfb8aa3b, v29
	v_exp_f32_e32 v168, v168
	v_exp_f32_e32 v169, v169
	v_exp_f32_e32 v170, v170
	v_exp_f32_e32 v171, v171
	v_add_f32_e32 v168, 1.0, v168
	v_add_f32_e32 v169, 1.0, v169
	v_add_f32_e32 v170, 1.0, v170
	v_add_f32_e32 v171, 1.0, v171
	v_rcp_f32_e32 v168, v168
	v_rcp_f32_e32 v169, v169
	v_rcp_f32_e32 v170, v170
	v_rcp_f32_e32 v171, v171
	v_mul_f32_e32 v168, 0xbf1b4598, v168
	v_mul_f32_e32 v169, 0xbf1b4598, v169
	v_mul_f32_e32 v170, 0xbf1b4598, v170
	v_mul_f32_e32 v171, 0xbf1b4598, v171
	global_store_dwordx4 v155, v[168:171], s[20:21]
	v_mul_f32_e32 v176, 0xbfb8aa3b, v30
	v_mul_f32_e32 v177, 0xbfb8aa3b, v31
	v_mul_f32_e32 v178, 0xbfb8aa3b, v32
	v_mul_f32_e32 v179, 0xbfb8aa3b, v33
	v_exp_f32_e32 v176, v176
	v_exp_f32_e32 v177, v177
	v_exp_f32_e32 v178, v178
	v_exp_f32_e32 v179, v179
	v_add_f32_e32 v176, 1.0, v176
	v_add_f32_e32 v177, 1.0, v177
	v_add_f32_e32 v178, 1.0, v178
	v_add_f32_e32 v179, 1.0, v179
	v_rcp_f32_e32 v176, v176
	v_rcp_f32_e32 v177, v177
	v_rcp_f32_e32 v178, v178
	v_rcp_f32_e32 v179, v179
	v_mul_f32_e32 v176, 0xbf1b4598, v176
	v_mul_f32_e32 v177, 0xbf1b4598, v177
	v_mul_f32_e32 v178, 0xbf1b4598, v178
	v_mul_f32_e32 v179, 0xbf1b4598, v179
	global_store_dwordx4 v156, v[176:179], s[20:21]
	s_waitcnt vmcnt(22)
	v_mfma_f32_16x16x32_bf16 v[26:29], v[42:45], v[2:5], 0
	v_mfma_f32_16x16x32_bf16 v[26:29], v[46:49], v[6:9], v[26:29]
	v_mfma_f32_16x16x32_bf16 v[30:33], v[42:45], v[10:13], 0
	v_mfma_f32_16x16x32_bf16 v[30:33], v[46:49], v[14:17], v[30:33]
	s_add_u32 s20, s56, 0x180
	s_addc_u32 s21, s57, 0
	s_nop 7
	v_pk_add_f32 v[26:27], v[26:27], v[50:51]
	v_pk_add_f32 v[28:29], v[28:29], v[52:53]
	v_pk_add_f32 v[30:31], v[30:31], v[50:51]
	v_pk_add_f32 v[32:33], v[32:33], v[52:53]
	s_add_u32 s16, s0, 0xb000
	s_addc_u32 s17, s1, 0
	global_load_dwordx4 v[42:45], v153, s[16:17] offset:0
	global_load_dwordx4 v[46:49], v153, s[16:17] offset:64
	s_add_u32 s18, s68, 0x2c0
	s_addc_u32 s19, s69, 0
	global_load_dwordx4 v[50:53], v159, s[18:19]
	v_mul_f32_e32 v168, 0xbfb8aa3b, v26
	v_mul_f32_e32 v169, 0xbfb8aa3b, v27
	v_mul_f32_e32 v170, 0xbfb8aa3b, v28
	v_mul_f32_e32 v171, 0xbfb8aa3b, v29
	v_exp_f32_e32 v168, v168
	v_exp_f32_e32 v169, v169
	v_exp_f32_e32 v170, v170
	v_exp_f32_e32 v171, v171
	v_add_f32_e32 v168, 1.0, v168
	v_add_f32_e32 v169, 1.0, v169
	v_add_f32_e32 v170, 1.0, v170
	v_add_f32_e32 v171, 1.0, v171
	v_rcp_f32_e32 v168, v168
	v_rcp_f32_e32 v169, v169
	v_rcp_f32_e32 v170, v170
	v_rcp_f32_e32 v171, v171
	v_mul_f32_e32 v168, 0xbf1b4598, v168
	v_mul_f32_e32 v169, 0xbf1b4598, v169
	v_mul_f32_e32 v170, 0xbf1b4598, v170
	v_mul_f32_e32 v171, 0xbf1b4598, v171
	global_store_dwordx4 v155, v[168:171], s[20:21]
	v_mul_f32_e32 v176, 0xbfb8aa3b, v30
	v_mul_f32_e32 v177, 0xbfb8aa3b, v31
	v_mul_f32_e32 v178, 0xbfb8aa3b, v32
	v_mul_f32_e32 v179, 0xbfb8aa3b, v33
	v_exp_f32_e32 v176, v176
	v_exp_f32_e32 v177, v177
	v_exp_f32_e32 v178, v178
	v_exp_f32_e32 v179, v179
	v_add_f32_e32 v176, 1.0, v176
	v_add_f32_e32 v177, 1.0, v177
	v_add_f32_e32 v178, 1.0, v178
	v_add_f32_e32 v179, 1.0, v179
	v_rcp_f32_e32 v176, v176
	v_rcp_f32_e32 v177, v177
	v_rcp_f32_e32 v178, v178
	v_rcp_f32_e32 v179, v179
	v_mul_f32_e32 v176, 0xbf1b4598, v176
	v_mul_f32_e32 v177, 0xbf1b4598, v177
	v_mul_f32_e32 v178, 0xbf1b4598, v178
	v_mul_f32_e32 v179, 0xbf1b4598, v179
	global_store_dwordx4 v156, v[176:179], s[20:21]
	s_waitcnt vmcnt(22)
	v_mfma_f32_16x16x32_bf16 v[26:29], v[54:57], v[2:5], 0
	v_mfma_f32_16x16x32_bf16 v[26:29], v[58:61], v[6:9], v[26:29]
	v_mfma_f32_16x16x32_bf16 v[30:33], v[54:57], v[10:13], 0
	v_mfma_f32_16x16x32_bf16 v[30:33], v[58:61], v[14:17], v[30:33]
	s_add_u32 s20, s56, 0x1c0
	s_addc_u32 s21, s57, 0
	s_nop 7
	v_pk_add_f32 v[26:27], v[26:27], v[62:63]
	v_pk_add_f32 v[28:29], v[28:29], v[64:65]
	v_pk_add_f32 v[30:31], v[30:31], v[62:63]
	v_pk_add_f32 v[32:33], v[32:33], v[64:65]
	s_add_u32 s16, s0, 0xc000
	s_addc_u32 s17, s1, 0
	global_load_dwordx4 v[54:57], v153, s[16:17] offset:0
	global_load_dwordx4 v[58:61], v153, s[16:17] offset:64
	s_add_u32 s18, s68, 0x300
	s_addc_u32 s19, s69, 0
	global_load_dwordx4 v[62:65], v159, s[18:19]
	v_mul_f32_e32 v168, 0xbfb8aa3b, v26
	v_mul_f32_e32 v169, 0xbfb8aa3b, v27
	v_mul_f32_e32 v170, 0xbfb8aa3b, v28
	v_mul_f32_e32 v171, 0xbfb8aa3b, v29
	v_exp_f32_e32 v168, v168
	v_exp_f32_e32 v169, v169
	v_exp_f32_e32 v170, v170
	v_exp_f32_e32 v171, v171
	v_add_f32_e32 v168, 1.0, v168
	v_add_f32_e32 v169, 1.0, v169
	v_add_f32_e32 v170, 1.0, v170
	v_add_f32_e32 v171, 1.0, v171
	v_rcp_f32_e32 v168, v168
	v_rcp_f32_e32 v169, v169
	v_rcp_f32_e32 v170, v170
	v_rcp_f32_e32 v171, v171
	v_mul_f32_e32 v168, 0xbf1b4598, v168
	v_mul_f32_e32 v169, 0xbf1b4598, v169
	v_mul_f32_e32 v170, 0xbf1b4598, v170
	v_mul_f32_e32 v171, 0xbf1b4598, v171
	global_store_dwordx4 v155, v[168:171], s[20:21]
	v_mul_f32_e32 v176, 0xbfb8aa3b, v30
	v_mul_f32_e32 v177, 0xbfb8aa3b, v31
	v_mul_f32_e32 v178, 0xbfb8aa3b, v32
	v_mul_f32_e32 v179, 0xbfb8aa3b, v33
	v_exp_f32_e32 v176, v176
	v_exp_f32_e32 v177, v177
	v_exp_f32_e32 v178, v178
	v_exp_f32_e32 v179, v179
	v_add_f32_e32 v176, 1.0, v176
	v_add_f32_e32 v177, 1.0, v177
	v_add_f32_e32 v178, 1.0, v178
	v_add_f32_e32 v179, 1.0, v179
	v_rcp_f32_e32 v176, v176
	v_rcp_f32_e32 v177, v177
	v_rcp_f32_e32 v178, v178
	v_rcp_f32_e32 v179, v179
	v_mul_f32_e32 v176, 0xbf1b4598, v176
	v_mul_f32_e32 v177, 0xbf1b4598, v177
	v_mul_f32_e32 v178, 0xbf1b4598, v178
	v_mul_f32_e32 v179, 0xbf1b4598, v179
	global_store_dwordx4 v156, v[176:179], s[20:21]
	s_waitcnt vmcnt(22)
	v_mfma_f32_16x16x32_bf16 v[26:29], v[66:69], v[2:5], 0
	v_mfma_f32_16x16x32_bf16 v[26:29], v[70:73], v[6:9], v[26:29]
	v_mfma_f32_16x16x32_bf16 v[30:33], v[66:69], v[10:13], 0
	v_mfma_f32_16x16x32_bf16 v[30:33], v[70:73], v[14:17], v[30:33]
	s_add_u32 s20, s56, 0x200
	s_addc_u32 s21, s57, 0
	s_nop 7
	v_pk_add_f32 v[26:27], v[26:27], v[74:75]
	v_pk_add_f32 v[28:29], v[28:29], v[76:77]
	v_pk_add_f32 v[30:31], v[30:31], v[74:75]
	v_pk_add_f32 v[32:33], v[32:33], v[76:77]
	s_add_u32 s16, s0, 0xd000
	s_addc_u32 s17, s1, 0
	global_load_dwordx4 v[66:69], v153, s[16:17] offset:0
	global_load_dwordx4 v[70:73], v153, s[16:17] offset:64
	s_add_u32 s18, s68, 0x340
	s_addc_u32 s19, s69, 0
	global_load_dwordx4 v[74:77], v159, s[18:19]
	v_mul_f32_e32 v168, 0xbfb8aa3b, v26
	v_mul_f32_e32 v169, 0xbfb8aa3b, v27
	v_mul_f32_e32 v170, 0xbfb8aa3b, v28
	v_mul_f32_e32 v171, 0xbfb8aa3b, v29
	v_exp_f32_e32 v168, v168
	v_exp_f32_e32 v169, v169
	v_exp_f32_e32 v170, v170
	v_exp_f32_e32 v171, v171
	v_add_f32_e32 v168, 1.0, v168
	v_add_f32_e32 v169, 1.0, v169
	v_add_f32_e32 v170, 1.0, v170
	v_add_f32_e32 v171, 1.0, v171
	v_rcp_f32_e32 v168, v168
	v_rcp_f32_e32 v169, v169
	v_rcp_f32_e32 v170, v170
	v_rcp_f32_e32 v171, v171
	v_mul_f32_e32 v168, 0xbf1b4598, v168
	v_mul_f32_e32 v169, 0xbf1b4598, v169
	v_mul_f32_e32 v170, 0xbf1b4598, v170
	v_mul_f32_e32 v171, 0xbf1b4598, v171
	global_store_dwordx4 v155, v[168:171], s[20:21]
	v_mul_f32_e32 v176, 0xbfb8aa3b, v30
	v_mul_f32_e32 v177, 0xbfb8aa3b, v31
	v_mul_f32_e32 v178, 0xbfb8aa3b, v32
	v_mul_f32_e32 v179, 0xbfb8aa3b, v33
	v_exp_f32_e32 v176, v176
	v_exp_f32_e32 v177, v177
	v_exp_f32_e32 v178, v178
	v_exp_f32_e32 v179, v179
	v_add_f32_e32 v176, 1.0, v176
	v_add_f32_e32 v177, 1.0, v177
	v_add_f32_e32 v178, 1.0, v178
	v_add_f32_e32 v179, 1.0, v179
	v_rcp_f32_e32 v176, v176
	v_rcp_f32_e32 v177, v177
	v_rcp_f32_e32 v178, v178
	v_rcp_f32_e32 v179, v179
	v_mul_f32_e32 v176, 0xbf1b4598, v176
	v_mul_f32_e32 v177, 0xbf1b4598, v177
	v_mul_f32_e32 v178, 0xbf1b4598, v178
	v_mul_f32_e32 v179, 0xbf1b4598, v179
	global_store_dwordx4 v156, v[176:179], s[20:21]
	s_waitcnt vmcnt(22)
	v_mfma_f32_16x16x32_bf16 v[26:29], v[78:81], v[2:5], 0
	v_mfma_f32_16x16x32_bf16 v[26:29], v[82:85], v[6:9], v[26:29]
	v_mfma_f32_16x16x32_bf16 v[30:33], v[78:81], v[10:13], 0
	v_mfma_f32_16x16x32_bf16 v[30:33], v[82:85], v[14:17], v[30:33]
	s_add_u32 s20, s56, 0x240
	s_addc_u32 s21, s57, 0
	s_nop 7
	v_pk_add_f32 v[26:27], v[26:27], v[86:87]
	v_pk_add_f32 v[28:29], v[28:29], v[88:89]
	v_pk_add_f32 v[30:31], v[30:31], v[86:87]
	v_pk_add_f32 v[32:33], v[32:33], v[88:89]
	s_add_u32 s16, s0, 0xe000
	s_addc_u32 s17, s1, 0
	global_load_dwordx4 v[78:81], v153, s[16:17] offset:0
	global_load_dwordx4 v[82:85], v153, s[16:17] offset:64
	s_add_u32 s18, s68, 0x380
	s_addc_u32 s19, s69, 0
	global_load_dwordx4 v[86:89], v159, s[18:19]
	v_mul_f32_e32 v168, 0xbfb8aa3b, v26
	v_mul_f32_e32 v169, 0xbfb8aa3b, v27
	v_mul_f32_e32 v170, 0xbfb8aa3b, v28
	v_mul_f32_e32 v171, 0xbfb8aa3b, v29
	v_exp_f32_e32 v168, v168
	v_exp_f32_e32 v169, v169
	v_exp_f32_e32 v170, v170
	v_exp_f32_e32 v171, v171
	v_add_f32_e32 v168, 1.0, v168
	v_add_f32_e32 v169, 1.0, v169
	v_add_f32_e32 v170, 1.0, v170
	v_add_f32_e32 v171, 1.0, v171
	v_rcp_f32_e32 v168, v168
	v_rcp_f32_e32 v169, v169
	v_rcp_f32_e32 v170, v170
	v_rcp_f32_e32 v171, v171
	v_mul_f32_e32 v168, 0xbf1b4598, v168
	v_mul_f32_e32 v169, 0xbf1b4598, v169
	v_mul_f32_e32 v170, 0xbf1b4598, v170
	v_mul_f32_e32 v171, 0xbf1b4598, v171
	global_store_dwordx4 v155, v[168:171], s[20:21]
	v_mul_f32_e32 v176, 0xbfb8aa3b, v30
	v_mul_f32_e32 v177, 0xbfb8aa3b, v31
	v_mul_f32_e32 v178, 0xbfb8aa3b, v32
	v_mul_f32_e32 v179, 0xbfb8aa3b, v33
	v_exp_f32_e32 v176, v176
	v_exp_f32_e32 v177, v177
	v_exp_f32_e32 v178, v178
	v_exp_f32_e32 v179, v179
	v_add_f32_e32 v176, 1.0, v176
	v_add_f32_e32 v177, 1.0, v177
	v_add_f32_e32 v178, 1.0, v178
	v_add_f32_e32 v179, 1.0, v179
	v_rcp_f32_e32 v176, v176
	v_rcp_f32_e32 v177, v177
	v_rcp_f32_e32 v178, v178
	v_rcp_f32_e32 v179, v179
	v_mul_f32_e32 v176, 0xbf1b4598, v176
	v_mul_f32_e32 v177, 0xbf1b4598, v177
	v_mul_f32_e32 v178, 0xbf1b4598, v178
	v_mul_f32_e32 v179, 0xbf1b4598, v179
	global_store_dwordx4 v156, v[176:179], s[20:21]
	s_waitcnt vmcnt(22)
	v_mfma_f32_16x16x32_bf16 v[26:29], v[18:21], v[2:5], 0
	v_mfma_f32_16x16x32_bf16 v[26:29], v[22:25], v[6:9], v[26:29]
	v_mfma_f32_16x16x32_bf16 v[30:33], v[18:21], v[10:13], 0
	v_mfma_f32_16x16x32_bf16 v[30:33], v[22:25], v[14:17], v[30:33]
	s_add_u32 s20, s56, 0x280
	s_addc_u32 s21, s57, 0
	s_nop 7
	v_pk_add_f32 v[26:27], v[26:27], v[38:39]
	v_pk_add_f32 v[28:29], v[28:29], v[40:41]
	v_pk_add_f32 v[30:31], v[30:31], v[38:39]
	v_pk_add_f32 v[32:33], v[32:33], v[40:41]
	v_mul_f32_e32 v168, 0xbfb8aa3b, v26
	v_mul_f32_e32 v169, 0xbfb8aa3b, v27
	v_mul_f32_e32 v170, 0xbfb8aa3b, v28
	v_mul_f32_e32 v171, 0xbfb8aa3b, v29
	v_exp_f32_e32 v168, v168
	v_exp_f32_e32 v169, v169
	v_exp_f32_e32 v170, v170
	v_exp_f32_e32 v171, v171
	v_add_f32_e32 v168, 1.0, v168
	v_add_f32_e32 v169, 1.0, v169
	v_add_f32_e32 v170, 1.0, v170
	v_add_f32_e32 v171, 1.0, v171
	v_rcp_f32_e32 v168, v168
	v_rcp_f32_e32 v169, v169
	v_rcp_f32_e32 v170, v170
	v_rcp_f32_e32 v171, v171
	v_mul_f32_e32 v168, 0xbf1b4598, v168
	v_mul_f32_e32 v169, 0xbf1b4598, v169
	v_mul_f32_e32 v170, 0xbf1b4598, v170
	v_mul_f32_e32 v171, 0xbf1b4598, v171
	global_store_dwordx4 v155, v[168:171], s[20:21]
	v_mul_f32_e32 v176, 0xbfb8aa3b, v30
	v_mul_f32_e32 v177, 0xbfb8aa3b, v31
	v_mul_f32_e32 v178, 0xbfb8aa3b, v32
	v_mul_f32_e32 v179, 0xbfb8aa3b, v33
	v_exp_f32_e32 v176, v176
	v_exp_f32_e32 v177, v177
	v_exp_f32_e32 v178, v178
	v_exp_f32_e32 v179, v179
	v_add_f32_e32 v176, 1.0, v176
	v_add_f32_e32 v177, 1.0, v177
	v_add_f32_e32 v178, 1.0, v178
	v_add_f32_e32 v179, 1.0, v179
	v_rcp_f32_e32 v176, v176
	v_rcp_f32_e32 v177, v177
	v_rcp_f32_e32 v178, v178
	v_rcp_f32_e32 v179, v179
	v_mul_f32_e32 v176, 0xbf1b4598, v176
	v_mul_f32_e32 v177, 0xbf1b4598, v177
	v_mul_f32_e32 v178, 0xbf1b4598, v178
	v_mul_f32_e32 v179, 0xbf1b4598, v179
	global_store_dwordx4 v156, v[176:179], s[20:21]
	s_waitcnt vmcnt(19)
	v_mfma_f32_16x16x32_bf16 v[26:29], v[42:45], v[2:5], 0
	v_mfma_f32_16x16x32_bf16 v[26:29], v[46:49], v[6:9], v[26:29]
	v_mfma_f32_16x16x32_bf16 v[30:33], v[42:45], v[10:13], 0
	v_mfma_f32_16x16x32_bf16 v[30:33], v[46:49], v[14:17], v[30:33]
	s_add_u32 s20, s56, 0x2c0
	s_addc_u32 s21, s57, 0
	s_nop 7
	v_pk_add_f32 v[26:27], v[26:27], v[50:51]
	v_pk_add_f32 v[28:29], v[28:29], v[52:53]
	v_pk_add_f32 v[30:31], v[30:31], v[50:51]
	v_pk_add_f32 v[32:33], v[32:33], v[52:53]
	v_mul_f32_e32 v168, 0xbfb8aa3b, v26
	v_mul_f32_e32 v169, 0xbfb8aa3b, v27
	v_mul_f32_e32 v170, 0xbfb8aa3b, v28
	v_mul_f32_e32 v171, 0xbfb8aa3b, v29
	v_exp_f32_e32 v168, v168
	v_exp_f32_e32 v169, v169
	v_exp_f32_e32 v170, v170
	v_exp_f32_e32 v171, v171
	v_add_f32_e32 v168, 1.0, v168
	v_add_f32_e32 v169, 1.0, v169
	v_add_f32_e32 v170, 1.0, v170
	v_add_f32_e32 v171, 1.0, v171
	v_rcp_f32_e32 v168, v168
	v_rcp_f32_e32 v169, v169
	v_rcp_f32_e32 v170, v170
	v_rcp_f32_e32 v171, v171
	v_mul_f32_e32 v168, 0xbf1b4598, v168
	v_mul_f32_e32 v169, 0xbf1b4598, v169
	v_mul_f32_e32 v170, 0xbf1b4598, v170
	v_mul_f32_e32 v171, 0xbf1b4598, v171
	global_store_dwordx4 v155, v[168:171], s[20:21]
	v_mul_f32_e32 v176, 0xbfb8aa3b, v30
	v_mul_f32_e32 v177, 0xbfb8aa3b, v31
	v_mul_f32_e32 v178, 0xbfb8aa3b, v32
	v_mul_f32_e32 v179, 0xbfb8aa3b, v33
	v_exp_f32_e32 v176, v176
	v_exp_f32_e32 v177, v177
	v_exp_f32_e32 v178, v178
	v_exp_f32_e32 v179, v179
	v_add_f32_e32 v176, 1.0, v176
	v_add_f32_e32 v177, 1.0, v177
	v_add_f32_e32 v178, 1.0, v178
	v_add_f32_e32 v179, 1.0, v179
	v_rcp_f32_e32 v176, v176
	v_rcp_f32_e32 v177, v177
	v_rcp_f32_e32 v178, v178
	v_rcp_f32_e32 v179, v179
	v_mul_f32_e32 v176, 0xbf1b4598, v176
	v_mul_f32_e32 v177, 0xbf1b4598, v177
	v_mul_f32_e32 v178, 0xbf1b4598, v178
	v_mul_f32_e32 v179, 0xbf1b4598, v179
	global_store_dwordx4 v156, v[176:179], s[20:21]
	s_waitcnt vmcnt(16)
	v_mfma_f32_16x16x32_bf16 v[26:29], v[54:57], v[2:5], 0
	v_mfma_f32_16x16x32_bf16 v[26:29], v[58:61], v[6:9], v[26:29]
	v_mfma_f32_16x16x32_bf16 v[30:33], v[54:57], v[10:13], 0
	v_mfma_f32_16x16x32_bf16 v[30:33], v[58:61], v[14:17], v[30:33]
	s_add_u32 s20, s56, 0x300
	s_addc_u32 s21, s57, 0
	s_nop 7
	v_pk_add_f32 v[26:27], v[26:27], v[62:63]
	v_pk_add_f32 v[28:29], v[28:29], v[64:65]
	v_pk_add_f32 v[30:31], v[30:31], v[62:63]
	v_pk_add_f32 v[32:33], v[32:33], v[64:65]
	v_mul_f32_e32 v168, 0xbfb8aa3b, v26
	v_mul_f32_e32 v169, 0xbfb8aa3b, v27
	v_mul_f32_e32 v170, 0xbfb8aa3b, v28
	v_mul_f32_e32 v171, 0xbfb8aa3b, v29
	v_exp_f32_e32 v168, v168
	v_exp_f32_e32 v169, v169
	v_exp_f32_e32 v170, v170
	v_exp_f32_e32 v171, v171
	v_add_f32_e32 v168, 1.0, v168
	v_add_f32_e32 v169, 1.0, v169
	v_add_f32_e32 v170, 1.0, v170
	v_add_f32_e32 v171, 1.0, v171
	v_rcp_f32_e32 v168, v168
	v_rcp_f32_e32 v169, v169
	v_rcp_f32_e32 v170, v170
	v_rcp_f32_e32 v171, v171
	v_mul_f32_e32 v168, 0xbf1b4598, v168
	v_mul_f32_e32 v169, 0xbf1b4598, v169
	v_mul_f32_e32 v170, 0xbf1b4598, v170
	v_mul_f32_e32 v171, 0xbf1b4598, v171
	global_store_dwordx4 v155, v[168:171], s[20:21]
	v_mul_f32_e32 v176, 0xbfb8aa3b, v30
	v_mul_f32_e32 v177, 0xbfb8aa3b, v31
	v_mul_f32_e32 v178, 0xbfb8aa3b, v32
	v_mul_f32_e32 v179, 0xbfb8aa3b, v33
	v_exp_f32_e32 v176, v176
	v_exp_f32_e32 v177, v177
	v_exp_f32_e32 v178, v178
	v_exp_f32_e32 v179, v179
	v_add_f32_e32 v176, 1.0, v176
	v_add_f32_e32 v177, 1.0, v177
	v_add_f32_e32 v178, 1.0, v178
	v_add_f32_e32 v179, 1.0, v179
	v_rcp_f32_e32 v176, v176
	v_rcp_f32_e32 v177, v177
	v_rcp_f32_e32 v178, v178
	v_rcp_f32_e32 v179, v179
	v_mul_f32_e32 v176, 0xbf1b4598, v176
	v_mul_f32_e32 v177, 0xbf1b4598, v177
	v_mul_f32_e32 v178, 0xbf1b4598, v178
	v_mul_f32_e32 v179, 0xbf1b4598, v179
	global_store_dwordx4 v156, v[176:179], s[20:21]
	s_waitcnt vmcnt(13)
	v_mfma_f32_16x16x32_bf16 v[26:29], v[66:69], v[2:5], 0
	v_mfma_f32_16x16x32_bf16 v[26:29], v[70:73], v[6:9], v[26:29]
	v_mfma_f32_16x16x32_bf16 v[30:33], v[66:69], v[10:13], 0
	v_mfma_f32_16x16x32_bf16 v[30:33], v[70:73], v[14:17], v[30:33]
	s_add_u32 s20, s56, 0x340
	s_addc_u32 s21, s57, 0
	s_nop 7
	v_pk_add_f32 v[26:27], v[26:27], v[74:75]
	v_pk_add_f32 v[28:29], v[28:29], v[76:77]
	v_pk_add_f32 v[30:31], v[30:31], v[74:75]
	v_pk_add_f32 v[32:33], v[32:33], v[76:77]
	v_mul_f32_e32 v168, 0xbfb8aa3b, v26
	v_mul_f32_e32 v169, 0xbfb8aa3b, v27
	v_mul_f32_e32 v170, 0xbfb8aa3b, v28
	v_mul_f32_e32 v171, 0xbfb8aa3b, v29
	v_exp_f32_e32 v168, v168
	v_exp_f32_e32 v169, v169
	v_exp_f32_e32 v170, v170
	v_exp_f32_e32 v171, v171
	v_add_f32_e32 v168, 1.0, v168
	v_add_f32_e32 v169, 1.0, v169
	v_add_f32_e32 v170, 1.0, v170
	v_add_f32_e32 v171, 1.0, v171
	v_rcp_f32_e32 v168, v168
	v_rcp_f32_e32 v169, v169
	v_rcp_f32_e32 v170, v170
	v_rcp_f32_e32 v171, v171
	v_mul_f32_e32 v168, 0xbf1b4598, v168
	v_mul_f32_e32 v169, 0xbf1b4598, v169
	v_mul_f32_e32 v170, 0xbf1b4598, v170
	v_mul_f32_e32 v171, 0xbf1b4598, v171
	global_store_dwordx4 v155, v[168:171], s[20:21]
	v_mul_f32_e32 v176, 0xbfb8aa3b, v30
	v_mul_f32_e32 v177, 0xbfb8aa3b, v31
	v_mul_f32_e32 v178, 0xbfb8aa3b, v32
	v_mul_f32_e32 v179, 0xbfb8aa3b, v33
	v_exp_f32_e32 v176, v176
	v_exp_f32_e32 v177, v177
	v_exp_f32_e32 v178, v178
	v_exp_f32_e32 v179, v179
	v_add_f32_e32 v176, 1.0, v176
	v_add_f32_e32 v177, 1.0, v177
	v_add_f32_e32 v178, 1.0, v178
	v_add_f32_e32 v179, 1.0, v179
	v_rcp_f32_e32 v176, v176
	v_rcp_f32_e32 v177, v177
	v_rcp_f32_e32 v178, v178
	v_rcp_f32_e32 v179, v179
	v_mul_f32_e32 v176, 0xbf1b4598, v176
	v_mul_f32_e32 v177, 0xbf1b4598, v177
	v_mul_f32_e32 v178, 0xbf1b4598, v178
	v_mul_f32_e32 v179, 0xbf1b4598, v179
	global_store_dwordx4 v156, v[176:179], s[20:21]
	s_waitcnt vmcnt(10)
	v_mfma_f32_16x16x32_bf16 v[26:29], v[78:81], v[2:5], 0
	v_mfma_f32_16x16x32_bf16 v[26:29], v[82:85], v[6:9], v[26:29]
	v_mfma_f32_16x16x32_bf16 v[30:33], v[78:81], v[10:13], 0
	v_mfma_f32_16x16x32_bf16 v[30:33], v[82:85], v[14:17], v[30:33]
	s_add_u32 s20, s56, 0x380
	s_addc_u32 s21, s57, 0
	s_nop 7
	v_pk_add_f32 v[26:27], v[26:27], v[86:87]
	v_pk_add_f32 v[28:29], v[28:29], v[88:89]
	v_pk_add_f32 v[30:31], v[30:31], v[86:87]
	v_pk_add_f32 v[32:33], v[32:33], v[88:89]
	v_mul_f32_e32 v168, 0xbfb8aa3b, v26
	v_mul_f32_e32 v169, 0xbfb8aa3b, v27
	v_mul_f32_e32 v170, 0xbfb8aa3b, v28
	v_mul_f32_e32 v171, 0xbfb8aa3b, v29
	v_exp_f32_e32 v168, v168
	v_exp_f32_e32 v169, v169
	v_exp_f32_e32 v170, v170
	v_exp_f32_e32 v171, v171
	v_add_f32_e32 v168, 1.0, v168
	v_add_f32_e32 v169, 1.0, v169
	v_add_f32_e32 v170, 1.0, v170
	v_add_f32_e32 v171, 1.0, v171
	v_rcp_f32_e32 v168, v168
	v_rcp_f32_e32 v169, v169
	v_rcp_f32_e32 v170, v170
	v_rcp_f32_e32 v171, v171
	v_mul_f32_e32 v168, 0xbf1b4598, v168
	v_mul_f32_e32 v169, 0xbf1b4598, v169
	v_mul_f32_e32 v170, 0xbf1b4598, v170
	v_mul_f32_e32 v171, 0xbf1b4598, v171
	global_store_dwordx4 v155, v[168:171], s[20:21]
	v_mul_f32_e32 v176, 0xbfb8aa3b, v30
	v_mul_f32_e32 v177, 0xbfb8aa3b, v31
	v_mul_f32_e32 v178, 0xbfb8aa3b, v32
	v_mul_f32_e32 v179, 0xbfb8aa3b, v33
	v_exp_f32_e32 v176, v176
	v_exp_f32_e32 v177, v177
	v_exp_f32_e32 v178, v178
	v_exp_f32_e32 v179, v179
	v_add_f32_e32 v176, 1.0, v176
	v_add_f32_e32 v177, 1.0, v177
	v_add_f32_e32 v178, 1.0, v178
	v_add_f32_e32 v179, 1.0, v179
	v_rcp_f32_e32 v176, v176
	v_rcp_f32_e32 v177, v177
	v_rcp_f32_e32 v178, v178
	v_rcp_f32_e32 v179, v179
	v_mul_f32_e32 v176, 0xbf1b4598, v176
	v_mul_f32_e32 v177, 0xbf1b4598, v177
	v_mul_f32_e32 v178, 0xbf1b4598, v178
	v_mul_f32_e32 v179, 0xbf1b4598, v179
	global_store_dwordx4 v156, v[176:179], s[20:21]
	s_branch .LBB0_402
.Lb3w_1:
	ds_read_b128 v[2:5], v0 offset:0
	ds_read_b128 v[6:9], v0 offset:64
	ds_read_b128 v[10:13], v0 offset:8448
	ds_read_b128 v[14:17], v0 offset:8512
	s_add_u32 s16, s0, 0xf000
	s_addc_u32 s17, s1, 0
	global_load_dwordx4 v[18:21], v153, s[16:17] offset:0
	global_load_dwordx4 v[22:25], v153, s[16:17] offset:64
	s_add_u32 s18, s68, 0x3c0
	s_addc_u32 s19, s69, 0
	global_load_dwordx4 v[38:41], v159, s[18:19]
	s_add_u32 s16, s0, 0x10000
	s_addc_u32 s17, s1, 0
	global_load_dwordx4 v[42:45], v153, s[16:17] offset:0
	global_load_dwordx4 v[46:49], v153, s[16:17] offset:64
	s_add_u32 s18, s68, 0x400
	s_addc_u32 s19, s69, 0
	global_load_dwordx4 v[50:53], v159, s[18:19]
	s_add_u32 s16, s0, 0x11000
	s_addc_u32 s17, s1, 0
	global_load_dwordx4 v[54:57], v153, s[16:17] offset:0
	global_load_dwordx4 v[58:61], v153, s[16:17] offset:64
	s_add_u32 s18, s68, 0x440
	s_addc_u32 s19, s69, 0
	global_load_dwordx4 v[62:65], v159, s[18:19]
	s_add_u32 s16, s0, 0x12000
	s_addc_u32 s17, s1, 0
	global_load_dwordx4 v[66:69], v153, s[16:17] offset:0
	global_load_dwordx4 v[70:73], v153, s[16:17] offset:64
	s_add_u32 s18, s68, 0x480
	s_addc_u32 s19, s69, 0
	global_load_dwordx4 v[74:77], v159, s[18:19]
	s_add_u32 s16, s0, 0x13000
	s_addc_u32 s17, s1, 0
	global_load_dwordx4 v[78:81], v153, s[16:17] offset:0
	global_load_dwordx4 v[82:85], v153, s[16:17] offset:64
	s_add_u32 s18, s68, 0x4c0
	s_addc_u32 s19, s69, 0
	global_load_dwordx4 v[86:89], v159, s[18:19]
	s_waitcnt vmcnt(12) lgkmcnt(0)
	v_mfma_f32_16x16x32_bf16 v[26:29], v[18:21], v[2:5], 0
	v_mfma_f32_16x16x32_bf16 v[26:29], v[22:25], v[6:9], v[26:29]
	v_mfma_f32_16x16x32_bf16 v[30:33], v[18:21], v[10:13], 0
	v_mfma_f32_16x16x32_bf16 v[30:33], v[22:25], v[14:17], v[30:33]
	s_add_u32 s20, s56, 0x3c0
	s_addc_u32 s21, s57, 0
	s_nop 7
	v_pk_add_f32 v[26:27], v[26:27], v[38:39]
	v_pk_add_f32 v[28:29], v[28:29], v[40:41]
	v_pk_add_f32 v[30:31], v[30:31], v[38:39]
	v_pk_add_f32 v[32:33], v[32:33], v[40:41]
	s_add_u32 s16, s0, 0x14000
	s_addc_u32 s17, s1, 0
	global_load_dwordx4 v[18:21], v153, s[16:17] offset:0
	global_load_dwordx4 v[22:25], v153, s[16:17] offset:64
	s_add_u32 s18, s68, 0x500
	s_addc_u32 s19, s69, 0
	global_load_dwordx4 v[38:41], v159, s[18:19]
	v_mul_f32_e32 v168, 0xbfb8aa3b, v26
	v_mul_f32_e32 v169, 0xbfb8aa3b, v27
	v_mul_f32_e32 v170, 0xbfb8aa3b, v28
	v_mul_f32_e32 v171, 0xbfb8aa3b, v29
	v_exp_f32_e32 v168, v168
	v_exp_f32_e32 v169, v169
	v_exp_f32_e32 v170, v170
	v_exp_f32_e32 v171, v171
	v_add_f32_e32 v168, 1.0, v168
	v_add_f32_e32 v169, 1.0, v169
	v_add_f32_e32 v170, 1.0, v170
	v_add_f32_e32 v171, 1.0, v171
	v_rcp_f32_e32 v168, v168
	v_rcp_f32_e32 v169, v169
	v_rcp_f32_e32 v170, v170
	v_rcp_f32_e32 v171, v171
	v_mul_f32_e32 v168, 0xbf1b4598, v168
	v_mul_f32_e32 v169, 0xbf1b4598, v169
	v_mul_f32_e32 v170, 0xbf1b4598, v170
	v_mul_f32_e32 v171, 0xbf1b4598, v171
	global_store_dwordx4 v155, v[168:171], s[20:21]
	v_mul_f32_e32 v176, 0xbfb8aa3b, v30
	v_mul_f32_e32 v177, 0xbfb8aa3b, v31
	v_mul_f32_e32 v178, 0xbfb8aa3b, v32
	v_mul_f32_e32 v179, 0xbfb8aa3b, v33
	v_exp_f32_e32 v176, v176
	v_exp_f32_e32 v177, v177
	v_exp_f32_e32 v178, v178
	v_exp_f32_e32 v179, v179
	v_add_f32_e32 v176, 1.0, v176
	v_add_f32_e32 v177, 1.0, v177
	v_add_f32_e32 v178, 1.0, v178
	v_add_f32_e32 v179, 1.0, v179
	v_rcp_f32_e32 v176, v176
	v_rcp_f32_e32 v177, v177
	v_rcp_f32_e32 v178, v178
	v_rcp_f32_e32 v179, v179
	v_mul_f32_e32 v176, 0xbf1b4598, v176
	v_mul_f32_e32 v177, 0xbf1b4598, v177
	v_mul_f32_e32 v178, 0xbf1b4598, v178
	v_mul_f32_e32 v179, 0xbf1b4598, v179
	global_store_dwordx4 v156, v[176:179], s[20:21]
	s_waitcnt vmcnt(14)
	v_mfma_f32_16x16x32_bf16 v[26:29], v[42:45], v[2:5], 0
	v_mfma_f32_16x16x32_bf16 v[26:29], v[46:49], v[6:9], v[26:29]
	v_mfma_f32_16x16x32_bf16 v[30:33], v[42:45], v[10:13], 0
	v_mfma_f32_16x16x32_bf16 v[30:33], v[46:49], v[14:17], v[30:33]
	s_add_u32 s20, s56, 0x400
	s_addc_u32 s21, s57, 0
	s_nop 7
	v_pk_add_f32 v[26:27], v[26:27], v[50:51]
	v_pk_add_f32 v[28:29], v[28:29], v[52:53]
	v_pk_add_f32 v[30:31], v[30:31], v[50:51]
	v_pk_add_f32 v[32:33], v[32:33], v[52:53]
	s_add_u32 s16, s0, 0x15000
	s_addc_u32 s17, s1, 0
	global_load_dwordx4 v[42:45], v153, s[16:17] offset:0
	global_load_dwordx4 v[46:49], v153, s[16:17] offset:64
	s_add_u32 s18, s68, 0x540
	s_addc_u32 s19, s69, 0
	global_load_dwordx4 v[50:53], v159, s[18:19]
	v_mul_f32_e32 v168, 0xbfb8aa3b, v26
	v_mul_f32_e32 v169, 0xbfb8aa3b, v27
	v_mul_f32_e32 v170, 0xbfb8aa3b, v28
	v_mul_f32_e32 v171, 0xbfb8aa3b, v29
	v_exp_f32_e32 v168, v168
	v_exp_f32_e32 v169, v169
	v_exp_f32_e32 v170, v170
	v_exp_f32_e32 v171, v171
	v_add_f32_e32 v168, 1.0, v168
	v_add_f32_e32 v169, 1.0, v169
	v_add_f32_e32 v170, 1.0, v170
	v_add_f32_e32 v171, 1.0, v171
	v_rcp_f32_e32 v168, v168
	v_rcp_f32_e32 v169, v169
	v_rcp_f32_e32 v170, v170
	v_rcp_f32_e32 v171, v171
	v_mul_f32_e32 v168, 0xbf1b4598, v168
	v_mul_f32_e32 v169, 0xbf1b4598, v169
	v_mul_f32_e32 v170, 0xbf1b4598, v170
	v_mul_f32_e32 v171, 0xbf1b4598, v171
	global_store_dwordx4 v155, v[168:171], s[20:21]
	v_mul_f32_e32 v176, 0xbfb8aa3b, v30
	v_mul_f32_e32 v177, 0xbfb8aa3b, v31
	v_mul_f32_e32 v178, 0xbfb8aa3b, v32
	v_mul_f32_e32 v179, 0xbfb8aa3b, v33
	v_exp_f32_e32 v176, v176
	v_exp_f32_e32 v177, v177
	v_exp_f32_e32 v178, v178
	v_exp_f32_e32 v179, v179
	v_add_f32_e32 v176, 1.0, v176
	v_add_f32_e32 v177, 1.0, v177
	v_add_f32_e32 v178, 1.0, v178
	v_add_f32_e32 v179, 1.0, v179
	v_rcp_f32_e32 v176, v176
	v_rcp_f32_e32 v177, v177
	v_rcp_f32_e32 v178, v178
	v_rcp_f32_e32 v179, v179
	v_mul_f32_e32 v176, 0xbf1b4598, v176
	v_mul_f32_e32 v177, 0xbf1b4598, v177
	v_mul_f32_e32 v178, 0xbf1b4598, v178
	v_mul_f32_e32 v179, 0xbf1b4598, v179
	global_store_dwordx4 v156, v[176:179], s[20:21]
	s_waitcnt vmcnt(16)
	v_mfma_f32_16x16x32_bf16 v[26:29], v[54:57], v[2:5], 0
	v_mfma_f32_16x16x32_bf16 v[26:29], v[58:61], v[6:9], v[26:29]
	v_mfma_f32_16x16x32_bf16 v[30:33], v[54:57], v[10:13], 0
	v_mfma_f32_16x16x32_bf16 v[30:33], v[58:61], v[14:17], v[30:33]
	s_add_u32 s20, s56, 0x440
	s_addc_u32 s21, s57, 0
	s_nop 7
	v_pk_add_f32 v[26:27], v[26:27], v[62:63]
	v_pk_add_f32 v[28:29], v[28:29], v[64:65]
	v_pk_add_f32 v[30:31], v[30:31], v[62:63]
	v_pk_add_f32 v[32:33], v[32:33], v[64:65]
	s_add_u32 s16, s0, 0x16000
	s_addc_u32 s17, s1, 0
	global_load_dwordx4 v[54:57], v153, s[16:17] offset:0
	global_load_dwordx4 v[58:61], v153, s[16:17] offset:64
	s_add_u32 s18, s68, 0x580
	s_addc_u32 s19, s69, 0
	global_load_dwordx4 v[62:65], v159, s[18:19]
	v_mul_f32_e32 v168, 0xbfb8aa3b, v26
	v_mul_f32_e32 v169, 0xbfb8aa3b, v27
	v_mul_f32_e32 v170, 0xbfb8aa3b, v28
	v_mul_f32_e32 v171, 0xbfb8aa3b, v29
	v_exp_f32_e32 v168, v168
	v_exp_f32_e32 v169, v169
	v_exp_f32_e32 v170, v170
	v_exp_f32_e32 v171, v171
	v_add_f32_e32 v168, 1.0, v168
	v_add_f32_e32 v169, 1.0, v169
	v_add_f32_e32 v170, 1.0, v170
	v_add_f32_e32 v171, 1.0, v171
	v_rcp_f32_e32 v168, v168
	v_rcp_f32_e32 v169, v169
	v_rcp_f32_e32 v170, v170
	v_rcp_f32_e32 v171, v171
	v_mul_f32_e32 v168, 0xbf1b4598, v168
	v_mul_f32_e32 v169, 0xbf1b4598, v169
	v_mul_f32_e32 v170, 0xbf1b4598, v170
	v_mul_f32_e32 v171, 0xbf1b4598, v171
	global_store_dwordx4 v155, v[168:171], s[20:21]
	v_mul_f32_e32 v176, 0xbfb8aa3b, v30
	v_mul_f32_e32 v177, 0xbfb8aa3b, v31
	v_mul_f32_e32 v178, 0xbfb8aa3b, v32
	v_mul_f32_e32 v179, 0xbfb8aa3b, v33
	v_exp_f32_e32 v176, v176
	v_exp_f32_e32 v177, v177
	v_exp_f32_e32 v178, v178
	v_exp_f32_e32 v179, v179
	v_add_f32_e32 v176, 1.0, v176
	v_add_f32_e32 v177, 1.0, v177
	v_add_f32_e32 v178, 1.0, v178
	v_add_f32_e32 v179, 1.0, v179
	v_rcp_f32_e32 v176, v176
	v_rcp_f32_e32 v177, v177
	v_rcp_f32_e32 v178, v178
	v_rcp_f32_e32 v179, v179
	v_mul_f32_e32 v176, 0xbf1b4598, v176
	v_mul_f32_e32 v177, 0xbf1b4598, v177
	v_mul_f32_e32 v178, 0xbf1b4598, v178
	v_mul_f32_e32 v179, 0xbf1b4598, v179
	global_store_dwordx4 v156, v[176:179], s[20:21]
	s_waitcnt vmcnt(18)
	v_mfma_f32_16x16x32_bf16 v[26:29], v[66:69], v[2:5], 0
	v_mfma_f32_16x16x32_bf16 v[26:29], v[70:73], v[6:9], v[26:29]
	v_mfma_f32_16x16x32_bf16 v[30:33], v[66:69], v[10:13], 0
	v_mfma_f32_16x16x32_bf16 v[30:33], v[70:73], v[14:17], v[30:33]
	s_add_u32 s20, s56, 0x480
	s_addc_u32 s21, s57, 0
	s_nop 7
	v_pk_add_f32 v[26:27], v[26:27], v[74:75]
	v_pk_add_f32 v[28:29], v[28:29], v[76:77]
	v_pk_add_f32 v[30:31], v[30:31], v[74:75]
	v_pk_add_f32 v[32:33], v[32:33], v[76:77]
	s_add_u32 s16, s0, 0x17000
	s_addc_u32 s17, s1, 0
	global_load_dwordx4 v[66:69], v153, s[16:17] offset:0
	global_load_dwordx4 v[70:73], v153, s[16:17] offset:64
	s_add_u32 s18, s68, 0x5c0
	s_addc_u32 s19, s69, 0
	global_load_dwordx4 v[74:77], v159, s[18:19]
	v_mul_f32_e32 v168, 0xbfb8aa3b, v26
	v_mul_f32_e32 v169, 0xbfb8aa3b, v27
	v_mul_f32_e32 v170, 0xbfb8aa3b, v28
	v_mul_f32_e32 v171, 0xbfb8aa3b, v29
	v_exp_f32_e32 v168, v168
	v_exp_f32_e32 v169, v169
	v_exp_f32_e32 v170, v170
	v_exp_f32_e32 v171, v171
	v_add_f32_e32 v168, 1.0, v168
	v_add_f32_e32 v169, 1.0, v169
	v_add_f32_e32 v170, 1.0, v170
	v_add_f32_e32 v171, 1.0, v171
	v_rcp_f32_e32 v168, v168
	v_rcp_f32_e32 v169, v169
	v_rcp_f32_e32 v170, v170
	v_rcp_f32_e32 v171, v171
	v_mul_f32_e32 v168, 0xbf1b4598, v168
	v_mul_f32_e32 v169, 0xbf1b4598, v169
	v_mul_f32_e32 v170, 0xbf1b4598, v170
	v_mul_f32_e32 v171, 0xbf1b4598, v171
	global_store_dwordx4 v155, v[168:171], s[20:21]
	v_mul_f32_e32 v176, 0xbfb8aa3b, v30
	v_mul_f32_e32 v177, 0xbfb8aa3b, v31
	v_mul_f32_e32 v178, 0xbfb8aa3b, v32
	v_mul_f32_e32 v179, 0xbfb8aa3b, v33
	v_exp_f32_e32 v176, v176
	v_exp_f32_e32 v177, v177
	v_exp_f32_e32 v178, v178
	v_exp_f32_e32 v179, v179
	v_add_f32_e32 v176, 1.0, v176
	v_add_f32_e32 v177, 1.0, v177
	v_add_f32_e32 v178, 1.0, v178
	v_add_f32_e32 v179, 1.0, v179
	v_rcp_f32_e32 v176, v176
	v_rcp_f32_e32 v177, v177
	v_rcp_f32_e32 v178, v178
	v_rcp_f32_e32 v179, v179
	v_mul_f32_e32 v176, 0xbf1b4598, v176
	v_mul_f32_e32 v177, 0xbf1b4598, v177
	v_mul_f32_e32 v178, 0xbf1b4598, v178
	v_mul_f32_e32 v179, 0xbf1b4598, v179
	global_store_dwordx4 v156, v[176:179], s[20:21]
	s_waitcnt vmcnt(20)
	v_mfma_f32_16x16x32_bf16 v[26:29], v[78:81], v[2:5], 0
	v_mfma_f32_16x16x32_bf16 v[26:29], v[82:85], v[6:9], v[26:29]
	v_mfma_f32_16x16x32_bf16 v[30:33], v[78:81], v[10:13], 0
	v_mfma_f32_16x16x32_bf16 v[30:33], v[82:85], v[14:17], v[30:33]
	s_add_u32 s20, s56, 0x4c0
	s_addc_u32 s21, s57, 0
	s_nop 7
	v_pk_add_f32 v[26:27], v[26:27], v[86:87]
	v_pk_add_f32 v[28:29], v[28:29], v[88:89]
	v_pk_add_f32 v[30:31], v[30:31], v[86:87]
	v_pk_add_f32 v[32:33], v[32:33], v[88:89]
	s_add_u32 s16, s0, 0x18000
	s_addc_u32 s17, s1, 0
	global_load_dwordx4 v[78:81], v153, s[16:17] offset:0
	global_load_dwordx4 v[82:85], v153, s[16:17] offset:64
	s_add_u32 s18, s68, 0x600
	s_addc_u32 s19, s69, 0
	global_load_dwordx4 v[86:89], v159, s[18:19]
	v_mul_f32_e32 v168, 0xbfb8aa3b, v26
	v_mul_f32_e32 v169, 0xbfb8aa3b, v27
	v_mul_f32_e32 v170, 0xbfb8aa3b, v28
	v_mul_f32_e32 v171, 0xbfb8aa3b, v29
	v_exp_f32_e32 v168, v168
	v_exp_f32_e32 v169, v169
	v_exp_f32_e32 v170, v170
	v_exp_f32_e32 v171, v171
	v_add_f32_e32 v168, 1.0, v168
	v_add_f32_e32 v169, 1.0, v169
	v_add_f32_e32 v170, 1.0, v170
	v_add_f32_e32 v171, 1.0, v171
	v_rcp_f32_e32 v168, v168
	v_rcp_f32_e32 v169, v169
	v_rcp_f32_e32 v170, v170
	v_rcp_f32_e32 v171, v171
	v_mul_f32_e32 v168, 0xbf1b4598, v168
	v_mul_f32_e32 v169, 0xbf1b4598, v169
	v_mul_f32_e32 v170, 0xbf1b4598, v170
	v_mul_f32_e32 v171, 0xbf1b4598, v171
	global_store_dwordx4 v155, v[168:171], s[20:21]
	v_mul_f32_e32 v176, 0xbfb8aa3b, v30
	v_mul_f32_e32 v177, 0xbfb8aa3b, v31
	v_mul_f32_e32 v178, 0xbfb8aa3b, v32
	v_mul_f32_e32 v179, 0xbfb8aa3b, v33
	v_exp_f32_e32 v176, v176
	v_exp_f32_e32 v177, v177
	v_exp_f32_e32 v178, v178
	v_exp_f32_e32 v179, v179
	v_add_f32_e32 v176, 1.0, v176
	v_add_f32_e32 v177, 1.0, v177
	v_add_f32_e32 v178, 1.0, v178
	v_add_f32_e32 v179, 1.0, v179
	v_rcp_f32_e32 v176, v176
	v_rcp_f32_e32 v177, v177
	v_rcp_f32_e32 v178, v178
	v_rcp_f32_e32 v179, v179
	v_mul_f32_e32 v176, 0xbf1b4598, v176
	v_mul_f32_e32 v177, 0xbf1b4598, v177
	v_mul_f32_e32 v178, 0xbf1b4598, v178
	v_mul_f32_e32 v179, 0xbf1b4598, v179
	global_store_dwordx4 v156, v[176:179], s[20:21]
	s_waitcnt vmcnt(22)
	v_mfma_f32_16x16x32_bf16 v[26:29], v[18:21], v[2:5], 0
	v_mfma_f32_16x16x32_bf16 v[26:29], v[22:25], v[6:9], v[26:29]
	v_mfma_f32_16x16x32_bf16 v[30:33], v[18:21], v[10:13], 0
	v_mfma_f32_16x16x32_bf16 v[30:33], v[22:25], v[14:17], v[30:33]
	s_add_u32 s20, s56, 0x500
	s_addc_u32 s21, s57, 0
	s_nop 7
	v_pk_add_f32 v[26:27], v[26:27], v[38:39]
	v_pk_add_f32 v[28:29], v[28:29], v[40:41]
	v_pk_add_f32 v[30:31], v[30:31], v[38:39]
	v_pk_add_f32 v[32:33], v[32:33], v[40:41]
	s_add_u32 s16, s0, 0x19000
	s_addc_u32 s17, s1, 0
	global_load_dwordx4 v[18:21], v153, s[16:17] offset:0
	global_load_dwordx4 v[22:25], v153, s[16:17] offset:64
	s_add_u32 s18, s68, 0x640
	s_addc_u32 s19, s69, 0
	global_load_dwordx4 v[38:41], v159, s[18:19]
	v_mul_f32_e32 v168, 0xbfb8aa3b, v26
	v_mul_f32_e32 v169, 0xbfb8aa3b, v27
	v_mul_f32_e32 v170, 0xbfb8aa3b, v28
	v_mul_f32_e32 v171, 0xbfb8aa3b, v29
	v_exp_f32_e32 v168, v168
	v_exp_f32_e32 v169, v169
	v_exp_f32_e32 v170, v170
	v_exp_f32_e32 v171, v171
	v_add_f32_e32 v168, 1.0, v168
	v_add_f32_e32 v169, 1.0, v169
	v_add_f32_e32 v170, 1.0, v170
	v_add_f32_e32 v171, 1.0, v171
	v_rcp_f32_e32 v168, v168
	v_rcp_f32_e32 v169, v169
	v_rcp_f32_e32 v170, v170
	v_rcp_f32_e32 v171, v171
	v_mul_f32_e32 v168, 0xbf1b4598, v168
	v_mul_f32_e32 v169, 0xbf1b4598, v169
	v_mul_f32_e32 v170, 0xbf1b4598, v170
	v_mul_f32_e32 v171, 0xbf1b4598, v171
	global_store_dwordx4 v155, v[168:171], s[20:21]
	v_mul_f32_e32 v176, 0xbfb8aa3b, v30
	v_mul_f32_e32 v177, 0xbfb8aa3b, v31
	v_mul_f32_e32 v178, 0xbfb8aa3b, v32
	v_mul_f32_e32 v179, 0xbfb8aa3b, v33
	v_exp_f32_e32 v176, v176
	v_exp_f32_e32 v177, v177
	v_exp_f32_e32 v178, v178
	v_exp_f32_e32 v179, v179
	v_add_f32_e32 v176, 1.0, v176
	v_add_f32_e32 v177, 1.0, v177
	v_add_f32_e32 v178, 1.0, v178
	v_add_f32_e32 v179, 1.0, v179
	v_rcp_f32_e32 v176, v176
	v_rcp_f32_e32 v177, v177
	v_rcp_f32_e32 v178, v178
	v_rcp_f32_e32 v179, v179
	v_mul_f32_e32 v176, 0xbf1b4598, v176
	v_mul_f32_e32 v177, 0xbf1b4598, v177
	v_mul_f32_e32 v178, 0xbf1b4598, v178
	v_mul_f32_e32 v179, 0xbf1b4598, v179
	global_store_dwordx4 v156, v[176:179], s[20:21]
	s_waitcnt vmcnt(22)
	v_mfma_f32_16x16x32_bf16 v[26:29], v[42:45], v[2:5], 0
	v_mfma_f32_16x16x32_bf16 v[26:29], v[46:49], v[6:9], v[26:29]
	v_mfma_f32_16x16x32_bf16 v[30:33], v[42:45], v[10:13], 0
	v_mfma_f32_16x16x32_bf16 v[30:33], v[46:49], v[14:17], v[30:33]
	s_add_u32 s20, s56, 0x540
	s_addc_u32 s21, s57, 0
	s_nop 7
	v_pk_add_f32 v[26:27], v[26:27], v[50:51]
	v_pk_add_f32 v[28:29], v[28:29], v[52:53]
	v_pk_add_f32 v[30:31], v[30:31], v[50:51]
	v_pk_add_f32 v[32:33], v[32:33], v[52:53]
	s_add_u32 s16, s0, 0x1a000
	s_addc_u32 s17, s1, 0
	global_load_dwordx4 v[42:45], v153, s[16:17] offset:0
	global_load_dwordx4 v[46:49], v153, s[16:17] offset:64
	s_add_u32 s18, s68, 0x680
	s_addc_u32 s19, s69, 0
	global_load_dwordx4 v[50:53], v159, s[18:19]
	v_mul_f32_e32 v168, 0xbfb8aa3b, v26
	v_mul_f32_e32 v169, 0xbfb8aa3b, v27
	v_mul_f32_e32 v170, 0xbfb8aa3b, v28
	v_mul_f32_e32 v171, 0xbfb8aa3b, v29
	v_exp_f32_e32 v168, v168
	v_exp_f32_e32 v169, v169
	v_exp_f32_e32 v170, v170
	v_exp_f32_e32 v171, v171
	v_add_f32_e32 v168, 1.0, v168
	v_add_f32_e32 v169, 1.0, v169
	v_add_f32_e32 v170, 1.0, v170
	v_add_f32_e32 v171, 1.0, v171
	v_rcp_f32_e32 v168, v168
	v_rcp_f32_e32 v169, v169
	v_rcp_f32_e32 v170, v170
	v_rcp_f32_e32 v171, v171
	v_mul_f32_e32 v168, 0xbf1b4598, v168
	v_mul_f32_e32 v169, 0xbf1b4598, v169
	v_mul_f32_e32 v170, 0xbf1b4598, v170
	v_mul_f32_e32 v171, 0xbf1b4598, v171
	global_store_dwordx4 v155, v[168:171], s[20:21]
	v_mul_f32_e32 v176, 0xbfb8aa3b, v30
	v_mul_f32_e32 v177, 0xbfb8aa3b, v31
	v_mul_f32_e32 v178, 0xbfb8aa3b, v32
	v_mul_f32_e32 v179, 0xbfb8aa3b, v33
	v_exp_f32_e32 v176, v176
	v_exp_f32_e32 v177, v177
	v_exp_f32_e32 v178, v178
	v_exp_f32_e32 v179, v179
	v_add_f32_e32 v176, 1.0, v176
	v_add_f32_e32 v177, 1.0, v177
	v_add_f32_e32 v178, 1.0, v178
	v_add_f32_e32 v179, 1.0, v179
	v_rcp_f32_e32 v176, v176
	v_rcp_f32_e32 v177, v177
	v_rcp_f32_e32 v178, v178
	v_rcp_f32_e32 v179, v179
	v_mul_f32_e32 v176, 0xbf1b4598, v176
	v_mul_f32_e32 v177, 0xbf1b4598, v177
	v_mul_f32_e32 v178, 0xbf1b4598, v178
	v_mul_f32_e32 v179, 0xbf1b4598, v179
	global_store_dwordx4 v156, v[176:179], s[20:21]
	s_waitcnt vmcnt(22)
	v_mfma_f32_16x16x32_bf16 v[26:29], v[54:57], v[2:5], 0
	v_mfma_f32_16x16x32_bf16 v[26:29], v[58:61], v[6:9], v[26:29]
	v_mfma_f32_16x16x32_bf16 v[30:33], v[54:57], v[10:13], 0
	v_mfma_f32_16x16x32_bf16 v[30:33], v[58:61], v[14:17], v[30:33]
	s_add_u32 s20, s56, 0x580
	s_addc_u32 s21, s57, 0
	s_nop 7
	v_pk_add_f32 v[26:27], v[26:27], v[62:63]
	v_pk_add_f32 v[28:29], v[28:29], v[64:65]
	v_pk_add_f32 v[30:31], v[30:31], v[62:63]
	v_pk_add_f32 v[32:33], v[32:33], v[64:65]
	s_add_u32 s16, s0, 0x1b000
	s_addc_u32 s17, s1, 0
	global_load_dwordx4 v[54:57], v153, s[16:17] offset:0
	global_load_dwordx4 v[58:61], v153, s[16:17] offset:64
	s_add_u32 s18, s68, 0x6c0
	s_addc_u32 s19, s69, 0
	global_load_dwordx4 v[62:65], v159, s[18:19]
	v_mul_f32_e32 v168, 0xbfb8aa3b, v26
	v_mul_f32_e32 v169, 0xbfb8aa3b, v27
	v_mul_f32_e32 v170, 0xbfb8aa3b, v28
	v_mul_f32_e32 v171, 0xbfb8aa3b, v29
	v_exp_f32_e32 v168, v168
	v_exp_f32_e32 v169, v169
	v_exp_f32_e32 v170, v170
	v_exp_f32_e32 v171, v171
	v_add_f32_e32 v168, 1.0, v168
	v_add_f32_e32 v169, 1.0, v169
	v_add_f32_e32 v170, 1.0, v170
	v_add_f32_e32 v171, 1.0, v171
	v_rcp_f32_e32 v168, v168
	v_rcp_f32_e32 v169, v169
	v_rcp_f32_e32 v170, v170
	v_rcp_f32_e32 v171, v171
	v_mul_f32_e32 v168, 0xbf1b4598, v168
	v_mul_f32_e32 v169, 0xbf1b4598, v169
	v_mul_f32_e32 v170, 0xbf1b4598, v170
	v_mul_f32_e32 v171, 0xbf1b4598, v171
	global_store_dwordx4 v155, v[168:171], s[20:21]
	v_mul_f32_e32 v176, 0xbfb8aa3b, v30
	v_mul_f32_e32 v177, 0xbfb8aa3b, v31
	v_mul_f32_e32 v178, 0xbfb8aa3b, v32
	v_mul_f32_e32 v179, 0xbfb8aa3b, v33
	v_exp_f32_e32 v176, v176
	v_exp_f32_e32 v177, v177
	v_exp_f32_e32 v178, v178
	v_exp_f32_e32 v179, v179
	v_add_f32_e32 v176, 1.0, v176
	v_add_f32_e32 v177, 1.0, v177
	v_add_f32_e32 v178, 1.0, v178
	v_add_f32_e32 v179, 1.0, v179
	v_rcp_f32_e32 v176, v176
	v_rcp_f32_e32 v177, v177
	v_rcp_f32_e32 v178, v178
	v_rcp_f32_e32 v179, v179
	v_mul_f32_e32 v176, 0xbf1b4598, v176
	v_mul_f32_e32 v177, 0xbf1b4598, v177
	v_mul_f32_e32 v178, 0xbf1b4598, v178
	v_mul_f32_e32 v179, 0xbf1b4598, v179
	global_store_dwordx4 v156, v[176:179], s[20:21]
	s_waitcnt vmcnt(22)
	v_mfma_f32_16x16x32_bf16 v[26:29], v[66:69], v[2:5], 0
	v_mfma_f32_16x16x32_bf16 v[26:29], v[70:73], v[6:9], v[26:29]
	v_mfma_f32_16x16x32_bf16 v[30:33], v[66:69], v[10:13], 0
	v_mfma_f32_16x16x32_bf16 v[30:33], v[70:73], v[14:17], v[30:33]
	s_add_u32 s20, s56, 0x5c0
	s_addc_u32 s21, s57, 0
	s_nop 7
	v_pk_add_f32 v[26:27], v[26:27], v[74:75]
	v_pk_add_f32 v[28:29], v[28:29], v[76:77]
	v_pk_add_f32 v[30:31], v[30:31], v[74:75]
	v_pk_add_f32 v[32:33], v[32:33], v[76:77]
	s_add_u32 s16, s0, 0x1c000
	s_addc_u32 s17, s1, 0
	global_load_dwordx4 v[66:69], v153, s[16:17] offset:0
	global_load_dwordx4 v[70:73], v153, s[16:17] offset:64
	s_add_u32 s18, s68, 0x700
	s_addc_u32 s19, s69, 0
	global_load_dwordx4 v[74:77], v159, s[18:19]
	v_mul_f32_e32 v168, 0xbfb8aa3b, v26
	v_mul_f32_e32 v169, 0xbfb8aa3b, v27
	v_mul_f32_e32 v170, 0xbfb8aa3b, v28
	v_mul_f32_e32 v171, 0xbfb8aa3b, v29
	v_exp_f32_e32 v168, v168
	v_exp_f32_e32 v169, v169
	v_exp_f32_e32 v170, v170
	v_exp_f32_e32 v171, v171
	v_add_f32_e32 v168, 1.0, v168
	v_add_f32_e32 v169, 1.0, v169
	v_add_f32_e32 v170, 1.0, v170
	v_add_f32_e32 v171, 1.0, v171
	v_rcp_f32_e32 v168, v168
	v_rcp_f32_e32 v169, v169
	v_rcp_f32_e32 v170, v170
	v_rcp_f32_e32 v171, v171
	v_mul_f32_e32 v168, 0xbf1b4598, v168
	v_mul_f32_e32 v169, 0xbf1b4598, v169
	v_mul_f32_e32 v170, 0xbf1b4598, v170
	v_mul_f32_e32 v171, 0xbf1b4598, v171
	global_store_dwordx4 v155, v[168:171], s[20:21]
	v_mul_f32_e32 v176, 0xbfb8aa3b, v30
	v_mul_f32_e32 v177, 0xbfb8aa3b, v31
	v_mul_f32_e32 v178, 0xbfb8aa3b, v32
	v_mul_f32_e32 v179, 0xbfb8aa3b, v33
	v_exp_f32_e32 v176, v176
	v_exp_f32_e32 v177, v177
	v_exp_f32_e32 v178, v178
	v_exp_f32_e32 v179, v179
	v_add_f32_e32 v176, 1.0, v176
	v_add_f32_e32 v177, 1.0, v177
	v_add_f32_e32 v178, 1.0, v178
	v_add_f32_e32 v179, 1.0, v179
	v_rcp_f32_e32 v176, v176
	v_rcp_f32_e32 v177, v177
	v_rcp_f32_e32 v178, v178
	v_rcp_f32_e32 v179, v179
	v_mul_f32_e32 v176, 0xbf1b4598, v176
	v_mul_f32_e32 v177, 0xbf1b4598, v177
	v_mul_f32_e32 v178, 0xbf1b4598, v178
	v_mul_f32_e32 v179, 0xbf1b4598, v179
	global_store_dwordx4 v156, v[176:179], s[20:21]
	s_waitcnt vmcnt(22)
	v_mfma_f32_16x16x32_bf16 v[26:29], v[78:81], v[2:5], 0
	v_mfma_f32_16x16x32_bf16 v[26:29], v[82:85], v[6:9], v[26:29]
	v_mfma_f32_16x16x32_bf16 v[30:33], v[78:81], v[10:13], 0
	v_mfma_f32_16x16x32_bf16 v[30:33], v[82:85], v[14:17], v[30:33]
	s_add_u32 s20, s56, 0x1800000
	s_addc_u32 s21, s57, 0
	s_nop 7
	v_pk_add_f32 v[26:27], v[26:27], v[86:87]
	v_pk_add_f32 v[28:29], v[28:29], v[88:89]
	v_pk_add_f32 v[30:31], v[30:31], v[86:87]
	v_pk_add_f32 v[32:33], v[32:33], v[88:89]
	s_add_u32 s16, s0, 0x1d000
	s_addc_u32 s17, s1, 0
	global_load_dwordx4 v[78:81], v153, s[16:17] offset:0
	global_load_dwordx4 v[82:85], v153, s[16:17] offset:64
	s_add_u32 s18, s68, 0x740
	s_addc_u32 s19, s69, 0
	global_load_dwordx4 v[86:89], v159, s[18:19]
	v_mul_f32_e32 v168, 0xbfb8aa3b, v26
	v_mul_f32_e32 v169, 0xbfb8aa3b, v27
	v_mul_f32_e32 v170, 0xbfb8aa3b, v28
	v_mul_f32_e32 v171, 0xbfb8aa3b, v29
	v_exp_f32_e32 v168, v168
	v_exp_f32_e32 v169, v169
	v_exp_f32_e32 v170, v170
	v_exp_f32_e32 v171, v171
	v_add_f32_e32 v168, 1.0, v168
	v_add_f32_e32 v169, 1.0, v169
	v_add_f32_e32 v170, 1.0, v170
	v_add_f32_e32 v171, 1.0, v171
	v_rcp_f32_e32 v168, v168
	v_rcp_f32_e32 v169, v169
	v_rcp_f32_e32 v170, v170
	v_rcp_f32_e32 v171, v171
	v_mul_f32_e32 v168, 0xbf1b4598, v168
	v_mul_f32_e32 v169, 0xbf1b4598, v169
	v_mul_f32_e32 v170, 0xbf1b4598, v170
	v_mul_f32_e32 v171, 0xbf1b4598, v171
	global_store_dwordx4 v155, v[168:171], s[20:21]
	v_mul_f32_e32 v176, 0xbfb8aa3b, v30
	v_mul_f32_e32 v177, 0xbfb8aa3b, v31
	v_mul_f32_e32 v178, 0xbfb8aa3b, v32
	v_mul_f32_e32 v179, 0xbfb8aa3b, v33
	v_exp_f32_e32 v176, v176
	v_exp_f32_e32 v177, v177
	v_exp_f32_e32 v178, v178
	v_exp_f32_e32 v179, v179
	v_add_f32_e32 v176, 1.0, v176
	v_add_f32_e32 v177, 1.0, v177
	v_add_f32_e32 v178, 1.0, v178
	v_add_f32_e32 v179, 1.0, v179
	v_rcp_f32_e32 v176, v176
	v_rcp_f32_e32 v177, v177
	v_rcp_f32_e32 v178, v178
	v_rcp_f32_e32 v179, v179
	v_mul_f32_e32 v176, 0xbf1b4598, v176
	v_mul_f32_e32 v177, 0xbf1b4598, v177
	v_mul_f32_e32 v178, 0xbf1b4598, v178
	v_mul_f32_e32 v179, 0xbf1b4598, v179
	global_store_dwordx4 v156, v[176:179], s[20:21]
	s_waitcnt vmcnt(22)
	v_mfma_f32_16x16x32_bf16 v[26:29], v[18:21], v[2:5], 0
	v_mfma_f32_16x16x32_bf16 v[26:29], v[22:25], v[6:9], v[26:29]
	v_mfma_f32_16x16x32_bf16 v[30:33], v[18:21], v[10:13], 0
	v_mfma_f32_16x16x32_bf16 v[30:33], v[22:25], v[14:17], v[30:33]
	s_add_u32 s20, s56, 0x1800040
	s_addc_u32 s21, s57, 0
	s_nop 7
	v_pk_add_f32 v[26:27], v[26:27], v[38:39]
	v_pk_add_f32 v[28:29], v[28:29], v[40:41]
	v_pk_add_f32 v[30:31], v[30:31], v[38:39]
	v_pk_add_f32 v[32:33], v[32:33], v[40:41]
	v_mul_f32_e32 v168, 0xbfb8aa3b, v26
	v_mul_f32_e32 v169, 0xbfb8aa3b, v27
	v_mul_f32_e32 v170, 0xbfb8aa3b, v28
	v_mul_f32_e32 v171, 0xbfb8aa3b, v29
	v_exp_f32_e32 v168, v168
	v_exp_f32_e32 v169, v169
	v_exp_f32_e32 v170, v170
	v_exp_f32_e32 v171, v171
	v_add_f32_e32 v168, 1.0, v168
	v_add_f32_e32 v169, 1.0, v169
	v_add_f32_e32 v170, 1.0, v170
	v_add_f32_e32 v171, 1.0, v171
	v_rcp_f32_e32 v168, v168
	v_rcp_f32_e32 v169, v169
	v_rcp_f32_e32 v170, v170
	v_rcp_f32_e32 v171, v171
	v_mul_f32_e32 v168, 0xbf1b4598, v168
	v_mul_f32_e32 v169, 0xbf1b4598, v169
	v_mul_f32_e32 v170, 0xbf1b4598, v170
	v_mul_f32_e32 v171, 0xbf1b4598, v171
	global_store_dwordx4 v155, v[168:171], s[20:21]
	v_mul_f32_e32 v176, 0xbfb8aa3b, v30
	v_mul_f32_e32 v177, 0xbfb8aa3b, v31
	v_mul_f32_e32 v178, 0xbfb8aa3b, v32
	v_mul_f32_e32 v179, 0xbfb8aa3b, v33
	v_exp_f32_e32 v176, v176
	v_exp_f32_e32 v177, v177
	v_exp_f32_e32 v178, v178
	v_exp_f32_e32 v179, v179
	v_add_f32_e32 v176, 1.0, v176
	v_add_f32_e32 v177, 1.0, v177
	v_add_f32_e32 v178, 1.0, v178
	v_add_f32_e32 v179, 1.0, v179
	v_rcp_f32_e32 v176, v176
	v_rcp_f32_e32 v177, v177
	v_rcp_f32_e32 v178, v178
	v_rcp_f32_e32 v179, v179
	v_mul_f32_e32 v176, 0xbf1b4598, v176
	v_mul_f32_e32 v177, 0xbf1b4598, v177
	v_mul_f32_e32 v178, 0xbf1b4598, v178
	v_mul_f32_e32 v179, 0xbf1b4598, v179
	global_store_dwordx4 v156, v[176:179], s[20:21]
	s_waitcnt vmcnt(19)
	v_mfma_f32_16x16x32_bf16 v[26:29], v[42:45], v[2:5], 0
	v_mfma_f32_16x16x32_bf16 v[26:29], v[46:49], v[6:9], v[26:29]
	v_mfma_f32_16x16x32_bf16 v[30:33], v[42:45], v[10:13], 0
	v_mfma_f32_16x16x32_bf16 v[30:33], v[46:49], v[14:17], v[30:33]
	s_add_u32 s20, s56, 0x1800080
	s_addc_u32 s21, s57, 0
	s_nop 7
	v_pk_add_f32 v[26:27], v[26:27], v[50:51]
	v_pk_add_f32 v[28:29], v[28:29], v[52:53]
	v_pk_add_f32 v[30:31], v[30:31], v[50:51]
	v_pk_add_f32 v[32:33], v[32:33], v[52:53]
	v_mul_f32_e32 v168, 0xbfb8aa3b, v26
	v_mul_f32_e32 v169, 0xbfb8aa3b, v27
	v_mul_f32_e32 v170, 0xbfb8aa3b, v28
	v_mul_f32_e32 v171, 0xbfb8aa3b, v29
	v_exp_f32_e32 v168, v168
	v_exp_f32_e32 v169, v169
	v_exp_f32_e32 v170, v170
	v_exp_f32_e32 v171, v171
	v_add_f32_e32 v168, 1.0, v168
	v_add_f32_e32 v169, 1.0, v169
	v_add_f32_e32 v170, 1.0, v170
	v_add_f32_e32 v171, 1.0, v171
	v_rcp_f32_e32 v168, v168
	v_rcp_f32_e32 v169, v169
	v_rcp_f32_e32 v170, v170
	v_rcp_f32_e32 v171, v171
	v_mul_f32_e32 v168, 0xbf1b4598, v168
	v_mul_f32_e32 v169, 0xbf1b4598, v169
	v_mul_f32_e32 v170, 0xbf1b4598, v170
	v_mul_f32_e32 v171, 0xbf1b4598, v171
	global_store_dwordx4 v155, v[168:171], s[20:21]
	v_mul_f32_e32 v176, 0xbfb8aa3b, v30
	v_mul_f32_e32 v177, 0xbfb8aa3b, v31
	v_mul_f32_e32 v178, 0xbfb8aa3b, v32
	v_mul_f32_e32 v179, 0xbfb8aa3b, v33
	v_exp_f32_e32 v176, v176
	v_exp_f32_e32 v177, v177
	v_exp_f32_e32 v178, v178
	v_exp_f32_e32 v179, v179
	v_add_f32_e32 v176, 1.0, v176
	v_add_f32_e32 v177, 1.0, v177
	v_add_f32_e32 v178, 1.0, v178
	v_add_f32_e32 v179, 1.0, v179
	v_rcp_f32_e32 v176, v176
	v_rcp_f32_e32 v177, v177
	v_rcp_f32_e32 v178, v178
	v_rcp_f32_e32 v179, v179
	v_mul_f32_e32 v176, 0xbf1b4598, v176
	v_mul_f32_e32 v177, 0xbf1b4598, v177
	v_mul_f32_e32 v178, 0xbf1b4598, v178
	v_mul_f32_e32 v179, 0xbf1b4598, v179
	global_store_dwordx4 v156, v[176:179], s[20:21]
	s_waitcnt vmcnt(16)
	v_mfma_f32_16x16x32_bf16 v[26:29], v[54:57], v[2:5], 0
	v_mfma_f32_16x16x32_bf16 v[26:29], v[58:61], v[6:9], v[26:29]
	v_mfma_f32_16x16x32_bf16 v[30:33], v[54:57], v[10:13], 0
	v_mfma_f32_16x16x32_bf16 v[30:33], v[58:61], v[14:17], v[30:33]
	s_add_u32 s20, s56, 0x18000c0
	s_addc_u32 s21, s57, 0
	s_nop 7
	v_pk_add_f32 v[26:27], v[26:27], v[62:63]
	v_pk_add_f32 v[28:29], v[28:29], v[64:65]
	v_pk_add_f32 v[30:31], v[30:31], v[62:63]
	v_pk_add_f32 v[32:33], v[32:33], v[64:65]
	v_mul_f32_e32 v168, 0xbfb8aa3b, v26
	v_mul_f32_e32 v169, 0xbfb8aa3b, v27
	v_mul_f32_e32 v170, 0xbfb8aa3b, v28
	v_mul_f32_e32 v171, 0xbfb8aa3b, v29
	v_exp_f32_e32 v168, v168
	v_exp_f32_e32 v169, v169
	v_exp_f32_e32 v170, v170
	v_exp_f32_e32 v171, v171
	v_add_f32_e32 v168, 1.0, v168
	v_add_f32_e32 v169, 1.0, v169
	v_add_f32_e32 v170, 1.0, v170
	v_add_f32_e32 v171, 1.0, v171
	v_rcp_f32_e32 v168, v168
	v_rcp_f32_e32 v169, v169
	v_rcp_f32_e32 v170, v170
	v_rcp_f32_e32 v171, v171
	v_mul_f32_e32 v168, 0xbf1b4598, v168
	v_mul_f32_e32 v169, 0xbf1b4598, v169
	v_mul_f32_e32 v170, 0xbf1b4598, v170
	v_mul_f32_e32 v171, 0xbf1b4598, v171
	global_store_dwordx4 v155, v[168:171], s[20:21]
	v_mul_f32_e32 v176, 0xbfb8aa3b, v30
	v_mul_f32_e32 v177, 0xbfb8aa3b, v31
	v_mul_f32_e32 v178, 0xbfb8aa3b, v32
	v_mul_f32_e32 v179, 0xbfb8aa3b, v33
	v_exp_f32_e32 v176, v176
	v_exp_f32_e32 v177, v177
	v_exp_f32_e32 v178, v178
	v_exp_f32_e32 v179, v179
	v_add_f32_e32 v176, 1.0, v176
	v_add_f32_e32 v177, 1.0, v177
	v_add_f32_e32 v178, 1.0, v178
	v_add_f32_e32 v179, 1.0, v179
	v_rcp_f32_e32 v176, v176
	v_rcp_f32_e32 v177, v177
	v_rcp_f32_e32 v178, v178
	v_rcp_f32_e32 v179, v179
	v_mul_f32_e32 v176, 0xbf1b4598, v176
	v_mul_f32_e32 v177, 0xbf1b4598, v177
	v_mul_f32_e32 v178, 0xbf1b4598, v178
	v_mul_f32_e32 v179, 0xbf1b4598, v179
	global_store_dwordx4 v156, v[176:179], s[20:21]
	s_waitcnt vmcnt(13)
	v_mfma_f32_16x16x32_bf16 v[26:29], v[66:69], v[2:5], 0
	v_mfma_f32_16x16x32_bf16 v[26:29], v[70:73], v[6:9], v[26:29]
	v_mfma_f32_16x16x32_bf16 v[30:33], v[66:69], v[10:13], 0
	v_mfma_f32_16x16x32_bf16 v[30:33], v[70:73], v[14:17], v[30:33]
	s_add_u32 s20, s56, 0x1800100
	s_addc_u32 s21, s57, 0
	s_nop 7
	v_pk_add_f32 v[26:27], v[26:27], v[74:75]
	v_pk_add_f32 v[28:29], v[28:29], v[76:77]
	v_pk_add_f32 v[30:31], v[30:31], v[74:75]
	v_pk_add_f32 v[32:33], v[32:33], v[76:77]
	v_mul_f32_e32 v168, 0xbfb8aa3b, v26
	v_mul_f32_e32 v169, 0xbfb8aa3b, v27
	v_mul_f32_e32 v170, 0xbfb8aa3b, v28
	v_mul_f32_e32 v171, 0xbfb8aa3b, v29
	v_exp_f32_e32 v168, v168
	v_exp_f32_e32 v169, v169
	v_exp_f32_e32 v170, v170
	v_exp_f32_e32 v171, v171
	v_add_f32_e32 v168, 1.0, v168
	v_add_f32_e32 v169, 1.0, v169
	v_add_f32_e32 v170, 1.0, v170
	v_add_f32_e32 v171, 1.0, v171
	v_rcp_f32_e32 v168, v168
	v_rcp_f32_e32 v169, v169
	v_rcp_f32_e32 v170, v170
	v_rcp_f32_e32 v171, v171
	v_mul_f32_e32 v168, 0xbf1b4598, v168
	v_mul_f32_e32 v169, 0xbf1b4598, v169
	v_mul_f32_e32 v170, 0xbf1b4598, v170
	v_mul_f32_e32 v171, 0xbf1b4598, v171
	global_store_dwordx4 v155, v[168:171], s[20:21]
	v_mul_f32_e32 v176, 0xbfb8aa3b, v30
	v_mul_f32_e32 v177, 0xbfb8aa3b, v31
	v_mul_f32_e32 v178, 0xbfb8aa3b, v32
	v_mul_f32_e32 v179, 0xbfb8aa3b, v33
	v_exp_f32_e32 v176, v176
	v_exp_f32_e32 v177, v177
	v_exp_f32_e32 v178, v178
	v_exp_f32_e32 v179, v179
	v_add_f32_e32 v176, 1.0, v176
	v_add_f32_e32 v177, 1.0, v177
	v_add_f32_e32 v178, 1.0, v178
	v_add_f32_e32 v179, 1.0, v179
	v_rcp_f32_e32 v176, v176
	v_rcp_f32_e32 v177, v177
	v_rcp_f32_e32 v178, v178
	v_rcp_f32_e32 v179, v179
	v_mul_f32_e32 v176, 0xbf1b4598, v176
	v_mul_f32_e32 v177, 0xbf1b4598, v177
	v_mul_f32_e32 v178, 0xbf1b4598, v178
	v_mul_f32_e32 v179, 0xbf1b4598, v179
	global_store_dwordx4 v156, v[176:179], s[20:21]
	s_waitcnt vmcnt(10)
	v_mfma_f32_16x16x32_bf16 v[26:29], v[78:81], v[2:5], 0
	v_mfma_f32_16x16x32_bf16 v[26:29], v[82:85], v[6:9], v[26:29]
	v_mfma_f32_16x16x32_bf16 v[30:33], v[78:81], v[10:13], 0
	v_mfma_f32_16x16x32_bf16 v[30:33], v[82:85], v[14:17], v[30:33]
	s_add_u32 s20, s56, 0x1800140
	s_addc_u32 s21, s57, 0
	s_nop 7
	v_pk_add_f32 v[26:27], v[26:27], v[86:87]
	v_pk_add_f32 v[28:29], v[28:29], v[88:89]
	v_pk_add_f32 v[30:31], v[30:31], v[86:87]
	v_pk_add_f32 v[32:33], v[32:33], v[88:89]
	v_mul_f32_e32 v168, 0xbfb8aa3b, v26
	v_mul_f32_e32 v169, 0xbfb8aa3b, v27
	v_mul_f32_e32 v170, 0xbfb8aa3b, v28
	v_mul_f32_e32 v171, 0xbfb8aa3b, v29
	v_exp_f32_e32 v168, v168
	v_exp_f32_e32 v169, v169
	v_exp_f32_e32 v170, v170
	v_exp_f32_e32 v171, v171
	v_add_f32_e32 v168, 1.0, v168
	v_add_f32_e32 v169, 1.0, v169
	v_add_f32_e32 v170, 1.0, v170
	v_add_f32_e32 v171, 1.0, v171
	v_rcp_f32_e32 v168, v168
	v_rcp_f32_e32 v169, v169
	v_rcp_f32_e32 v170, v170
	v_rcp_f32_e32 v171, v171
	v_mul_f32_e32 v168, 0xbf1b4598, v168
	v_mul_f32_e32 v169, 0xbf1b4598, v169
	v_mul_f32_e32 v170, 0xbf1b4598, v170
	v_mul_f32_e32 v171, 0xbf1b4598, v171
	global_store_dwordx4 v155, v[168:171], s[20:21]
	v_mul_f32_e32 v176, 0xbfb8aa3b, v30
	v_mul_f32_e32 v177, 0xbfb8aa3b, v31
	v_mul_f32_e32 v178, 0xbfb8aa3b, v32
	v_mul_f32_e32 v179, 0xbfb8aa3b, v33
	v_exp_f32_e32 v176, v176
	v_exp_f32_e32 v177, v177
	v_exp_f32_e32 v178, v178
	v_exp_f32_e32 v179, v179
	v_add_f32_e32 v176, 1.0, v176
	v_add_f32_e32 v177, 1.0, v177
	v_add_f32_e32 v178, 1.0, v178
	v_add_f32_e32 v179, 1.0, v179
	v_rcp_f32_e32 v176, v176
	v_rcp_f32_e32 v177, v177
	v_rcp_f32_e32 v178, v178
	v_rcp_f32_e32 v179, v179
	v_mul_f32_e32 v176, 0xbf1b4598, v176
	v_mul_f32_e32 v177, 0xbf1b4598, v177
	v_mul_f32_e32 v178, 0xbf1b4598, v178
	v_mul_f32_e32 v179, 0xbf1b4598, v179
	global_store_dwordx4 v156, v[176:179], s[20:21]
	s_branch .LBB0_402
.Lb3w_2:
	ds_read_b128 v[2:5], v0 offset:0
	ds_read_b128 v[6:9], v0 offset:64
	ds_read_b128 v[10:13], v0 offset:8448
	ds_read_b128 v[14:17], v0 offset:8512
	s_add_u32 s16, s0, 0x1e000
	s_addc_u32 s17, s1, 0
	global_load_dwordx4 v[18:21], v153, s[16:17] offset:0
	global_load_dwordx4 v[22:25], v153, s[16:17] offset:64
	s_add_u32 s18, s68, 0x780
	s_addc_u32 s19, s69, 0
	global_load_dwordx4 v[38:41], v159, s[18:19]
	s_add_u32 s16, s0, 0x1f000
	s_addc_u32 s17, s1, 0
	global_load_dwordx4 v[42:45], v153, s[16:17] offset:0
	global_load_dwordx4 v[46:49], v153, s[16:17] offset:64
	s_add_u32 s18, s68, 0x7c0
	s_addc_u32 s19, s69, 0
	global_load_dwordx4 v[50:53], v159, s[18:19]
	s_add_u32 s16, s0, 0x20000
	s_addc_u32 s17, s1, 0
	global_load_dwordx4 v[54:57], v153, s[16:17] offset:0
	global_load_dwordx4 v[58:61], v153, s[16:17] offset:64
	s_add_u32 s18, s68, 0x800
	s_addc_u32 s19, s69, 0
	global_load_dwordx4 v[62:65], v159, s[18:19]
	s_add_u32 s16, s0, 0x21000
	s_addc_u32 s17, s1, 0
	global_load_dwordx4 v[66:69], v153, s[16:17] offset:0
	global_load_dwordx4 v[70:73], v153, s[16:17] offset:64
	s_add_u32 s18, s68, 0x840
	s_addc_u32 s19, s69, 0
	global_load_dwordx4 v[74:77], v159, s[18:19]
	s_add_u32 s16, s0, 0x22000
	s_addc_u32 s17, s1, 0
	global_load_dwordx4 v[78:81], v153, s[16:17] offset:0
	global_load_dwordx4 v[82:85], v153, s[16:17] offset:64
	s_add_u32 s18, s68, 0x880
	s_addc_u32 s19, s69, 0
	global_load_dwordx4 v[86:89], v159, s[18:19]
	s_waitcnt vmcnt(12) lgkmcnt(0)
	v_mfma_f32_16x16x32_bf16 v[26:29], v[18:21], v[2:5], 0
	v_mfma_f32_16x16x32_bf16 v[26:29], v[22:25], v[6:9], v[26:29]
	v_mfma_f32_16x16x32_bf16 v[30:33], v[18:21], v[10:13], 0
	v_mfma_f32_16x16x32_bf16 v[30:33], v[22:25], v[14:17], v[30:33]
	s_add_u32 s20, s56, 0x1800180
	s_addc_u32 s21, s57, 0
	s_nop 7
	v_pk_add_f32 v[26:27], v[26:27], v[38:39]
	v_pk_add_f32 v[28:29], v[28:29], v[40:41]
	v_pk_add_f32 v[30:31], v[30:31], v[38:39]
	v_pk_add_f32 v[32:33], v[32:33], v[40:41]
	s_add_u32 s16, s0, 0x23000
	s_addc_u32 s17, s1, 0
	global_load_dwordx4 v[18:21], v153, s[16:17] offset:0
	global_load_dwordx4 v[22:25], v153, s[16:17] offset:64
	s_add_u32 s18, s68, 0x8c0
	s_addc_u32 s19, s69, 0
	global_load_dwordx4 v[38:41], v159, s[18:19]
	v_mul_f32_e32 v168, 0xbfb8aa3b, v26
	v_mul_f32_e32 v169, 0xbfb8aa3b, v27
	v_mul_f32_e32 v170, 0xbfb8aa3b, v28
	v_mul_f32_e32 v171, 0xbfb8aa3b, v29
	v_exp_f32_e32 v168, v168
	v_exp_f32_e32 v169, v169
	v_exp_f32_e32 v170, v170
	v_exp_f32_e32 v171, v171
	v_add_f32_e32 v168, 1.0, v168
	v_add_f32_e32 v169, 1.0, v169
	v_add_f32_e32 v170, 1.0, v170
	v_add_f32_e32 v171, 1.0, v171
	v_rcp_f32_e32 v168, v168
	v_rcp_f32_e32 v169, v169
	v_rcp_f32_e32 v170, v170
	v_rcp_f32_e32 v171, v171
	v_mul_f32_e32 v168, 0xbf1b4598, v168
	v_mul_f32_e32 v169, 0xbf1b4598, v169
	v_mul_f32_e32 v170, 0xbf1b4598, v170
	v_mul_f32_e32 v171, 0xbf1b4598, v171
	global_store_dwordx4 v155, v[168:171], s[20:21]
	v_mul_f32_e32 v176, 0xbfb8aa3b, v30
	v_mul_f32_e32 v177, 0xbfb8aa3b, v31
	v_mul_f32_e32 v178, 0xbfb8aa3b, v32
	v_mul_f32_e32 v179, 0xbfb8aa3b, v33
	v_exp_f32_e32 v176, v176
	v_exp_f32_e32 v177, v177
	v_exp_f32_e32 v178, v178
	v_exp_f32_e32 v179, v179
	v_add_f32_e32 v176, 1.0, v176
	v_add_f32_e32 v177, 1.0, v177
	v_add_f32_e32 v178, 1.0, v178
	v_add_f32_e32 v179, 1.0, v179
	v_rcp_f32_e32 v176, v176
	v_rcp_f32_e32 v177, v177
	v_rcp_f32_e32 v178, v178
	v_rcp_f32_e32 v179, v179
	v_mul_f32_e32 v176, 0xbf1b4598, v176
	v_mul_f32_e32 v177, 0xbf1b4598, v177
	v_mul_f32_e32 v178, 0xbf1b4598, v178
	v_mul_f32_e32 v179, 0xbf1b4598, v179
	global_store_dwordx4 v156, v[176:179], s[20:21]
	s_waitcnt vmcnt(14)
	v_mfma_f32_16x16x32_bf16 v[26:29], v[42:45], v[2:5], 0
	v_mfma_f32_16x16x32_bf16 v[26:29], v[46:49], v[6:9], v[26:29]
	v_mfma_f32_16x16x32_bf16 v[30:33], v[42:45], v[10:13], 0
	v_mfma_f32_16x16x32_bf16 v[30:33], v[46:49], v[14:17], v[30:33]
	s_add_u32 s20, s56, 0x18001c0
	s_addc_u32 s21, s57, 0
	s_nop 7
	v_pk_add_f32 v[26:27], v[26:27], v[50:51]
	v_pk_add_f32 v[28:29], v[28:29], v[52:53]
	v_pk_add_f32 v[30:31], v[30:31], v[50:51]
	v_pk_add_f32 v[32:33], v[32:33], v[52:53]
	s_add_u32 s16, s0, 0x24000
	s_addc_u32 s17, s1, 0
	global_load_dwordx4 v[42:45], v153, s[16:17] offset:0
	global_load_dwordx4 v[46:49], v153, s[16:17] offset:64
	s_add_u32 s18, s68, 0x900
	s_addc_u32 s19, s69, 0
	global_load_dwordx4 v[50:53], v159, s[18:19]
	v_mul_f32_e32 v168, 0xbfb8aa3b, v26
	v_mul_f32_e32 v169, 0xbfb8aa3b, v27
	v_mul_f32_e32 v170, 0xbfb8aa3b, v28
	v_mul_f32_e32 v171, 0xbfb8aa3b, v29
	v_exp_f32_e32 v168, v168
	v_exp_f32_e32 v169, v169
	v_exp_f32_e32 v170, v170
	v_exp_f32_e32 v171, v171
	v_add_f32_e32 v168, 1.0, v168
	v_add_f32_e32 v169, 1.0, v169
	v_add_f32_e32 v170, 1.0, v170
	v_add_f32_e32 v171, 1.0, v171
	v_rcp_f32_e32 v168, v168
	v_rcp_f32_e32 v169, v169
	v_rcp_f32_e32 v170, v170
	v_rcp_f32_e32 v171, v171
	v_mul_f32_e32 v168, 0xbf1b4598, v168
	v_mul_f32_e32 v169, 0xbf1b4598, v169
	v_mul_f32_e32 v170, 0xbf1b4598, v170
	v_mul_f32_e32 v171, 0xbf1b4598, v171
	global_store_dwordx4 v155, v[168:171], s[20:21]
	v_mul_f32_e32 v176, 0xbfb8aa3b, v30
	v_mul_f32_e32 v177, 0xbfb8aa3b, v31
	v_mul_f32_e32 v178, 0xbfb8aa3b, v32
	v_mul_f32_e32 v179, 0xbfb8aa3b, v33
	v_exp_f32_e32 v176, v176
	v_exp_f32_e32 v177, v177
	v_exp_f32_e32 v178, v178
	v_exp_f32_e32 v179, v179
	v_add_f32_e32 v176, 1.0, v176
	v_add_f32_e32 v177, 1.0, v177
	v_add_f32_e32 v178, 1.0, v178
	v_add_f32_e32 v179, 1.0, v179
	v_rcp_f32_e32 v176, v176
	v_rcp_f32_e32 v177, v177
	v_rcp_f32_e32 v178, v178
	v_rcp_f32_e32 v179, v179
	v_mul_f32_e32 v176, 0xbf1b4598, v176
	v_mul_f32_e32 v177, 0xbf1b4598, v177
	v_mul_f32_e32 v178, 0xbf1b4598, v178
	v_mul_f32_e32 v179, 0xbf1b4598, v179
	global_store_dwordx4 v156, v[176:179], s[20:21]
	s_waitcnt vmcnt(16)
	v_mfma_f32_16x16x32_bf16 v[26:29], v[54:57], v[2:5], 0
	v_mfma_f32_16x16x32_bf16 v[26:29], v[58:61], v[6:9], v[26:29]
	v_mfma_f32_16x16x32_bf16 v[30:33], v[54:57], v[10:13], 0
	v_mfma_f32_16x16x32_bf16 v[30:33], v[58:61], v[14:17], v[30:33]
	s_add_u32 s20, s56, 0x1800200
	s_addc_u32 s21, s57, 0
	s_nop 7
	v_pk_add_f32 v[26:27], v[26:27], v[62:63]
	v_pk_add_f32 v[28:29], v[28:29], v[64:65]
	v_pk_add_f32 v[30:31], v[30:31], v[62:63]
	v_pk_add_f32 v[32:33], v[32:33], v[64:65]
	s_add_u32 s16, s0, 0x25000
	s_addc_u32 s17, s1, 0
	global_load_dwordx4 v[54:57], v153, s[16:17] offset:0
	global_load_dwordx4 v[58:61], v153, s[16:17] offset:64
	s_add_u32 s18, s68, 0x940
	s_addc_u32 s19, s69, 0
	global_load_dwordx4 v[62:65], v159, s[18:19]
	v_mul_f32_e32 v168, 0xbfb8aa3b, v26
	v_mul_f32_e32 v169, 0xbfb8aa3b, v27
	v_mul_f32_e32 v170, 0xbfb8aa3b, v28
	v_mul_f32_e32 v171, 0xbfb8aa3b, v29
	v_exp_f32_e32 v168, v168
	v_exp_f32_e32 v169, v169
	v_exp_f32_e32 v170, v170
	v_exp_f32_e32 v171, v171
	v_add_f32_e32 v168, 1.0, v168
	v_add_f32_e32 v169, 1.0, v169
	v_add_f32_e32 v170, 1.0, v170
	v_add_f32_e32 v171, 1.0, v171
	v_rcp_f32_e32 v168, v168
	v_rcp_f32_e32 v169, v169
	v_rcp_f32_e32 v170, v170
	v_rcp_f32_e32 v171, v171
	v_mul_f32_e32 v168, 0xbf1b4598, v168
	v_mul_f32_e32 v169, 0xbf1b4598, v169
	v_mul_f32_e32 v170, 0xbf1b4598, v170
	v_mul_f32_e32 v171, 0xbf1b4598, v171
	global_store_dwordx4 v155, v[168:171], s[20:21]
	v_mul_f32_e32 v176, 0xbfb8aa3b, v30
	v_mul_f32_e32 v177, 0xbfb8aa3b, v31
	v_mul_f32_e32 v178, 0xbfb8aa3b, v32
	v_mul_f32_e32 v179, 0xbfb8aa3b, v33
	v_exp_f32_e32 v176, v176
	v_exp_f32_e32 v177, v177
	v_exp_f32_e32 v178, v178
	v_exp_f32_e32 v179, v179
	v_add_f32_e32 v176, 1.0, v176
	v_add_f32_e32 v177, 1.0, v177
	v_add_f32_e32 v178, 1.0, v178
	v_add_f32_e32 v179, 1.0, v179
	v_rcp_f32_e32 v176, v176
	v_rcp_f32_e32 v177, v177
	v_rcp_f32_e32 v178, v178
	v_rcp_f32_e32 v179, v179
	v_mul_f32_e32 v176, 0xbf1b4598, v176
	v_mul_f32_e32 v177, 0xbf1b4598, v177
	v_mul_f32_e32 v178, 0xbf1b4598, v178
	v_mul_f32_e32 v179, 0xbf1b4598, v179
	global_store_dwordx4 v156, v[176:179], s[20:21]
	s_waitcnt vmcnt(18)
	v_mfma_f32_16x16x32_bf16 v[26:29], v[66:69], v[2:5], 0
	v_mfma_f32_16x16x32_bf16 v[26:29], v[70:73], v[6:9], v[26:29]
	v_mfma_f32_16x16x32_bf16 v[30:33], v[66:69], v[10:13], 0
	v_mfma_f32_16x16x32_bf16 v[30:33], v[70:73], v[14:17], v[30:33]
	s_add_u32 s20, s56, 0x1800240
	s_addc_u32 s21, s57, 0
	s_nop 7
	v_pk_add_f32 v[26:27], v[26:27], v[74:75]
	v_pk_add_f32 v[28:29], v[28:29], v[76:77]
	v_pk_add_f32 v[30:31], v[30:31], v[74:75]
	v_pk_add_f32 v[32:33], v[32:33], v[76:77]
	s_add_u32 s16, s0, 0x26000
	s_addc_u32 s17, s1, 0
	global_load_dwordx4 v[66:69], v153, s[16:17] offset:0
	global_load_dwordx4 v[70:73], v153, s[16:17] offset:64
	s_add_u32 s18, s68, 0x980
	s_addc_u32 s19, s69, 0
	global_load_dwordx4 v[74:77], v159, s[18:19]
	v_mul_f32_e32 v168, 0xbfb8aa3b, v26
	v_mul_f32_e32 v169, 0xbfb8aa3b, v27
	v_mul_f32_e32 v170, 0xbfb8aa3b, v28
	v_mul_f32_e32 v171, 0xbfb8aa3b, v29
	v_exp_f32_e32 v168, v168
	v_exp_f32_e32 v169, v169
	v_exp_f32_e32 v170, v170
	v_exp_f32_e32 v171, v171
	v_add_f32_e32 v168, 1.0, v168
	v_add_f32_e32 v169, 1.0, v169
	v_add_f32_e32 v170, 1.0, v170
	v_add_f32_e32 v171, 1.0, v171
	v_rcp_f32_e32 v168, v168
	v_rcp_f32_e32 v169, v169
	v_rcp_f32_e32 v170, v170
	v_rcp_f32_e32 v171, v171
	v_mul_f32_e32 v168, 0xbf1b4598, v168
	v_mul_f32_e32 v169, 0xbf1b4598, v169
	v_mul_f32_e32 v170, 0xbf1b4598, v170
	v_mul_f32_e32 v171, 0xbf1b4598, v171
	global_store_dwordx4 v155, v[168:171], s[20:21]
	v_mul_f32_e32 v176, 0xbfb8aa3b, v30
	v_mul_f32_e32 v177, 0xbfb8aa3b, v31
	v_mul_f32_e32 v178, 0xbfb8aa3b, v32
	v_mul_f32_e32 v179, 0xbfb8aa3b, v33
	v_exp_f32_e32 v176, v176
	v_exp_f32_e32 v177, v177
	v_exp_f32_e32 v178, v178
	v_exp_f32_e32 v179, v179
	v_add_f32_e32 v176, 1.0, v176
	v_add_f32_e32 v177, 1.0, v177
	v_add_f32_e32 v178, 1.0, v178
	v_add_f32_e32 v179, 1.0, v179
	v_rcp_f32_e32 v176, v176
	v_rcp_f32_e32 v177, v177
	v_rcp_f32_e32 v178, v178
	v_rcp_f32_e32 v179, v179
	v_mul_f32_e32 v176, 0xbf1b4598, v176
	v_mul_f32_e32 v177, 0xbf1b4598, v177
	v_mul_f32_e32 v178, 0xbf1b4598, v178
	v_mul_f32_e32 v179, 0xbf1b4598, v179
	global_store_dwordx4 v156, v[176:179], s[20:21]
	s_waitcnt vmcnt(20)
	v_mfma_f32_16x16x32_bf16 v[26:29], v[78:81], v[2:5], 0
	v_mfma_f32_16x16x32_bf16 v[26:29], v[82:85], v[6:9], v[26:29]
	v_mfma_f32_16x16x32_bf16 v[30:33], v[78:81], v[10:13], 0
	v_mfma_f32_16x16x32_bf16 v[30:33], v[82:85], v[14:17], v[30:33]
	s_add_u32 s20, s56, 0x1800280
	s_addc_u32 s21, s57, 0
	s_nop 7
	v_pk_add_f32 v[26:27], v[26:27], v[86:87]
	v_pk_add_f32 v[28:29], v[28:29], v[88:89]
	v_pk_add_f32 v[30:31], v[30:31], v[86:87]
	v_pk_add_f32 v[32:33], v[32:33], v[88:89]
	s_add_u32 s16, s0, 0x27000
	s_addc_u32 s17, s1, 0
	global_load_dwordx4 v[78:81], v153, s[16:17] offset:0
	global_load_dwordx4 v[82:85], v153, s[16:17] offset:64
	s_add_u32 s18, s68, 0x9c0
	s_addc_u32 s19, s69, 0
	global_load_dwordx4 v[86:89], v159, s[18:19]
	v_mul_f32_e32 v168, 0xbfb8aa3b, v26
	v_mul_f32_e32 v169, 0xbfb8aa3b, v27
	v_mul_f32_e32 v170, 0xbfb8aa3b, v28
	v_mul_f32_e32 v171, 0xbfb8aa3b, v29
	v_exp_f32_e32 v168, v168
	v_exp_f32_e32 v169, v169
	v_exp_f32_e32 v170, v170
	v_exp_f32_e32 v171, v171
	v_add_f32_e32 v168, 1.0, v168
	v_add_f32_e32 v169, 1.0, v169
	v_add_f32_e32 v170, 1.0, v170
	v_add_f32_e32 v171, 1.0, v171
	v_rcp_f32_e32 v168, v168
	v_rcp_f32_e32 v169, v169
	v_rcp_f32_e32 v170, v170
	v_rcp_f32_e32 v171, v171
	v_mul_f32_e32 v168, 0xbf1b4598, v168
	v_mul_f32_e32 v169, 0xbf1b4598, v169
	v_mul_f32_e32 v170, 0xbf1b4598, v170
	v_mul_f32_e32 v171, 0xbf1b4598, v171
	global_store_dwordx4 v155, v[168:171], s[20:21]
	v_mul_f32_e32 v176, 0xbfb8aa3b, v30
	v_mul_f32_e32 v177, 0xbfb8aa3b, v31
	v_mul_f32_e32 v178, 0xbfb8aa3b, v32
	v_mul_f32_e32 v179, 0xbfb8aa3b, v33
	v_exp_f32_e32 v176, v176
	v_exp_f32_e32 v177, v177
	v_exp_f32_e32 v178, v178
	v_exp_f32_e32 v179, v179
	v_add_f32_e32 v176, 1.0, v176
	v_add_f32_e32 v177, 1.0, v177
	v_add_f32_e32 v178, 1.0, v178
	v_add_f32_e32 v179, 1.0, v179
	v_rcp_f32_e32 v176, v176
	v_rcp_f32_e32 v177, v177
	v_rcp_f32_e32 v178, v178
	v_rcp_f32_e32 v179, v179
	v_mul_f32_e32 v176, 0xbf1b4598, v176
	v_mul_f32_e32 v177, 0xbf1b4598, v177
	v_mul_f32_e32 v178, 0xbf1b4598, v178
	v_mul_f32_e32 v179, 0xbf1b4598, v179
	global_store_dwordx4 v156, v[176:179], s[20:21]
	s_waitcnt vmcnt(22)
	v_mfma_f32_16x16x32_bf16 v[26:29], v[18:21], v[2:5], 0
	v_mfma_f32_16x16x32_bf16 v[26:29], v[22:25], v[6:9], v[26:29]
	v_mfma_f32_16x16x32_bf16 v[30:33], v[18:21], v[10:13], 0
	v_mfma_f32_16x16x32_bf16 v[30:33], v[22:25], v[14:17], v[30:33]
	s_add_u32 s20, s56, 0x18002c0
	s_addc_u32 s21, s57, 0
	s_nop 7
	v_pk_add_f32 v[26:27], v[26:27], v[38:39]
	v_pk_add_f32 v[28:29], v[28:29], v[40:41]
	v_pk_add_f32 v[30:31], v[30:31], v[38:39]
	v_pk_add_f32 v[32:33], v[32:33], v[40:41]
	s_add_u32 s16, s0, 0x28000
	s_addc_u32 s17, s1, 0
	global_load_dwordx4 v[18:21], v153, s[16:17] offset:0
	global_load_dwordx4 v[22:25], v153, s[16:17] offset:64
	s_add_u32 s18, s68, 0xa00
	s_addc_u32 s19, s69, 0
	global_load_dwordx4 v[38:41], v159, s[18:19]
	v_mul_f32_e32 v168, 0xbfb8aa3b, v26
	v_mul_f32_e32 v169, 0xbfb8aa3b, v27
	v_mul_f32_e32 v170, 0xbfb8aa3b, v28
	v_mul_f32_e32 v171, 0xbfb8aa3b, v29
	v_exp_f32_e32 v168, v168
	v_exp_f32_e32 v169, v169
	v_exp_f32_e32 v170, v170
	v_exp_f32_e32 v171, v171
	v_add_f32_e32 v168, 1.0, v168
	v_add_f32_e32 v169, 1.0, v169
	v_add_f32_e32 v170, 1.0, v170
	v_add_f32_e32 v171, 1.0, v171
	v_rcp_f32_e32 v168, v168
	v_rcp_f32_e32 v169, v169
	v_rcp_f32_e32 v170, v170
	v_rcp_f32_e32 v171, v171
	v_mul_f32_e32 v168, 0xbf1b4598, v168
	v_mul_f32_e32 v169, 0xbf1b4598, v169
	v_mul_f32_e32 v170, 0xbf1b4598, v170
	v_mul_f32_e32 v171, 0xbf1b4598, v171
	global_store_dwordx4 v155, v[168:171], s[20:21]
	v_mul_f32_e32 v176, 0xbfb8aa3b, v30
	v_mul_f32_e32 v177, 0xbfb8aa3b, v31
	v_mul_f32_e32 v178, 0xbfb8aa3b, v32
	v_mul_f32_e32 v179, 0xbfb8aa3b, v33
	v_exp_f32_e32 v176, v176
	v_exp_f32_e32 v177, v177
	v_exp_f32_e32 v178, v178
	v_exp_f32_e32 v179, v179
	v_add_f32_e32 v176, 1.0, v176
	v_add_f32_e32 v177, 1.0, v177
	v_add_f32_e32 v178, 1.0, v178
	v_add_f32_e32 v179, 1.0, v179
	v_rcp_f32_e32 v176, v176
	v_rcp_f32_e32 v177, v177
	v_rcp_f32_e32 v178, v178
	v_rcp_f32_e32 v179, v179
	v_mul_f32_e32 v176, 0xbf1b4598, v176
	v_mul_f32_e32 v177, 0xbf1b4598, v177
	v_mul_f32_e32 v178, 0xbf1b4598, v178
	v_mul_f32_e32 v179, 0xbf1b4598, v179
	global_store_dwordx4 v156, v[176:179], s[20:21]
	s_waitcnt vmcnt(22)
	v_mfma_f32_16x16x32_bf16 v[26:29], v[42:45], v[2:5], 0
	v_mfma_f32_16x16x32_bf16 v[26:29], v[46:49], v[6:9], v[26:29]
	v_mfma_f32_16x16x32_bf16 v[30:33], v[42:45], v[10:13], 0
	v_mfma_f32_16x16x32_bf16 v[30:33], v[46:49], v[14:17], v[30:33]
	s_add_u32 s20, s56, 0x1800300
	s_addc_u32 s21, s57, 0
	s_nop 7
	v_pk_add_f32 v[26:27], v[26:27], v[50:51]
	v_pk_add_f32 v[28:29], v[28:29], v[52:53]
	v_pk_add_f32 v[30:31], v[30:31], v[50:51]
	v_pk_add_f32 v[32:33], v[32:33], v[52:53]
	s_add_u32 s16, s0, 0x29000
	s_addc_u32 s17, s1, 0
	global_load_dwordx4 v[42:45], v153, s[16:17] offset:0
	global_load_dwordx4 v[46:49], v153, s[16:17] offset:64
	s_add_u32 s18, s68, 0xa40
	s_addc_u32 s19, s69, 0
	global_load_dwordx4 v[50:53], v159, s[18:19]
	v_mul_f32_e32 v168, 0xbfb8aa3b, v26
	v_mul_f32_e32 v169, 0xbfb8aa3b, v27
	v_mul_f32_e32 v170, 0xbfb8aa3b, v28
	v_mul_f32_e32 v171, 0xbfb8aa3b, v29
	v_exp_f32_e32 v168, v168
	v_exp_f32_e32 v169, v169
	v_exp_f32_e32 v170, v170
	v_exp_f32_e32 v171, v171
	v_add_f32_e32 v168, 1.0, v168
	v_add_f32_e32 v169, 1.0, v169
	v_add_f32_e32 v170, 1.0, v170
	v_add_f32_e32 v171, 1.0, v171
	v_rcp_f32_e32 v168, v168
	v_rcp_f32_e32 v169, v169
	v_rcp_f32_e32 v170, v170
	v_rcp_f32_e32 v171, v171
	v_mul_f32_e32 v168, 0xbf1b4598, v168
	v_mul_f32_e32 v169, 0xbf1b4598, v169
	v_mul_f32_e32 v170, 0xbf1b4598, v170
	v_mul_f32_e32 v171, 0xbf1b4598, v171
	global_store_dwordx4 v155, v[168:171], s[20:21]
	v_mul_f32_e32 v176, 0xbfb8aa3b, v30
	v_mul_f32_e32 v177, 0xbfb8aa3b, v31
	v_mul_f32_e32 v178, 0xbfb8aa3b, v32
	v_mul_f32_e32 v179, 0xbfb8aa3b, v33
	v_exp_f32_e32 v176, v176
	v_exp_f32_e32 v177, v177
	v_exp_f32_e32 v178, v178
	v_exp_f32_e32 v179, v179
	v_add_f32_e32 v176, 1.0, v176
	v_add_f32_e32 v177, 1.0, v177
	v_add_f32_e32 v178, 1.0, v178
	v_add_f32_e32 v179, 1.0, v179
	v_rcp_f32_e32 v176, v176
	v_rcp_f32_e32 v177, v177
	v_rcp_f32_e32 v178, v178
	v_rcp_f32_e32 v179, v179
	v_mul_f32_e32 v176, 0xbf1b4598, v176
	v_mul_f32_e32 v177, 0xbf1b4598, v177
	v_mul_f32_e32 v178, 0xbf1b4598, v178
	v_mul_f32_e32 v179, 0xbf1b4598, v179
	global_store_dwordx4 v156, v[176:179], s[20:21]
	s_waitcnt vmcnt(22)
	v_mfma_f32_16x16x32_bf16 v[26:29], v[54:57], v[2:5], 0
	v_mfma_f32_16x16x32_bf16 v[26:29], v[58:61], v[6:9], v[26:29]
	v_mfma_f32_16x16x32_bf16 v[30:33], v[54:57], v[10:13], 0
	v_mfma_f32_16x16x32_bf16 v[30:33], v[58:61], v[14:17], v[30:33]
	s_add_u32 s20, s56, 0x1800340
	s_addc_u32 s21, s57, 0
	s_nop 7
	v_pk_add_f32 v[26:27], v[26:27], v[62:63]
	v_pk_add_f32 v[28:29], v[28:29], v[64:65]
	v_pk_add_f32 v[30:31], v[30:31], v[62:63]
	v_pk_add_f32 v[32:33], v[32:33], v[64:65]
	s_add_u32 s16, s0, 0x2a000
	s_addc_u32 s17, s1, 0
	global_load_dwordx4 v[54:57], v153, s[16:17] offset:0
	global_load_dwordx4 v[58:61], v153, s[16:17] offset:64
	s_add_u32 s18, s68, 0xa80
	s_addc_u32 s19, s69, 0
	global_load_dwordx4 v[62:65], v159, s[18:19]
	v_mul_f32_e32 v168, 0xbfb8aa3b, v26
	v_mul_f32_e32 v169, 0xbfb8aa3b, v27
	v_mul_f32_e32 v170, 0xbfb8aa3b, v28
	v_mul_f32_e32 v171, 0xbfb8aa3b, v29
	v_exp_f32_e32 v168, v168
	v_exp_f32_e32 v169, v169
	v_exp_f32_e32 v170, v170
	v_exp_f32_e32 v171, v171
	v_add_f32_e32 v168, 1.0, v168
	v_add_f32_e32 v169, 1.0, v169
	v_add_f32_e32 v170, 1.0, v170
	v_add_f32_e32 v171, 1.0, v171
	v_rcp_f32_e32 v168, v168
	v_rcp_f32_e32 v169, v169
	v_rcp_f32_e32 v170, v170
	v_rcp_f32_e32 v171, v171
	v_mul_f32_e32 v168, 0xbf1b4598, v168
	v_mul_f32_e32 v169, 0xbf1b4598, v169
	v_mul_f32_e32 v170, 0xbf1b4598, v170
	v_mul_f32_e32 v171, 0xbf1b4598, v171
	global_store_dwordx4 v155, v[168:171], s[20:21]
	v_mul_f32_e32 v176, 0xbfb8aa3b, v30
	v_mul_f32_e32 v177, 0xbfb8aa3b, v31
	v_mul_f32_e32 v178, 0xbfb8aa3b, v32
	v_mul_f32_e32 v179, 0xbfb8aa3b, v33
	v_exp_f32_e32 v176, v176
	v_exp_f32_e32 v177, v177
	v_exp_f32_e32 v178, v178
	v_exp_f32_e32 v179, v179
	v_add_f32_e32 v176, 1.0, v176
	v_add_f32_e32 v177, 1.0, v177
	v_add_f32_e32 v178, 1.0, v178
	v_add_f32_e32 v179, 1.0, v179
	v_rcp_f32_e32 v176, v176
	v_rcp_f32_e32 v177, v177
	v_rcp_f32_e32 v178, v178
	v_rcp_f32_e32 v179, v179
	v_mul_f32_e32 v176, 0xbf1b4598, v176
	v_mul_f32_e32 v177, 0xbf1b4598, v177
	v_mul_f32_e32 v178, 0xbf1b4598, v178
	v_mul_f32_e32 v179, 0xbf1b4598, v179
	global_store_dwordx4 v156, v[176:179], s[20:21]
	s_waitcnt vmcnt(22)
	v_mfma_f32_16x16x32_bf16 v[26:29], v[66:69], v[2:5], 0
	v_mfma_f32_16x16x32_bf16 v[26:29], v[70:73], v[6:9], v[26:29]
	v_mfma_f32_16x16x32_bf16 v[30:33], v[66:69], v[10:13], 0
	v_mfma_f32_16x16x32_bf16 v[30:33], v[70:73], v[14:17], v[30:33]
	s_add_u32 s20, s56, 0x1800380
	s_addc_u32 s21, s57, 0
	s_nop 7
	v_pk_add_f32 v[26:27], v[26:27], v[74:75]
	v_pk_add_f32 v[28:29], v[28:29], v[76:77]
	v_pk_add_f32 v[30:31], v[30:31], v[74:75]
	v_pk_add_f32 v[32:33], v[32:33], v[76:77]
	s_add_u32 s16, s0, 0x2b000
	s_addc_u32 s17, s1, 0
	global_load_dwordx4 v[66:69], v153, s[16:17] offset:0
	global_load_dwordx4 v[70:73], v153, s[16:17] offset:64
	s_add_u32 s18, s68, 0xac0
	s_addc_u32 s19, s69, 0
	global_load_dwordx4 v[74:77], v159, s[18:19]
	v_mul_f32_e32 v168, 0xbfb8aa3b, v26
	v_mul_f32_e32 v169, 0xbfb8aa3b, v27
	v_mul_f32_e32 v170, 0xbfb8aa3b, v28
	v_mul_f32_e32 v171, 0xbfb8aa3b, v29
	v_exp_f32_e32 v168, v168
	v_exp_f32_e32 v169, v169
	v_exp_f32_e32 v170, v170
	v_exp_f32_e32 v171, v171
	v_add_f32_e32 v168, 1.0, v168
	v_add_f32_e32 v169, 1.0, v169
	v_add_f32_e32 v170, 1.0, v170
	v_add_f32_e32 v171, 1.0, v171
	v_rcp_f32_e32 v168, v168
	v_rcp_f32_e32 v169, v169
	v_rcp_f32_e32 v170, v170
	v_rcp_f32_e32 v171, v171
	v_mul_f32_e32 v168, 0xbf1b4598, v168
	v_mul_f32_e32 v169, 0xbf1b4598, v169
	v_mul_f32_e32 v170, 0xbf1b4598, v170
	v_mul_f32_e32 v171, 0xbf1b4598, v171
	global_store_dwordx4 v155, v[168:171], s[20:21]
	v_mul_f32_e32 v176, 0xbfb8aa3b, v30
	v_mul_f32_e32 v177, 0xbfb8aa3b, v31
	v_mul_f32_e32 v178, 0xbfb8aa3b, v32
	v_mul_f32_e32 v179, 0xbfb8aa3b, v33
	v_exp_f32_e32 v176, v176
	v_exp_f32_e32 v177, v177
	v_exp_f32_e32 v178, v178
	v_exp_f32_e32 v179, v179
	v_add_f32_e32 v176, 1.0, v176
	v_add_f32_e32 v177, 1.0, v177
	v_add_f32_e32 v178, 1.0, v178
	v_add_f32_e32 v179, 1.0, v179
	v_rcp_f32_e32 v176, v176
	v_rcp_f32_e32 v177, v177
	v_rcp_f32_e32 v178, v178
	v_rcp_f32_e32 v179, v179
	v_mul_f32_e32 v176, 0xbf1b4598, v176
	v_mul_f32_e32 v177, 0xbf1b4598, v177
	v_mul_f32_e32 v178, 0xbf1b4598, v178
	v_mul_f32_e32 v179, 0xbf1b4598, v179
	global_store_dwordx4 v156, v[176:179], s[20:21]
	s_waitcnt vmcnt(22)
	v_mfma_f32_16x16x32_bf16 v[26:29], v[78:81], v[2:5], 0
	v_mfma_f32_16x16x32_bf16 v[26:29], v[82:85], v[6:9], v[26:29]
	v_mfma_f32_16x16x32_bf16 v[30:33], v[78:81], v[10:13], 0
	v_mfma_f32_16x16x32_bf16 v[30:33], v[82:85], v[14:17], v[30:33]
	s_add_u32 s20, s56, 0x18003c0
	s_addc_u32 s21, s57, 0
	s_nop 7
	v_pk_add_f32 v[26:27], v[26:27], v[86:87]
	v_pk_add_f32 v[28:29], v[28:29], v[88:89]
	v_pk_add_f32 v[30:31], v[30:31], v[86:87]
	v_pk_add_f32 v[32:33], v[32:33], v[88:89]
	s_add_u32 s16, s0, 0x2c000
	s_addc_u32 s17, s1, 0
	global_load_dwordx4 v[78:81], v153, s[16:17] offset:0
	global_load_dwordx4 v[82:85], v153, s[16:17] offset:64
	s_add_u32 s18, s68, 0xb00
	s_addc_u32 s19, s69, 0
	global_load_dwordx4 v[86:89], v159, s[18:19]
	v_mul_f32_e32 v168, 0xbfb8aa3b, v26
	v_mul_f32_e32 v169, 0xbfb8aa3b, v27
	v_mul_f32_e32 v170, 0xbfb8aa3b, v28
	v_mul_f32_e32 v171, 0xbfb8aa3b, v29
	v_exp_f32_e32 v168, v168
	v_exp_f32_e32 v169, v169
	v_exp_f32_e32 v170, v170
	v_exp_f32_e32 v171, v171
	v_add_f32_e32 v168, 1.0, v168
	v_add_f32_e32 v169, 1.0, v169
	v_add_f32_e32 v170, 1.0, v170
	v_add_f32_e32 v171, 1.0, v171
	v_rcp_f32_e32 v168, v168
	v_rcp_f32_e32 v169, v169
	v_rcp_f32_e32 v170, v170
	v_rcp_f32_e32 v171, v171
	v_mul_f32_e32 v168, 0xbf1b4598, v168
	v_mul_f32_e32 v169, 0xbf1b4598, v169
	v_mul_f32_e32 v170, 0xbf1b4598, v170
	v_mul_f32_e32 v171, 0xbf1b4598, v171
	global_store_dwordx4 v155, v[168:171], s[20:21]
	v_mul_f32_e32 v176, 0xbfb8aa3b, v30
	v_mul_f32_e32 v177, 0xbfb8aa3b, v31
	v_mul_f32_e32 v178, 0xbfb8aa3b, v32
	v_mul_f32_e32 v179, 0xbfb8aa3b, v33
	v_exp_f32_e32 v176, v176
	v_exp_f32_e32 v177, v177
	v_exp_f32_e32 v178, v178
	v_exp_f32_e32 v179, v179
	v_add_f32_e32 v176, 1.0, v176
	v_add_f32_e32 v177, 1.0, v177
	v_add_f32_e32 v178, 1.0, v178
	v_add_f32_e32 v179, 1.0, v179
	v_rcp_f32_e32 v176, v176
	v_rcp_f32_e32 v177, v177
	v_rcp_f32_e32 v178, v178
	v_rcp_f32_e32 v179, v179
	v_mul_f32_e32 v176, 0xbf1b4598, v176
	v_mul_f32_e32 v177, 0xbf1b4598, v177
	v_mul_f32_e32 v178, 0xbf1b4598, v178
	v_mul_f32_e32 v179, 0xbf1b4598, v179
	global_store_dwordx4 v156, v[176:179], s[20:21]
	s_waitcnt vmcnt(22)
	v_mfma_f32_16x16x32_bf16 v[26:29], v[18:21], v[2:5], 0
	v_mfma_f32_16x16x32_bf16 v[26:29], v[22:25], v[6:9], v[26:29]
	v_mfma_f32_16x16x32_bf16 v[30:33], v[18:21], v[10:13], 0
	v_mfma_f32_16x16x32_bf16 v[30:33], v[22:25], v[14:17], v[30:33]
	s_add_u32 s20, s56, 0x1800400
	s_addc_u32 s21, s57, 0
	s_nop 7
	v_pk_add_f32 v[26:27], v[26:27], v[38:39]
	v_pk_add_f32 v[28:29], v[28:29], v[40:41]
	v_pk_add_f32 v[30:31], v[30:31], v[38:39]
	v_pk_add_f32 v[32:33], v[32:33], v[40:41]
	v_mul_f32_e32 v168, 0xbfb8aa3b, v26
	v_mul_f32_e32 v169, 0xbfb8aa3b, v27
	v_mul_f32_e32 v170, 0xbfb8aa3b, v28
	v_mul_f32_e32 v171, 0xbfb8aa3b, v29
	v_exp_f32_e32 v168, v168
	v_exp_f32_e32 v169, v169
	v_exp_f32_e32 v170, v170
	v_exp_f32_e32 v171, v171
	v_add_f32_e32 v168, 1.0, v168
	v_add_f32_e32 v169, 1.0, v169
	v_add_f32_e32 v170, 1.0, v170
	v_add_f32_e32 v171, 1.0, v171
	v_rcp_f32_e32 v168, v168
	v_rcp_f32_e32 v169, v169
	v_rcp_f32_e32 v170, v170
	v_rcp_f32_e32 v171, v171
	v_mul_f32_e32 v168, 0xbf1b4598, v168
	v_mul_f32_e32 v169, 0xbf1b4598, v169
	v_mul_f32_e32 v170, 0xbf1b4598, v170
	v_mul_f32_e32 v171, 0xbf1b4598, v171
	global_store_dwordx4 v155, v[168:171], s[20:21]
	v_mul_f32_e32 v176, 0xbfb8aa3b, v30
	v_mul_f32_e32 v177, 0xbfb8aa3b, v31
	v_mul_f32_e32 v178, 0xbfb8aa3b, v32
	v_mul_f32_e32 v179, 0xbfb8aa3b, v33
	v_exp_f32_e32 v176, v176
	v_exp_f32_e32 v177, v177
	v_exp_f32_e32 v178, v178
	v_exp_f32_e32 v179, v179
	v_add_f32_e32 v176, 1.0, v176
	v_add_f32_e32 v177, 1.0, v177
	v_add_f32_e32 v178, 1.0, v178
	v_add_f32_e32 v179, 1.0, v179
	v_rcp_f32_e32 v176, v176
	v_rcp_f32_e32 v177, v177
	v_rcp_f32_e32 v178, v178
	v_rcp_f32_e32 v179, v179
	v_mul_f32_e32 v176, 0xbf1b4598, v176
	v_mul_f32_e32 v177, 0xbf1b4598, v177
	v_mul_f32_e32 v178, 0xbf1b4598, v178
	v_mul_f32_e32 v179, 0xbf1b4598, v179
	global_store_dwordx4 v156, v[176:179], s[20:21]
	s_waitcnt vmcnt(19)
	v_mfma_f32_16x16x32_bf16 v[26:29], v[42:45], v[2:5], 0
	v_mfma_f32_16x16x32_bf16 v[26:29], v[46:49], v[6:9], v[26:29]
	v_mfma_f32_16x16x32_bf16 v[30:33], v[42:45], v[10:13], 0
	v_mfma_f32_16x16x32_bf16 v[30:33], v[46:49], v[14:17], v[30:33]
	s_add_u32 s20, s56, 0x1800440
	s_addc_u32 s21, s57, 0
	s_nop 7
	v_pk_add_f32 v[26:27], v[26:27], v[50:51]
	v_pk_add_f32 v[28:29], v[28:29], v[52:53]
	v_pk_add_f32 v[30:31], v[30:31], v[50:51]
	v_pk_add_f32 v[32:33], v[32:33], v[52:53]
	v_mul_f32_e32 v168, 0xbfb8aa3b, v26
	v_mul_f32_e32 v169, 0xbfb8aa3b, v27
	v_mul_f32_e32 v170, 0xbfb8aa3b, v28
	v_mul_f32_e32 v171, 0xbfb8aa3b, v29
	v_exp_f32_e32 v168, v168
	v_exp_f32_e32 v169, v169
	v_exp_f32_e32 v170, v170
	v_exp_f32_e32 v171, v171
	v_add_f32_e32 v168, 1.0, v168
	v_add_f32_e32 v169, 1.0, v169
	v_add_f32_e32 v170, 1.0, v170
	v_add_f32_e32 v171, 1.0, v171
	v_rcp_f32_e32 v168, v168
	v_rcp_f32_e32 v169, v169
	v_rcp_f32_e32 v170, v170
	v_rcp_f32_e32 v171, v171
	v_mul_f32_e32 v168, 0xbf1b4598, v168
	v_mul_f32_e32 v169, 0xbf1b4598, v169
	v_mul_f32_e32 v170, 0xbf1b4598, v170
	v_mul_f32_e32 v171, 0xbf1b4598, v171
	global_store_dwordx4 v155, v[168:171], s[20:21]
	v_mul_f32_e32 v176, 0xbfb8aa3b, v30
	v_mul_f32_e32 v177, 0xbfb8aa3b, v31
	v_mul_f32_e32 v178, 0xbfb8aa3b, v32
	v_mul_f32_e32 v179, 0xbfb8aa3b, v33
	v_exp_f32_e32 v176, v176
	v_exp_f32_e32 v177, v177
	v_exp_f32_e32 v178, v178
	v_exp_f32_e32 v179, v179
	v_add_f32_e32 v176, 1.0, v176
	v_add_f32_e32 v177, 1.0, v177
	v_add_f32_e32 v178, 1.0, v178
	v_add_f32_e32 v179, 1.0, v179
	v_rcp_f32_e32 v176, v176
	v_rcp_f32_e32 v177, v177
	v_rcp_f32_e32 v178, v178
	v_rcp_f32_e32 v179, v179
	v_mul_f32_e32 v176, 0xbf1b4598, v176
	v_mul_f32_e32 v177, 0xbf1b4598, v177
	v_mul_f32_e32 v178, 0xbf1b4598, v178
	v_mul_f32_e32 v179, 0xbf1b4598, v179
	global_store_dwordx4 v156, v[176:179], s[20:21]
	s_waitcnt vmcnt(16)
	v_mfma_f32_16x16x32_bf16 v[26:29], v[54:57], v[2:5], 0
	v_mfma_f32_16x16x32_bf16 v[26:29], v[58:61], v[6:9], v[26:29]
	v_mfma_f32_16x16x32_bf16 v[30:33], v[54:57], v[10:13], 0
	v_mfma_f32_16x16x32_bf16 v[30:33], v[58:61], v[14:17], v[30:33]
	s_add_u32 s20, s56, 0x1800480
	s_addc_u32 s21, s57, 0
	s_nop 7
	v_pk_add_f32 v[26:27], v[26:27], v[62:63]
	v_pk_add_f32 v[28:29], v[28:29], v[64:65]
	v_pk_add_f32 v[30:31], v[30:31], v[62:63]
	v_pk_add_f32 v[32:33], v[32:33], v[64:65]
	v_mul_f32_e32 v168, 0xbfb8aa3b, v26
	v_mul_f32_e32 v169, 0xbfb8aa3b, v27
	v_mul_f32_e32 v170, 0xbfb8aa3b, v28
	v_mul_f32_e32 v171, 0xbfb8aa3b, v29
	v_exp_f32_e32 v168, v168
	v_exp_f32_e32 v169, v169
	v_exp_f32_e32 v170, v170
	v_exp_f32_e32 v171, v171
	v_add_f32_e32 v168, 1.0, v168
	v_add_f32_e32 v169, 1.0, v169
	v_add_f32_e32 v170, 1.0, v170
	v_add_f32_e32 v171, 1.0, v171
	v_rcp_f32_e32 v168, v168
	v_rcp_f32_e32 v169, v169
	v_rcp_f32_e32 v170, v170
	v_rcp_f32_e32 v171, v171
	v_mul_f32_e32 v168, 0xbf1b4598, v168
	v_mul_f32_e32 v169, 0xbf1b4598, v169
	v_mul_f32_e32 v170, 0xbf1b4598, v170
	v_mul_f32_e32 v171, 0xbf1b4598, v171
	global_store_dwordx4 v155, v[168:171], s[20:21]
	v_mul_f32_e32 v176, 0xbfb8aa3b, v30
	v_mul_f32_e32 v177, 0xbfb8aa3b, v31
	v_mul_f32_e32 v178, 0xbfb8aa3b, v32
	v_mul_f32_e32 v179, 0xbfb8aa3b, v33
	v_exp_f32_e32 v176, v176
	v_exp_f32_e32 v177, v177
	v_exp_f32_e32 v178, v178
	v_exp_f32_e32 v179, v179
	v_add_f32_e32 v176, 1.0, v176
	v_add_f32_e32 v177, 1.0, v177
	v_add_f32_e32 v178, 1.0, v178
	v_add_f32_e32 v179, 1.0, v179
	v_rcp_f32_e32 v176, v176
	v_rcp_f32_e32 v177, v177
	v_rcp_f32_e32 v178, v178
	v_rcp_f32_e32 v179, v179
	v_mul_f32_e32 v176, 0xbf1b4598, v176
	v_mul_f32_e32 v177, 0xbf1b4598, v177
	v_mul_f32_e32 v178, 0xbf1b4598, v178
	v_mul_f32_e32 v179, 0xbf1b4598, v179
	global_store_dwordx4 v156, v[176:179], s[20:21]
	s_waitcnt vmcnt(13)
	v_mfma_f32_16x16x32_bf16 v[26:29], v[66:69], v[2:5], 0
	v_mfma_f32_16x16x32_bf16 v[26:29], v[70:73], v[6:9], v[26:29]
	v_mfma_f32_16x16x32_bf16 v[30:33], v[66:69], v[10:13], 0
	v_mfma_f32_16x16x32_bf16 v[30:33], v[70:73], v[14:17], v[30:33]
	s_add_u32 s20, s56, 0x18004c0
	s_addc_u32 s21, s57, 0
	s_nop 7
	v_pk_add_f32 v[26:27], v[26:27], v[74:75]
	v_pk_add_f32 v[28:29], v[28:29], v[76:77]
	v_pk_add_f32 v[30:31], v[30:31], v[74:75]
	v_pk_add_f32 v[32:33], v[32:33], v[76:77]
	v_mul_f32_e32 v168, 0xbfb8aa3b, v26
	v_mul_f32_e32 v169, 0xbfb8aa3b, v27
	v_mul_f32_e32 v170, 0xbfb8aa3b, v28
	v_mul_f32_e32 v171, 0xbfb8aa3b, v29
	v_exp_f32_e32 v168, v168
	v_exp_f32_e32 v169, v169
	v_exp_f32_e32 v170, v170
	v_exp_f32_e32 v171, v171
	v_add_f32_e32 v168, 1.0, v168
	v_add_f32_e32 v169, 1.0, v169
	v_add_f32_e32 v170, 1.0, v170
	v_add_f32_e32 v171, 1.0, v171
	v_rcp_f32_e32 v168, v168
	v_rcp_f32_e32 v169, v169
	v_rcp_f32_e32 v170, v170
	v_rcp_f32_e32 v171, v171
	v_mul_f32_e32 v168, 0xbf1b4598, v168
	v_mul_f32_e32 v169, 0xbf1b4598, v169
	v_mul_f32_e32 v170, 0xbf1b4598, v170
	v_mul_f32_e32 v171, 0xbf1b4598, v171
	global_store_dwordx4 v155, v[168:171], s[20:21]
	v_mul_f32_e32 v176, 0xbfb8aa3b, v30
	v_mul_f32_e32 v177, 0xbfb8aa3b, v31
	v_mul_f32_e32 v178, 0xbfb8aa3b, v32
	v_mul_f32_e32 v179, 0xbfb8aa3b, v33
	v_exp_f32_e32 v176, v176
	v_exp_f32_e32 v177, v177
	v_exp_f32_e32 v178, v178
	v_exp_f32_e32 v179, v179
	v_add_f32_e32 v176, 1.0, v176
	v_add_f32_e32 v177, 1.0, v177
	v_add_f32_e32 v178, 1.0, v178
	v_add_f32_e32 v179, 1.0, v179
	v_rcp_f32_e32 v176, v176
	v_rcp_f32_e32 v177, v177
	v_rcp_f32_e32 v178, v178
	v_rcp_f32_e32 v179, v179
	v_mul_f32_e32 v176, 0xbf1b4598, v176
	v_mul_f32_e32 v177, 0xbf1b4598, v177
	v_mul_f32_e32 v178, 0xbf1b4598, v178
	v_mul_f32_e32 v179, 0xbf1b4598, v179
	global_store_dwordx4 v156, v[176:179], s[20:21]
	s_waitcnt vmcnt(10)
	v_mfma_f32_16x16x32_bf16 v[26:29], v[78:81], v[2:5], 0
	v_mfma_f32_16x16x32_bf16 v[26:29], v[82:85], v[6:9], v[26:29]
	v_mfma_f32_16x16x32_bf16 v[30:33], v[78:81], v[10:13], 0
	v_mfma_f32_16x16x32_bf16 v[30:33], v[82:85], v[14:17], v[30:33]
	s_add_u32 s20, s56, 0x1800500
	s_addc_u32 s21, s57, 0
	s_nop 7
	v_pk_add_f32 v[26:27], v[26:27], v[86:87]
	v_pk_add_f32 v[28:29], v[28:29], v[88:89]
	v_pk_add_f32 v[30:31], v[30:31], v[86:87]
	v_pk_add_f32 v[32:33], v[32:33], v[88:89]
	v_mul_f32_e32 v168, 0xbfb8aa3b, v26
	v_mul_f32_e32 v169, 0xbfb8aa3b, v27
	v_mul_f32_e32 v170, 0xbfb8aa3b, v28
	v_mul_f32_e32 v171, 0xbfb8aa3b, v29
	v_exp_f32_e32 v168, v168
	v_exp_f32_e32 v169, v169
	v_exp_f32_e32 v170, v170
	v_exp_f32_e32 v171, v171
	v_add_f32_e32 v168, 1.0, v168
	v_add_f32_e32 v169, 1.0, v169
	v_add_f32_e32 v170, 1.0, v170
	v_add_f32_e32 v171, 1.0, v171
	v_rcp_f32_e32 v168, v168
	v_rcp_f32_e32 v169, v169
	v_rcp_f32_e32 v170, v170
	v_rcp_f32_e32 v171, v171
	v_mul_f32_e32 v168, 0xbf1b4598, v168
	v_mul_f32_e32 v169, 0xbf1b4598, v169
	v_mul_f32_e32 v170, 0xbf1b4598, v170
	v_mul_f32_e32 v171, 0xbf1b4598, v171
	global_store_dwordx4 v155, v[168:171], s[20:21]
	v_mul_f32_e32 v176, 0xbfb8aa3b, v30
	v_mul_f32_e32 v177, 0xbfb8aa3b, v31
	v_mul_f32_e32 v178, 0xbfb8aa3b, v32
	v_mul_f32_e32 v179, 0xbfb8aa3b, v33
	v_exp_f32_e32 v176, v176
	v_exp_f32_e32 v177, v177
	v_exp_f32_e32 v178, v178
	v_exp_f32_e32 v179, v179
	v_add_f32_e32 v176, 1.0, v176
	v_add_f32_e32 v177, 1.0, v177
	v_add_f32_e32 v178, 1.0, v178
	v_add_f32_e32 v179, 1.0, v179
	v_rcp_f32_e32 v176, v176
	v_rcp_f32_e32 v177, v177
	v_rcp_f32_e32 v178, v178
	v_rcp_f32_e32 v179, v179
	v_mul_f32_e32 v176, 0xbf1b4598, v176
	v_mul_f32_e32 v177, 0xbf1b4598, v177
	v_mul_f32_e32 v178, 0xbf1b4598, v178
	v_mul_f32_e32 v179, 0xbf1b4598, v179
	global_store_dwordx4 v156, v[176:179], s[20:21]
	s_branch .LBB0_402
.Lb3w_3:
	ds_read_b128 v[2:5], v0 offset:0
	ds_read_b128 v[6:9], v0 offset:64
	ds_read_b128 v[10:13], v0 offset:8448
	ds_read_b128 v[14:17], v0 offset:8512
	ds_read_b128 v[18:21], v0 offset:128
	ds_read_b128 v[22:25], v0 offset:192
	ds_read_b128 v[38:41], v0 offset:8576
	ds_read_b128 v[42:45], v0 offset:8640
	s_add_u32 s16, s0, 0x2d000
	s_addc_u32 s17, s1, 0
	global_load_dwordx4 v[46:49], v153, s[16:17] offset:0
	global_load_dwordx4 v[50:53], v153, s[16:17] offset:64
	s_add_u32 s18, s68, 0xb40
	s_addc_u32 s19, s69, 0
	global_load_dwordx4 v[54:57], v159, s[18:19]
	s_add_u32 s16, s0, 0x2e000
	s_addc_u32 s17, s1, 0
	global_load_dwordx4 v[58:61], v153, s[16:17] offset:0
	global_load_dwordx4 v[62:65], v153, s[16:17] offset:64
	s_add_u32 s18, s68, 0xb80
	s_addc_u32 s19, s69, 0
	global_load_dwordx4 v[66:69], v159, s[18:19]
	s_add_u32 s16, s0, 0x2f000
	s_addc_u32 s17, s1, 0
	global_load_dwordx4 v[70:73], v153, s[16:17] offset:0
	global_load_dwordx4 v[74:77], v153, s[16:17] offset:64
	s_add_u32 s18, s68, 0xbc0
	s_addc_u32 s19, s69, 0
	global_load_dwordx4 v[78:81], v159, s[18:19]
	s_add_u32 s16, s0, 0x30000
	s_addc_u32 s17, s1, 0
	global_load_dwordx4 v[82:85], v153, s[16:17] offset:0
	global_load_dwordx4 v[86:89], v153, s[16:17] offset:64
	s_add_u32 s18, s70, 0x0
	s_addc_u32 s19, s71, 0
	global_load_dwordx4 v[90:93], v159, s[18:19]
	s_add_u32 s16, s0, 0x31000
	s_addc_u32 s17, s1, 0
	global_load_dwordx4 v[94:97], v153, s[16:17] offset:0
	global_load_dwordx4 v[160:163], v153, s[16:17] offset:64
	s_add_u32 s18, s70, 0x40
	s_addc_u32 s19, s71, 0
	global_load_dwordx4 v[164:167], v159, s[18:19]
	s_waitcnt vmcnt(12) lgkmcnt(0)
	v_mfma_f32_16x16x32_bf16 v[26:29], v[46:49], v[2:5], 0
	v_mfma_f32_16x16x32_bf16 v[26:29], v[50:53], v[6:9], v[26:29]
	v_mfma_f32_16x16x32_bf16 v[30:33], v[46:49], v[10:13], 0
	v_mfma_f32_16x16x32_bf16 v[30:33], v[50:53], v[14:17], v[30:33]
	s_add_u32 s20, s56, 0x1800540
	s_addc_u32 s21, s57, 0
	s_nop 7
	v_pk_add_f32 v[26:27], v[26:27], v[54:55]
	v_pk_add_f32 v[28:29], v[28:29], v[56:57]
	v_pk_add_f32 v[30:31], v[30:31], v[54:55]
	v_pk_add_f32 v[32:33], v[32:33], v[56:57]
	s_add_u32 s16, s0, 0x32000
	s_addc_u32 s17, s1, 0
	global_load_dwordx4 v[46:49], v153, s[16:17] offset:0
	global_load_dwordx4 v[50:53], v153, s[16:17] offset:64
	s_add_u32 s18, s70, 0x80
	s_addc_u32 s19, s71, 0
	global_load_dwordx4 v[54:57], v159, s[18:19]
	v_mul_f32_e32 v168, 0xbfb8aa3b, v26
	v_mul_f32_e32 v169, 0xbfb8aa3b, v27
	v_mul_f32_e32 v170, 0xbfb8aa3b, v28
	v_mul_f32_e32 v171, 0xbfb8aa3b, v29
	v_exp_f32_e32 v168, v168
	v_exp_f32_e32 v169, v169
	v_exp_f32_e32 v170, v170
	v_exp_f32_e32 v171, v171
	v_add_f32_e32 v168, 1.0, v168
	v_add_f32_e32 v169, 1.0, v169
	v_add_f32_e32 v170, 1.0, v170
	v_add_f32_e32 v171, 1.0, v171
	v_rcp_f32_e32 v168, v168
	v_rcp_f32_e32 v169, v169
	v_rcp_f32_e32 v170, v170
	v_rcp_f32_e32 v171, v171
	v_mul_f32_e32 v168, 0xbf1b4598, v168
	v_mul_f32_e32 v169, 0xbf1b4598, v169
	v_mul_f32_e32 v170, 0xbf1b4598, v170
	v_mul_f32_e32 v171, 0xbf1b4598, v171
	global_store_dwordx4 v155, v[168:171], s[20:21]
	v_mul_f32_e32 v176, 0xbfb8aa3b, v30
	v_mul_f32_e32 v177, 0xbfb8aa3b, v31
	v_mul_f32_e32 v178, 0xbfb8aa3b, v32
	v_mul_f32_e32 v179, 0xbfb8aa3b, v33
	v_exp_f32_e32 v176, v176
	v_exp_f32_e32 v177, v177
	v_exp_f32_e32 v178, v178
	v_exp_f32_e32 v179, v179
	v_add_f32_e32 v176, 1.0, v176
	v_add_f32_e32 v177, 1.0, v177
	v_add_f32_e32 v178, 1.0, v178
	v_add_f32_e32 v179, 1.0, v179
	v_rcp_f32_e32 v176, v176
	v_rcp_f32_e32 v177, v177
	v_rcp_f32_e32 v178, v178
	v_rcp_f32_e32 v179, v179
	v_mul_f32_e32 v176, 0xbf1b4598, v176
	v_mul_f32_e32 v177, 0xbf1b4598, v177
	v_mul_f32_e32 v178, 0xbf1b4598, v178
	v_mul_f32_e32 v179, 0xbf1b4598, v179
	global_store_dwordx4 v156, v[176:179], s[20:21]
	s_waitcnt vmcnt(14)
	v_mfma_f32_16x16x32_bf16 v[26:29], v[58:61], v[2:5], 0
	v_mfma_f32_16x16x32_bf16 v[26:29], v[62:65], v[6:9], v[26:29]
	v_mfma_f32_16x16x32_bf16 v[30:33], v[58:61], v[10:13], 0
	v_mfma_f32_16x16x32_bf16 v[30:33], v[62:65], v[14:17], v[30:33]
	s_add_u32 s20, s56, 0x1800580
	s_addc_u32 s21, s57, 0
	s_nop 7
	v_pk_add_f32 v[26:27], v[26:27], v[66:67]
	v_pk_add_f32 v[28:29], v[28:29], v[68:69]
	v_pk_add_f32 v[30:31], v[30:31], v[66:67]
	v_pk_add_f32 v[32:33], v[32:33], v[68:69]
	s_add_u32 s16, s0, 0x33000
	s_addc_u32 s17, s1, 0
	global_load_dwordx4 v[58:61], v153, s[16:17] offset:0
	global_load_dwordx4 v[62:65], v153, s[16:17] offset:64
	s_add_u32 s18, s70, 0xc0
	s_addc_u32 s19, s71, 0
	global_load_dwordx4 v[66:69], v159, s[18:19]
	v_mul_f32_e32 v168, 0xbfb8aa3b, v26
	v_mul_f32_e32 v169, 0xbfb8aa3b, v27
	v_mul_f32_e32 v170, 0xbfb8aa3b, v28
	v_mul_f32_e32 v171, 0xbfb8aa3b, v29
	v_exp_f32_e32 v168, v168
	v_exp_f32_e32 v169, v169
	v_exp_f32_e32 v170, v170
	v_exp_f32_e32 v171, v171
	v_add_f32_e32 v168, 1.0, v168
	v_add_f32_e32 v169, 1.0, v169
	v_add_f32_e32 v170, 1.0, v170
	v_add_f32_e32 v171, 1.0, v171
	v_rcp_f32_e32 v168, v168
	v_rcp_f32_e32 v169, v169
	v_rcp_f32_e32 v170, v170
	v_rcp_f32_e32 v171, v171
	v_mul_f32_e32 v168, 0xbf1b4598, v168
	v_mul_f32_e32 v169, 0xbf1b4598, v169
	v_mul_f32_e32 v170, 0xbf1b4598, v170
	v_mul_f32_e32 v171, 0xbf1b4598, v171
	global_store_dwordx4 v155, v[168:171], s[20:21]
	v_mul_f32_e32 v176, 0xbfb8aa3b, v30
	v_mul_f32_e32 v177, 0xbfb8aa3b, v31
	v_mul_f32_e32 v178, 0xbfb8aa3b, v32
	v_mul_f32_e32 v179, 0xbfb8aa3b, v33
	v_exp_f32_e32 v176, v176
	v_exp_f32_e32 v177, v177
	v_exp_f32_e32 v178, v178
	v_exp_f32_e32 v179, v179
	v_add_f32_e32 v176, 1.0, v176
	v_add_f32_e32 v177, 1.0, v177
	v_add_f32_e32 v178, 1.0, v178
	v_add_f32_e32 v179, 1.0, v179
	v_rcp_f32_e32 v176, v176
	v_rcp_f32_e32 v177, v177
	v_rcp_f32_e32 v178, v178
	v_rcp_f32_e32 v179, v179
	v_mul_f32_e32 v176, 0xbf1b4598, v176
	v_mul_f32_e32 v177, 0xbf1b4598, v177
	v_mul_f32_e32 v178, 0xbf1b4598, v178
	v_mul_f32_e32 v179, 0xbf1b4598, v179
	global_store_dwordx4 v156, v[176:179], s[20:21]
	s_waitcnt vmcnt(16)
	v_mfma_f32_16x16x32_bf16 v[26:29], v[70:73], v[2:5], 0
	v_mfma_f32_16x16x32_bf16 v[26:29], v[74:77], v[6:9], v[26:29]
	v_mfma_f32_16x16x32_bf16 v[30:33], v[70:73], v[10:13], 0
	v_mfma_f32_16x16x32_bf16 v[30:33], v[74:77], v[14:17], v[30:33]
	s_add_u32 s20, s56, 0x18005c0
	s_addc_u32 s21, s57, 0
	s_nop 7
	v_pk_add_f32 v[26:27], v[26:27], v[78:79]
	v_pk_add_f32 v[28:29], v[28:29], v[80:81]
	v_pk_add_f32 v[30:31], v[30:31], v[78:79]
	v_pk_add_f32 v[32:33], v[32:33], v[80:81]
	s_add_u32 s16, s0, 0x34000
	s_addc_u32 s17, s1, 0
	global_load_dwordx4 v[70:73], v153, s[16:17] offset:0
	global_load_dwordx4 v[74:77], v153, s[16:17] offset:64
	s_add_u32 s18, s70, 0x100
	s_addc_u32 s19, s71, 0
	global_load_dwordx4 v[78:81], v159, s[18:19]
	v_mul_f32_e32 v168, 0xbfb8aa3b, v26
	v_mul_f32_e32 v169, 0xbfb8aa3b, v27
	v_mul_f32_e32 v170, 0xbfb8aa3b, v28
	v_mul_f32_e32 v171, 0xbfb8aa3b, v29
	v_exp_f32_e32 v168, v168
	v_exp_f32_e32 v169, v169
	v_exp_f32_e32 v170, v170
	v_exp_f32_e32 v171, v171
	v_add_f32_e32 v168, 1.0, v168
	v_add_f32_e32 v169, 1.0, v169
	v_add_f32_e32 v170, 1.0, v170
	v_add_f32_e32 v171, 1.0, v171
	v_rcp_f32_e32 v168, v168
	v_rcp_f32_e32 v169, v169
	v_rcp_f32_e32 v170, v170
	v_rcp_f32_e32 v171, v171
	v_mul_f32_e32 v168, 0xbf1b4598, v168
	v_mul_f32_e32 v169, 0xbf1b4598, v169
	v_mul_f32_e32 v170, 0xbf1b4598, v170
	v_mul_f32_e32 v171, 0xbf1b4598, v171
	global_store_dwordx4 v155, v[168:171], s[20:21]
	v_mul_f32_e32 v176, 0xbfb8aa3b, v30
	v_mul_f32_e32 v177, 0xbfb8aa3b, v31
	v_mul_f32_e32 v178, 0xbfb8aa3b, v32
	v_mul_f32_e32 v179, 0xbfb8aa3b, v33
	v_exp_f32_e32 v176, v176
	v_exp_f32_e32 v177, v177
	v_exp_f32_e32 v178, v178
	v_exp_f32_e32 v179, v179
	v_add_f32_e32 v176, 1.0, v176
	v_add_f32_e32 v177, 1.0, v177
	v_add_f32_e32 v178, 1.0, v178
	v_add_f32_e32 v179, 1.0, v179
	v_rcp_f32_e32 v176, v176
	v_rcp_f32_e32 v177, v177
	v_rcp_f32_e32 v178, v178
	v_rcp_f32_e32 v179, v179
	v_mul_f32_e32 v176, 0xbf1b4598, v176
	v_mul_f32_e32 v177, 0xbf1b4598, v177
	v_mul_f32_e32 v178, 0xbf1b4598, v178
	v_mul_f32_e32 v179, 0xbf1b4598, v179
	global_store_dwordx4 v156, v[176:179], s[20:21]
	s_waitcnt vmcnt(18)
	v_mfma_f32_16x16x32_bf16 v[26:29], v[82:85], v[18:21], 0
	v_mfma_f32_16x16x32_bf16 v[26:29], v[86:89], v[22:25], v[26:29]
	v_mfma_f32_16x16x32_bf16 v[30:33], v[82:85], v[38:41], 0
	v_mfma_f32_16x16x32_bf16 v[30:33], v[86:89], v[42:45], v[30:33]
	v_add_u32_e32 v108, 0x0, v154
	s_nop 7
	v_pk_add_f32 v[26:27], v[26:27], v[90:91]
	v_pk_add_f32 v[28:29], v[28:29], v[92:93]
	v_pk_add_f32 v[30:31], v[30:31], v[90:91]
	v_pk_add_f32 v[32:33], v[32:33], v[92:93]
	s_add_u32 s16, s0, 0x35000
	s_addc_u32 s17, s1, 0
	global_load_dwordx4 v[82:85], v153, s[16:17] offset:0
	global_load_dwordx4 v[86:89], v153, s[16:17] offset:64
	s_add_u32 s18, s70, 0x140
	s_addc_u32 s19, s71, 0
	global_load_dwordx4 v[90:93], v159, s[18:19]
	v_mul_f32_e32 v168, 0xbfb8aa3b, v26
	v_mul_f32_e32 v169, 0xbfb8aa3b, v27
	v_mul_f32_e32 v170, 0xbfb8aa3b, v28
	v_mul_f32_e32 v171, 0xbfb8aa3b, v29
	v_exp_f32_e32 v168, v168
	v_exp_f32_e32 v169, v169
	v_exp_f32_e32 v170, v170
	v_exp_f32_e32 v171, v171
	v_add_f32_e32 v168, 1.0, v168
	v_add_f32_e32 v169, 1.0, v169
	v_add_f32_e32 v170, 1.0, v170
	v_add_f32_e32 v171, 1.0, v171
	v_rcp_f32_e32 v168, v168
	v_rcp_f32_e32 v169, v169
	v_rcp_f32_e32 v170, v170
	v_rcp_f32_e32 v171, v171
	s_nop 0
	v_cvt_pk_bf16_f32 v168, v168, v169
	v_cvt_pk_bf16_f32 v169, v170, v171
	ds_write_b64 v108, v[168:169] offset:0
	v_mul_f32_e32 v176, 0xbfb8aa3b, v30
	v_mul_f32_e32 v177, 0xbfb8aa3b, v31
	v_mul_f32_e32 v178, 0xbfb8aa3b, v32
	v_mul_f32_e32 v179, 0xbfb8aa3b, v33
	v_exp_f32_e32 v176, v176
	v_exp_f32_e32 v177, v177
	v_exp_f32_e32 v178, v178
	v_exp_f32_e32 v179, v179
	v_add_f32_e32 v176, 1.0, v176
	v_add_f32_e32 v177, 1.0, v177
	v_add_f32_e32 v178, 1.0, v178
	v_add_f32_e32 v179, 1.0, v179
	v_rcp_f32_e32 v176, v176
	v_rcp_f32_e32 v177, v177
	v_rcp_f32_e32 v178, v178
	v_rcp_f32_e32 v179, v179
	s_nop 0
	v_cvt_pk_bf16_f32 v176, v176, v177
	v_cvt_pk_bf16_f32 v177, v178, v179
	ds_write_b64 v108, v[176:177] offset:12288
	s_waitcnt vmcnt(18)
	v_mfma_f32_16x16x32_bf16 v[26:29], v[94:97], v[18:21], 0
	v_mfma_f32_16x16x32_bf16 v[26:29], v[160:163], v[22:25], v[26:29]
	v_mfma_f32_16x16x32_bf16 v[30:33], v[94:97], v[38:41], 0
	v_mfma_f32_16x16x32_bf16 v[30:33], v[160:163], v[42:45], v[30:33]
	v_add_u32_e32 v108, 0x20, v154
	s_nop 7
	v_pk_add_f32 v[26:27], v[26:27], v[164:165]
	v_pk_add_f32 v[28:29], v[28:29], v[166:167]
	v_pk_add_f32 v[30:31], v[30:31], v[164:165]
	v_pk_add_f32 v[32:33], v[32:33], v[166:167]
	s_add_u32 s16, s0, 0x36000
	s_addc_u32 s17, s1, 0
	global_load_dwordx4 v[94:97], v153, s[16:17] offset:0
	global_load_dwordx4 v[160:163], v153, s[16:17] offset:64
	s_add_u32 s18, s70, 0x180
	s_addc_u32 s19, s71, 0
	global_load_dwordx4 v[164:167], v159, s[18:19]
	v_mul_f32_e32 v168, 0xbfb8aa3b, v26
	v_mul_f32_e32 v169, 0xbfb8aa3b, v27
	v_mul_f32_e32 v170, 0xbfb8aa3b, v28
	v_mul_f32_e32 v171, 0xbfb8aa3b, v29
	v_exp_f32_e32 v168, v168
	v_exp_f32_e32 v169, v169
	v_exp_f32_e32 v170, v170
	v_exp_f32_e32 v171, v171
	v_add_f32_e32 v168, 1.0, v168
	v_add_f32_e32 v169, 1.0, v169
	v_add_f32_e32 v170, 1.0, v170
	v_add_f32_e32 v171, 1.0, v171
	v_rcp_f32_e32 v168, v168
	v_rcp_f32_e32 v169, v169
	v_rcp_f32_e32 v170, v170
	v_rcp_f32_e32 v171, v171
	s_nop 0
	v_cvt_pk_bf16_f32 v168, v168, v169
	v_cvt_pk_bf16_f32 v169, v170, v171
	ds_write_b64 v108, v[168:169] offset:0
	v_mul_f32_e32 v176, 0xbfb8aa3b, v30
	v_mul_f32_e32 v177, 0xbfb8aa3b, v31
	v_mul_f32_e32 v178, 0xbfb8aa3b, v32
	v_mul_f32_e32 v179, 0xbfb8aa3b, v33
	v_exp_f32_e32 v176, v176
	v_exp_f32_e32 v177, v177
	v_exp_f32_e32 v178, v178
	v_exp_f32_e32 v179, v179
	v_add_f32_e32 v176, 1.0, v176
	v_add_f32_e32 v177, 1.0, v177
	v_add_f32_e32 v178, 1.0, v178
	v_add_f32_e32 v179, 1.0, v179
	v_rcp_f32_e32 v176, v176
	v_rcp_f32_e32 v177, v177
	v_rcp_f32_e32 v178, v178
	v_rcp_f32_e32 v179, v179
	s_nop 0
	v_cvt_pk_bf16_f32 v176, v176, v177
	v_cvt_pk_bf16_f32 v177, v178, v179
	ds_write_b64 v108, v[176:177] offset:12288
	s_waitcnt vmcnt(18)
	v_mfma_f32_16x16x32_bf16 v[26:29], v[46:49], v[18:21], 0
	v_mfma_f32_16x16x32_bf16 v[26:29], v[50:53], v[22:25], v[26:29]
	v_mfma_f32_16x16x32_bf16 v[30:33], v[46:49], v[38:41], 0
	v_mfma_f32_16x16x32_bf16 v[30:33], v[50:53], v[42:45], v[30:33]
	v_add_u32_e32 v108, 0x40, v154
	s_nop 7
	v_pk_add_f32 v[26:27], v[26:27], v[54:55]
	v_pk_add_f32 v[28:29], v[28:29], v[56:57]
	v_pk_add_f32 v[30:31], v[30:31], v[54:55]
	v_pk_add_f32 v[32:33], v[32:33], v[56:57]
	s_add_u32 s16, s0, 0x37000
	s_addc_u32 s17, s1, 0
	global_load_dwordx4 v[46:49], v153, s[16:17] offset:0
	global_load_dwordx4 v[50:53], v153, s[16:17] offset:64
	s_add_u32 s18, s70, 0x1c0
	s_addc_u32 s19, s71, 0
	global_load_dwordx4 v[54:57], v159, s[18:19]
	v_mul_f32_e32 v168, 0xbfb8aa3b, v26
	v_mul_f32_e32 v169, 0xbfb8aa3b, v27
	v_mul_f32_e32 v170, 0xbfb8aa3b, v28
	v_mul_f32_e32 v171, 0xbfb8aa3b, v29
	v_exp_f32_e32 v168, v168
	v_exp_f32_e32 v169, v169
	v_exp_f32_e32 v170, v170
	v_exp_f32_e32 v171, v171
	v_add_f32_e32 v168, 1.0, v168
	v_add_f32_e32 v169, 1.0, v169
	v_add_f32_e32 v170, 1.0, v170
	v_add_f32_e32 v171, 1.0, v171
	v_rcp_f32_e32 v168, v168
	v_rcp_f32_e32 v169, v169
	v_rcp_f32_e32 v170, v170
	v_rcp_f32_e32 v171, v171
	s_nop 0
	v_cvt_pk_bf16_f32 v168, v168, v169
	v_cvt_pk_bf16_f32 v169, v170, v171
	ds_write_b64 v108, v[168:169] offset:0
	v_mul_f32_e32 v176, 0xbfb8aa3b, v30
	v_mul_f32_e32 v177, 0xbfb8aa3b, v31
	v_mul_f32_e32 v178, 0xbfb8aa3b, v32
	v_mul_f32_e32 v179, 0xbfb8aa3b, v33
	v_exp_f32_e32 v176, v176
	v_exp_f32_e32 v177, v177
	v_exp_f32_e32 v178, v178
	v_exp_f32_e32 v179, v179
	v_add_f32_e32 v176, 1.0, v176
	v_add_f32_e32 v177, 1.0, v177
	v_add_f32_e32 v178, 1.0, v178
	v_add_f32_e32 v179, 1.0, v179
	v_rcp_f32_e32 v176, v176
	v_rcp_f32_e32 v177, v177
	v_rcp_f32_e32 v178, v178
	v_rcp_f32_e32 v179, v179
	s_nop 0
	v_cvt_pk_bf16_f32 v176, v176, v177
	v_cvt_pk_bf16_f32 v177, v178, v179
	ds_write_b64 v108, v[176:177] offset:12288
	s_waitcnt vmcnt(16)
	v_mfma_f32_16x16x32_bf16 v[26:29], v[58:61], v[18:21], 0
	v_mfma_f32_16x16x32_bf16 v[26:29], v[62:65], v[22:25], v[26:29]
	v_mfma_f32_16x16x32_bf16 v[30:33], v[58:61], v[38:41], 0
	v_mfma_f32_16x16x32_bf16 v[30:33], v[62:65], v[42:45], v[30:33]
	v_add_u32_e32 v108, 0x60, v154
	s_nop 7
	v_pk_add_f32 v[26:27], v[26:27], v[66:67]
	v_pk_add_f32 v[28:29], v[28:29], v[68:69]
	v_pk_add_f32 v[30:31], v[30:31], v[66:67]
	v_pk_add_f32 v[32:33], v[32:33], v[68:69]
	s_add_u32 s16, s0, 0x38000
	s_addc_u32 s17, s1, 0
	global_load_dwordx4 v[58:61], v153, s[16:17] offset:0
	global_load_dwordx4 v[62:65], v153, s[16:17] offset:64
	s_add_u32 s18, s70, 0x200
	s_addc_u32 s19, s71, 0
	global_load_dwordx4 v[66:69], v159, s[18:19]
	v_mul_f32_e32 v168, 0xbfb8aa3b, v26
	v_mul_f32_e32 v169, 0xbfb8aa3b, v27
	v_mul_f32_e32 v170, 0xbfb8aa3b, v28
	v_mul_f32_e32 v171, 0xbfb8aa3b, v29
	v_exp_f32_e32 v168, v168
	v_exp_f32_e32 v169, v169
	v_exp_f32_e32 v170, v170
	v_exp_f32_e32 v171, v171
	v_add_f32_e32 v168, 1.0, v168
	v_add_f32_e32 v169, 1.0, v169
	v_add_f32_e32 v170, 1.0, v170
	v_add_f32_e32 v171, 1.0, v171
	v_rcp_f32_e32 v168, v168
	v_rcp_f32_e32 v169, v169
	v_rcp_f32_e32 v170, v170
	v_rcp_f32_e32 v171, v171
	s_nop 0
	v_cvt_pk_bf16_f32 v168, v168, v169
	v_cvt_pk_bf16_f32 v169, v170, v171
	ds_write_b64 v108, v[168:169] offset:0
	v_mul_f32_e32 v176, 0xbfb8aa3b, v30
	v_mul_f32_e32 v177, 0xbfb8aa3b, v31
	v_mul_f32_e32 v178, 0xbfb8aa3b, v32
	v_mul_f32_e32 v179, 0xbfb8aa3b, v33
	v_exp_f32_e32 v176, v176
	v_exp_f32_e32 v177, v177
	v_exp_f32_e32 v178, v178
	v_exp_f32_e32 v179, v179
	v_add_f32_e32 v176, 1.0, v176
	v_add_f32_e32 v177, 1.0, v177
	v_add_f32_e32 v178, 1.0, v178
	v_add_f32_e32 v179, 1.0, v179
	v_rcp_f32_e32 v176, v176
	v_rcp_f32_e32 v177, v177
	v_rcp_f32_e32 v178, v178
	v_rcp_f32_e32 v179, v179
	s_nop 0
	v_cvt_pk_bf16_f32 v176, v176, v177
	v_cvt_pk_bf16_f32 v177, v178, v179
	ds_write_b64 v108, v[176:177] offset:12288
	s_waitcnt vmcnt(14)
	v_mfma_f32_16x16x32_bf16 v[26:29], v[70:73], v[18:21], 0
	v_mfma_f32_16x16x32_bf16 v[26:29], v[74:77], v[22:25], v[26:29]
	v_mfma_f32_16x16x32_bf16 v[30:33], v[70:73], v[38:41], 0
	v_mfma_f32_16x16x32_bf16 v[30:33], v[74:77], v[42:45], v[30:33]
	v_add_u32_e32 v108, 0x80, v154
	s_nop 7
	v_pk_add_f32 v[26:27], v[26:27], v[78:79]
	v_pk_add_f32 v[28:29], v[28:29], v[80:81]
	v_pk_add_f32 v[30:31], v[30:31], v[78:79]
	v_pk_add_f32 v[32:33], v[32:33], v[80:81]
	s_add_u32 s16, s0, 0x39000
	s_addc_u32 s17, s1, 0
	global_load_dwordx4 v[70:73], v153, s[16:17] offset:0
	global_load_dwordx4 v[74:77], v153, s[16:17] offset:64
	s_add_u32 s18, s70, 0x240
	s_addc_u32 s19, s71, 0
	global_load_dwordx4 v[78:81], v159, s[18:19]
	v_mul_f32_e32 v168, 0xbfb8aa3b, v26
	v_mul_f32_e32 v169, 0xbfb8aa3b, v27
	v_mul_f32_e32 v170, 0xbfb8aa3b, v28
	v_mul_f32_e32 v171, 0xbfb8aa3b, v29
	v_exp_f32_e32 v168, v168
	v_exp_f32_e32 v169, v169
	v_exp_f32_e32 v170, v170
	v_exp_f32_e32 v171, v171
	v_add_f32_e32 v168, 1.0, v168
	v_add_f32_e32 v169, 1.0, v169
	v_add_f32_e32 v170, 1.0, v170
	v_add_f32_e32 v171, 1.0, v171
	v_rcp_f32_e32 v168, v168
	v_rcp_f32_e32 v169, v169
	v_rcp_f32_e32 v170, v170
	v_rcp_f32_e32 v171, v171
	s_nop 0
	v_cvt_pk_bf16_f32 v168, v168, v169
	v_cvt_pk_bf16_f32 v169, v170, v171
	ds_write_b64 v108, v[168:169] offset:0
	v_mul_f32_e32 v176, 0xbfb8aa3b, v30
	v_mul_f32_e32 v177, 0xbfb8aa3b, v31
	v_mul_f32_e32 v178, 0xbfb8aa3b, v32
	v_mul_f32_e32 v179, 0xbfb8aa3b, v33
	v_exp_f32_e32 v176, v176
	v_exp_f32_e32 v177, v177
	v_exp_f32_e32 v178, v178
	v_exp_f32_e32 v179, v179
	v_add_f32_e32 v176, 1.0, v176
	v_add_f32_e32 v177, 1.0, v177
	v_add_f32_e32 v178, 1.0, v178
	v_add_f32_e32 v179, 1.0, v179
	v_rcp_f32_e32 v176, v176
	v_rcp_f32_e32 v177, v177
	v_rcp_f32_e32 v178, v178
	v_rcp_f32_e32 v179, v179
	s_nop 0
	v_cvt_pk_bf16_f32 v176, v176, v177
	v_cvt_pk_bf16_f32 v177, v178, v179
	ds_write_b64 v108, v[176:177] offset:12288
	s_waitcnt vmcnt(12)
	v_mfma_f32_16x16x32_bf16 v[26:29], v[82:85], v[18:21], 0
	v_mfma_f32_16x16x32_bf16 v[26:29], v[86:89], v[22:25], v[26:29]
	v_mfma_f32_16x16x32_bf16 v[30:33], v[82:85], v[38:41], 0
	v_mfma_f32_16x16x32_bf16 v[30:33], v[86:89], v[42:45], v[30:33]
	v_add_u32_e32 v108, 0xa0, v154
	s_nop 7
	v_pk_add_f32 v[26:27], v[26:27], v[90:91]
	v_pk_add_f32 v[28:29], v[28:29], v[92:93]
	v_pk_add_f32 v[30:31], v[30:31], v[90:91]
	v_pk_add_f32 v[32:33], v[32:33], v[92:93]
	s_add_u32 s16, s0, 0x3a000
	s_addc_u32 s17, s1, 0
	global_load_dwordx4 v[82:85], v153, s[16:17] offset:0
	global_load_dwordx4 v[86:89], v153, s[16:17] offset:64
	s_add_u32 s18, s70, 0x280
	s_addc_u32 s19, s71, 0
	global_load_dwordx4 v[90:93], v159, s[18:19]
	v_mul_f32_e32 v168, 0xbfb8aa3b, v26
	v_mul_f32_e32 v169, 0xbfb8aa3b, v27
	v_mul_f32_e32 v170, 0xbfb8aa3b, v28
	v_mul_f32_e32 v171, 0xbfb8aa3b, v29
	v_exp_f32_e32 v168, v168
	v_exp_f32_e32 v169, v169
	v_exp_f32_e32 v170, v170
	v_exp_f32_e32 v171, v171
	v_add_f32_e32 v168, 1.0, v168
	v_add_f32_e32 v169, 1.0, v169
	v_add_f32_e32 v170, 1.0, v170
	v_add_f32_e32 v171, 1.0, v171
	v_rcp_f32_e32 v168, v168
	v_rcp_f32_e32 v169, v169
	v_rcp_f32_e32 v170, v170
	v_rcp_f32_e32 v171, v171
	s_nop 0
	v_cvt_pk_bf16_f32 v168, v168, v169
	v_cvt_pk_bf16_f32 v169, v170, v171
	ds_write_b64 v108, v[168:169] offset:0
	v_mul_f32_e32 v176, 0xbfb8aa3b, v30
	v_mul_f32_e32 v177, 0xbfb8aa3b, v31
	v_mul_f32_e32 v178, 0xbfb8aa3b, v32
	v_mul_f32_e32 v179, 0xbfb8aa3b, v33
	v_exp_f32_e32 v176, v176
	v_exp_f32_e32 v177, v177
	v_exp_f32_e32 v178, v178
	v_exp_f32_e32 v179, v179
	v_add_f32_e32 v176, 1.0, v176
	v_add_f32_e32 v177, 1.0, v177
	v_add_f32_e32 v178, 1.0, v178
	v_add_f32_e32 v179, 1.0, v179
	v_rcp_f32_e32 v176, v176
	v_rcp_f32_e32 v177, v177
	v_rcp_f32_e32 v178, v178
	v_rcp_f32_e32 v179, v179
	s_nop 0
	v_cvt_pk_bf16_f32 v176, v176, v177
	v_cvt_pk_bf16_f32 v177, v178, v179
	ds_write_b64 v108, v[176:177] offset:12288
	s_waitcnt vmcnt(12)
	v_mfma_f32_16x16x32_bf16 v[26:29], v[94:97], v[18:21], 0
	v_mfma_f32_16x16x32_bf16 v[26:29], v[160:163], v[22:25], v[26:29]
	v_mfma_f32_16x16x32_bf16 v[30:33], v[94:97], v[38:41], 0
	v_mfma_f32_16x16x32_bf16 v[30:33], v[160:163], v[42:45], v[30:33]
	v_add_u32_e32 v108, 0xc0, v154
	s_nop 7
	v_pk_add_f32 v[26:27], v[26:27], v[164:165]
	v_pk_add_f32 v[28:29], v[28:29], v[166:167]
	v_pk_add_f32 v[30:31], v[30:31], v[164:165]
	v_pk_add_f32 v[32:33], v[32:33], v[166:167]
	s_add_u32 s16, s0, 0x3b000
	s_addc_u32 s17, s1, 0
	global_load_dwordx4 v[94:97], v153, s[16:17] offset:0
	global_load_dwordx4 v[160:163], v153, s[16:17] offset:64
	s_add_u32 s18, s70, 0x2c0
	s_addc_u32 s19, s71, 0
	global_load_dwordx4 v[164:167], v159, s[18:19]
	v_mul_f32_e32 v168, 0xbfb8aa3b, v26
	v_mul_f32_e32 v169, 0xbfb8aa3b, v27
	v_mul_f32_e32 v170, 0xbfb8aa3b, v28
	v_mul_f32_e32 v171, 0xbfb8aa3b, v29
	v_exp_f32_e32 v168, v168
	v_exp_f32_e32 v169, v169
	v_exp_f32_e32 v170, v170
	v_exp_f32_e32 v171, v171
	v_add_f32_e32 v168, 1.0, v168
	v_add_f32_e32 v169, 1.0, v169
	v_add_f32_e32 v170, 1.0, v170
	v_add_f32_e32 v171, 1.0, v171
	v_rcp_f32_e32 v168, v168
	v_rcp_f32_e32 v169, v169
	v_rcp_f32_e32 v170, v170
	v_rcp_f32_e32 v171, v171
	s_nop 0
	v_cvt_pk_bf16_f32 v168, v168, v169
	v_cvt_pk_bf16_f32 v169, v170, v171
	ds_write_b64 v108, v[168:169] offset:0
	v_mul_f32_e32 v176, 0xbfb8aa3b, v30
	v_mul_f32_e32 v177, 0xbfb8aa3b, v31
	v_mul_f32_e32 v178, 0xbfb8aa3b, v32
	v_mul_f32_e32 v179, 0xbfb8aa3b, v33
	v_exp_f32_e32 v176, v176
	v_exp_f32_e32 v177, v177
	v_exp_f32_e32 v178, v178
	v_exp_f32_e32 v179, v179
	v_add_f32_e32 v176, 1.0, v176
	v_add_f32_e32 v177, 1.0, v177
	v_add_f32_e32 v178, 1.0, v178
	v_add_f32_e32 v179, 1.0, v179
	v_rcp_f32_e32 v176, v176
	v_rcp_f32_e32 v177, v177
	v_rcp_f32_e32 v178, v178
	v_rcp_f32_e32 v179, v179
	s_nop 0
	v_cvt_pk_bf16_f32 v176, v176, v177
	v_cvt_pk_bf16_f32 v177, v178, v179
	ds_write_b64 v108, v[176:177] offset:12288
	s_waitcnt vmcnt(12)
	v_mfma_f32_16x16x32_bf16 v[26:29], v[46:49], v[18:21], 0
	v_mfma_f32_16x16x32_bf16 v[26:29], v[50:53], v[22:25], v[26:29]
	v_mfma_f32_16x16x32_bf16 v[30:33], v[46:49], v[38:41], 0
	v_mfma_f32_16x16x32_bf16 v[30:33], v[50:53], v[42:45], v[30:33]
	v_add_u32_e32 v108, 0xe0, v154
	s_nop 7
	v_pk_add_f32 v[26:27], v[26:27], v[54:55]
	v_pk_add_f32 v[28:29], v[28:29], v[56:57]
	v_pk_add_f32 v[30:31], v[30:31], v[54:55]
	v_pk_add_f32 v[32:33], v[32:33], v[56:57]
	v_mul_f32_e32 v168, 0xbfb8aa3b, v26
	v_mul_f32_e32 v169, 0xbfb8aa3b, v27
	v_mul_f32_e32 v170, 0xbfb8aa3b, v28
	v_mul_f32_e32 v171, 0xbfb8aa3b, v29
	v_exp_f32_e32 v168, v168
	v_exp_f32_e32 v169, v169
	v_exp_f32_e32 v170, v170
	v_exp_f32_e32 v171, v171
	v_add_f32_e32 v168, 1.0, v168
	v_add_f32_e32 v169, 1.0, v169
	v_add_f32_e32 v170, 1.0, v170
	v_add_f32_e32 v171, 1.0, v171
	v_rcp_f32_e32 v168, v168
	v_rcp_f32_e32 v169, v169
	v_rcp_f32_e32 v170, v170
	v_rcp_f32_e32 v171, v171
	s_nop 0
	v_cvt_pk_bf16_f32 v168, v168, v169
	v_cvt_pk_bf16_f32 v169, v170, v171
	ds_write_b64 v108, v[168:169] offset:0
	v_mul_f32_e32 v176, 0xbfb8aa3b, v30
	v_mul_f32_e32 v177, 0xbfb8aa3b, v31
	v_mul_f32_e32 v178, 0xbfb8aa3b, v32
	v_mul_f32_e32 v179, 0xbfb8aa3b, v33
	v_exp_f32_e32 v176, v176
	v_exp_f32_e32 v177, v177
	v_exp_f32_e32 v178, v178
	v_exp_f32_e32 v179, v179
	v_add_f32_e32 v176, 1.0, v176
	v_add_f32_e32 v177, 1.0, v177
	v_add_f32_e32 v178, 1.0, v178
	v_add_f32_e32 v179, 1.0, v179
	v_rcp_f32_e32 v176, v176
	v_rcp_f32_e32 v177, v177
	v_rcp_f32_e32 v178, v178
	v_rcp_f32_e32 v179, v179
	s_nop 0
	v_cvt_pk_bf16_f32 v176, v176, v177
	v_cvt_pk_bf16_f32 v177, v178, v179
	ds_write_b64 v108, v[176:177] offset:12288
	s_waitcnt vmcnt(9)
	v_mfma_f32_16x16x32_bf16 v[26:29], v[58:61], v[18:21], 0
	v_mfma_f32_16x16x32_bf16 v[26:29], v[62:65], v[22:25], v[26:29]
	v_mfma_f32_16x16x32_bf16 v[30:33], v[58:61], v[38:41], 0
	v_mfma_f32_16x16x32_bf16 v[30:33], v[62:65], v[42:45], v[30:33]
	v_add_u32_e32 v108, 0x100, v154
	s_nop 7
	v_pk_add_f32 v[26:27], v[26:27], v[66:67]
	v_pk_add_f32 v[28:29], v[28:29], v[68:69]
	v_pk_add_f32 v[30:31], v[30:31], v[66:67]
	v_pk_add_f32 v[32:33], v[32:33], v[68:69]
	v_mul_f32_e32 v168, 0xbfb8aa3b, v26
	v_mul_f32_e32 v169, 0xbfb8aa3b, v27
	v_mul_f32_e32 v170, 0xbfb8aa3b, v28
	v_mul_f32_e32 v171, 0xbfb8aa3b, v29
	v_exp_f32_e32 v168, v168
	v_exp_f32_e32 v169, v169
	v_exp_f32_e32 v170, v170
	v_exp_f32_e32 v171, v171
	v_add_f32_e32 v168, 1.0, v168
	v_add_f32_e32 v169, 1.0, v169
	v_add_f32_e32 v170, 1.0, v170
	v_add_f32_e32 v171, 1.0, v171
	v_rcp_f32_e32 v168, v168
	v_rcp_f32_e32 v169, v169
	v_rcp_f32_e32 v170, v170
	v_rcp_f32_e32 v171, v171
	s_nop 0
	v_cvt_pk_bf16_f32 v168, v168, v169
	v_cvt_pk_bf16_f32 v169, v170, v171
	ds_write_b64 v108, v[168:169] offset:0
	v_mul_f32_e32 v176, 0xbfb8aa3b, v30
	v_mul_f32_e32 v177, 0xbfb8aa3b, v31
	v_mul_f32_e32 v178, 0xbfb8aa3b, v32
	v_mul_f32_e32 v179, 0xbfb8aa3b, v33
	v_exp_f32_e32 v176, v176
	v_exp_f32_e32 v177, v177
	v_exp_f32_e32 v178, v178
	v_exp_f32_e32 v179, v179
	v_add_f32_e32 v176, 1.0, v176
	v_add_f32_e32 v177, 1.0, v177
	v_add_f32_e32 v178, 1.0, v178
	v_add_f32_e32 v179, 1.0, v179
	v_rcp_f32_e32 v176, v176
	v_rcp_f32_e32 v177, v177
	v_rcp_f32_e32 v178, v178
	v_rcp_f32_e32 v179, v179
	s_nop 0
	v_cvt_pk_bf16_f32 v176, v176, v177
	v_cvt_pk_bf16_f32 v177, v178, v179
	ds_write_b64 v108, v[176:177] offset:12288
	s_waitcnt vmcnt(6)
	v_mfma_f32_16x16x32_bf16 v[26:29], v[70:73], v[18:21], 0
	v_mfma_f32_16x16x32_bf16 v[26:29], v[74:77], v[22:25], v[26:29]
	v_mfma_f32_16x16x32_bf16 v[30:33], v[70:73], v[38:41], 0
	v_mfma_f32_16x16x32_bf16 v[30:33], v[74:77], v[42:45], v[30:33]
	v_add_u32_e32 v108, 0x120, v154
	s_nop 7
	v_pk_add_f32 v[26:27], v[26:27], v[78:79]
	v_pk_add_f32 v[28:29], v[28:29], v[80:81]
	v_pk_add_f32 v[30:31], v[30:31], v[78:79]
	v_pk_add_f32 v[32:33], v[32:33], v[80:81]
	v_mul_f32_e32 v168, 0xbfb8aa3b, v26
	v_mul_f32_e32 v169, 0xbfb8aa3b, v27
	v_mul_f32_e32 v170, 0xbfb8aa3b, v28
	v_mul_f32_e32 v171, 0xbfb8aa3b, v29
	v_exp_f32_e32 v168, v168
	v_exp_f32_e32 v169, v169
	v_exp_f32_e32 v170, v170
	v_exp_f32_e32 v171, v171
	v_add_f32_e32 v168, 1.0, v168
	v_add_f32_e32 v169, 1.0, v169
	v_add_f32_e32 v170, 1.0, v170
	v_add_f32_e32 v171, 1.0, v171
	v_rcp_f32_e32 v168, v168
	v_rcp_f32_e32 v169, v169
	v_rcp_f32_e32 v170, v170
	v_rcp_f32_e32 v171, v171
	s_nop 0
	v_cvt_pk_bf16_f32 v168, v168, v169
	v_cvt_pk_bf16_f32 v169, v170, v171
	ds_write_b64 v108, v[168:169] offset:0
	v_mul_f32_e32 v176, 0xbfb8aa3b, v30
	v_mul_f32_e32 v177, 0xbfb8aa3b, v31
	v_mul_f32_e32 v178, 0xbfb8aa3b, v32
	v_mul_f32_e32 v179, 0xbfb8aa3b, v33
	v_exp_f32_e32 v176, v176
	v_exp_f32_e32 v177, v177
	v_exp_f32_e32 v178, v178
	v_exp_f32_e32 v179, v179
	v_add_f32_e32 v176, 1.0, v176
	v_add_f32_e32 v177, 1.0, v177
	v_add_f32_e32 v178, 1.0, v178
	v_add_f32_e32 v179, 1.0, v179
	v_rcp_f32_e32 v176, v176
	v_rcp_f32_e32 v177, v177
	v_rcp_f32_e32 v178, v178
	v_rcp_f32_e32 v179, v179
	s_nop 0
	v_cvt_pk_bf16_f32 v176, v176, v177
	v_cvt_pk_bf16_f32 v177, v178, v179
	ds_write_b64 v108, v[176:177] offset:12288
	s_waitcnt vmcnt(3)
	v_mfma_f32_16x16x32_bf16 v[26:29], v[82:85], v[18:21], 0
	v_mfma_f32_16x16x32_bf16 v[26:29], v[86:89], v[22:25], v[26:29]
	v_mfma_f32_16x16x32_bf16 v[30:33], v[82:85], v[38:41], 0
	v_mfma_f32_16x16x32_bf16 v[30:33], v[86:89], v[42:45], v[30:33]
	v_add_u32_e32 v108, 0x140, v154
	s_nop 7
	v_pk_add_f32 v[26:27], v[26:27], v[90:91]
	v_pk_add_f32 v[28:29], v[28:29], v[92:93]
	v_pk_add_f32 v[30:31], v[30:31], v[90:91]
	v_pk_add_f32 v[32:33], v[32:33], v[92:93]
	v_mul_f32_e32 v168, 0xbfb8aa3b, v26
	v_mul_f32_e32 v169, 0xbfb8aa3b, v27
	v_mul_f32_e32 v170, 0xbfb8aa3b, v28
	v_mul_f32_e32 v171, 0xbfb8aa3b, v29
	v_exp_f32_e32 v168, v168
	v_exp_f32_e32 v169, v169
	v_exp_f32_e32 v170, v170
	v_exp_f32_e32 v171, v171
	v_add_f32_e32 v168, 1.0, v168
	v_add_f32_e32 v169, 1.0, v169
	v_add_f32_e32 v170, 1.0, v170
	v_add_f32_e32 v171, 1.0, v171
	v_rcp_f32_e32 v168, v168
	v_rcp_f32_e32 v169, v169
	v_rcp_f32_e32 v170, v170
	v_rcp_f32_e32 v171, v171
	s_nop 0
	v_cvt_pk_bf16_f32 v168, v168, v169
	v_cvt_pk_bf16_f32 v169, v170, v171
	ds_write_b64 v108, v[168:169] offset:0
	v_mul_f32_e32 v176, 0xbfb8aa3b, v30
	v_mul_f32_e32 v177, 0xbfb8aa3b, v31
	v_mul_f32_e32 v178, 0xbfb8aa3b, v32
	v_mul_f32_e32 v179, 0xbfb8aa3b, v33
	v_exp_f32_e32 v176, v176
	v_exp_f32_e32 v177, v177
	v_exp_f32_e32 v178, v178
	v_exp_f32_e32 v179, v179
	v_add_f32_e32 v176, 1.0, v176
	v_add_f32_e32 v177, 1.0, v177
	v_add_f32_e32 v178, 1.0, v178
	v_add_f32_e32 v179, 1.0, v179
	v_rcp_f32_e32 v176, v176
	v_rcp_f32_e32 v177, v177
	v_rcp_f32_e32 v178, v178
	v_rcp_f32_e32 v179, v179
	s_nop 0
	v_cvt_pk_bf16_f32 v176, v176, v177
	v_cvt_pk_bf16_f32 v177, v178, v179
	ds_write_b64 v108, v[176:177] offset:12288
	s_waitcnt vmcnt(0)
	v_mfma_f32_16x16x32_bf16 v[26:29], v[94:97], v[18:21], 0
	v_mfma_f32_16x16x32_bf16 v[26:29], v[160:163], v[22:25], v[26:29]
	v_mfma_f32_16x16x32_bf16 v[30:33], v[94:97], v[38:41], 0
	v_mfma_f32_16x16x32_bf16 v[30:33], v[160:163], v[42:45], v[30:33]
	v_add_u32_e32 v108, 0x160, v154
	s_nop 7
	v_pk_add_f32 v[26:27], v[26:27], v[164:165]
	v_pk_add_f32 v[28:29], v[28:29], v[166:167]
	v_pk_add_f32 v[30:31], v[30:31], v[164:165]
	v_pk_add_f32 v[32:33], v[32:33], v[166:167]
	v_mul_f32_e32 v168, 0xbfb8aa3b, v26
	v_mul_f32_e32 v169, 0xbfb8aa3b, v27
	v_mul_f32_e32 v170, 0xbfb8aa3b, v28
	v_mul_f32_e32 v171, 0xbfb8aa3b, v29
	v_exp_f32_e32 v168, v168
	v_exp_f32_e32 v169, v169
	v_exp_f32_e32 v170, v170
	v_exp_f32_e32 v171, v171
	v_add_f32_e32 v168, 1.0, v168
	v_add_f32_e32 v169, 1.0, v169
	v_add_f32_e32 v170, 1.0, v170
	v_add_f32_e32 v171, 1.0, v171
	v_rcp_f32_e32 v168, v168
	v_rcp_f32_e32 v169, v169
	v_rcp_f32_e32 v170, v170
	v_rcp_f32_e32 v171, v171
	s_nop 0
	v_cvt_pk_bf16_f32 v168, v168, v169
	v_cvt_pk_bf16_f32 v169, v170, v171
	ds_write_b64 v108, v[168:169] offset:0
	v_mul_f32_e32 v176, 0xbfb8aa3b, v30
	v_mul_f32_e32 v177, 0xbfb8aa3b, v31
	v_mul_f32_e32 v178, 0xbfb8aa3b, v32
	v_mul_f32_e32 v179, 0xbfb8aa3b, v33
	v_exp_f32_e32 v176, v176
	v_exp_f32_e32 v177, v177
	v_exp_f32_e32 v178, v178
	v_exp_f32_e32 v179, v179
	v_add_f32_e32 v176, 1.0, v176
	v_add_f32_e32 v177, 1.0, v177
	v_add_f32_e32 v178, 1.0, v178
	v_add_f32_e32 v179, 1.0, v179
	v_rcp_f32_e32 v176, v176
	v_rcp_f32_e32 v177, v177
	v_rcp_f32_e32 v178, v178
	v_rcp_f32_e32 v179, v179
	s_nop 0
	v_cvt_pk_bf16_f32 v176, v176, v177
	v_cvt_pk_bf16_f32 v177, v178, v179
	ds_write_b64 v108, v[176:177] offset:12288
	s_branch .LBB0_402
.Lb3w_4:
	ds_read_b128 v[2:5], v0 offset:128
	ds_read_b128 v[6:9], v0 offset:192
	ds_read_b128 v[10:13], v0 offset:8576
	ds_read_b128 v[14:17], v0 offset:8640
	s_add_u32 s16, s0, 0x3c000
	s_addc_u32 s17, s1, 0
	global_load_dwordx4 v[18:21], v153, s[16:17] offset:0
	global_load_dwordx4 v[22:25], v153, s[16:17] offset:64
	s_add_u32 s18, s70, 0x300
	s_addc_u32 s19, s71, 0
	global_load_dwordx4 v[38:41], v159, s[18:19]
	s_add_u32 s16, s0, 0x3d000
	s_addc_u32 s17, s1, 0
	global_load_dwordx4 v[42:45], v153, s[16:17] offset:0
	global_load_dwordx4 v[46:49], v153, s[16:17] offset:64
	s_add_u32 s18, s70, 0x340
	s_addc_u32 s19, s71, 0
	global_load_dwordx4 v[50:53], v159, s[18:19]
	s_add_u32 s16, s0, 0x3e000
	s_addc_u32 s17, s1, 0
	global_load_dwordx4 v[54:57], v153, s[16:17] offset:0
	global_load_dwordx4 v[58:61], v153, s[16:17] offset:64
	s_add_u32 s18, s70, 0x380
	s_addc_u32 s19, s71, 0
	global_load_dwordx4 v[62:65], v159, s[18:19]
	s_add_u32 s16, s0, 0x3f000
	s_addc_u32 s17, s1, 0
	global_load_dwordx4 v[66:69], v153, s[16:17] offset:0
	global_load_dwordx4 v[70:73], v153, s[16:17] offset:64
	s_add_u32 s18, s70, 0x3c0
	s_addc_u32 s19, s71, 0
	global_load_dwordx4 v[74:77], v159, s[18:19]
	s_add_u32 s16, s0, 0x40000
	s_addc_u32 s17, s1, 0
	global_load_dwordx4 v[78:81], v153, s[16:17] offset:0
	global_load_dwordx4 v[82:85], v153, s[16:17] offset:64
	s_add_u32 s18, s70, 0x400
	s_addc_u32 s19, s71, 0
	global_load_dwordx4 v[86:89], v159, s[18:19]
	s_waitcnt vmcnt(12) lgkmcnt(0)
	v_mfma_f32_16x16x32_bf16 v[26:29], v[18:21], v[2:5], 0
	v_mfma_f32_16x16x32_bf16 v[26:29], v[22:25], v[6:9], v[26:29]
	v_mfma_f32_16x16x32_bf16 v[30:33], v[18:21], v[10:13], 0
	v_mfma_f32_16x16x32_bf16 v[30:33], v[22:25], v[14:17], v[30:33]
	v_add_u32_e32 v108, 0x180, v154
	s_nop 7
	v_pk_add_f32 v[26:27], v[26:27], v[38:39]
	v_pk_add_f32 v[28:29], v[28:29], v[40:41]
	v_pk_add_f32 v[30:31], v[30:31], v[38:39]
	v_pk_add_f32 v[32:33], v[32:33], v[40:41]
	s_add_u32 s16, s0, 0x41000
	s_addc_u32 s17, s1, 0
	global_load_dwordx4 v[18:21], v153, s[16:17] offset:0
	global_load_dwordx4 v[22:25], v153, s[16:17] offset:64
	s_add_u32 s18, s70, 0x440
	s_addc_u32 s19, s71, 0
	global_load_dwordx4 v[38:41], v159, s[18:19]
	v_mul_f32_e32 v168, 0xbfb8aa3b, v26
	v_mul_f32_e32 v169, 0xbfb8aa3b, v27
	v_mul_f32_e32 v170, 0xbfb8aa3b, v28
	v_mul_f32_e32 v171, 0xbfb8aa3b, v29
	v_exp_f32_e32 v168, v168
	v_exp_f32_e32 v169, v169
	v_exp_f32_e32 v170, v170
	v_exp_f32_e32 v171, v171
	v_add_f32_e32 v168, 1.0, v168
	v_add_f32_e32 v169, 1.0, v169
	v_add_f32_e32 v170, 1.0, v170
	v_add_f32_e32 v171, 1.0, v171
	v_rcp_f32_e32 v168, v168
	v_rcp_f32_e32 v169, v169
	v_rcp_f32_e32 v170, v170
	v_rcp_f32_e32 v171, v171
	s_nop 0
	v_cvt_pk_bf16_f32 v168, v168, v169
	v_cvt_pk_bf16_f32 v169, v170, v171
	ds_write_b64 v108, v[168:169] offset:0
	v_mul_f32_e32 v176, 0xbfb8aa3b, v30
	v_mul_f32_e32 v177, 0xbfb8aa3b, v31
	v_mul_f32_e32 v178, 0xbfb8aa3b, v32
	v_mul_f32_e32 v179, 0xbfb8aa3b, v33
	v_exp_f32_e32 v176, v176
	v_exp_f32_e32 v177, v177
	v_exp_f32_e32 v178, v178
	v_exp_f32_e32 v179, v179
	v_add_f32_e32 v176, 1.0, v176
	v_add_f32_e32 v177, 1.0, v177
	v_add_f32_e32 v178, 1.0, v178
	v_add_f32_e32 v179, 1.0, v179
	v_rcp_f32_e32 v176, v176
	v_rcp_f32_e32 v177, v177
	v_rcp_f32_e32 v178, v178
	v_rcp_f32_e32 v179, v179
	s_nop 0
	v_cvt_pk_bf16_f32 v176, v176, v177
	v_cvt_pk_bf16_f32 v177, v178, v179
	ds_write_b64 v108, v[176:177] offset:12288
	s_waitcnt vmcnt(12)
	v_mfma_f32_16x16x32_bf16 v[26:29], v[42:45], v[2:5], 0
	v_mfma_f32_16x16x32_bf16 v[26:29], v[46:49], v[6:9], v[26:29]
	v_mfma_f32_16x16x32_bf16 v[30:33], v[42:45], v[10:13], 0
	v_mfma_f32_16x16x32_bf16 v[30:33], v[46:49], v[14:17], v[30:33]
	v_add_u32_e32 v108, 0x1a0, v154
	s_nop 7
	v_pk_add_f32 v[26:27], v[26:27], v[50:51]
	v_pk_add_f32 v[28:29], v[28:29], v[52:53]
	v_pk_add_f32 v[30:31], v[30:31], v[50:51]
	v_pk_add_f32 v[32:33], v[32:33], v[52:53]
	s_add_u32 s16, s0, 0x42000
	s_addc_u32 s17, s1, 0
	global_load_dwordx4 v[42:45], v153, s[16:17] offset:0
	global_load_dwordx4 v[46:49], v153, s[16:17] offset:64
	s_add_u32 s18, s70, 0x480
	s_addc_u32 s19, s71, 0
	global_load_dwordx4 v[50:53], v159, s[18:19]
	v_mul_f32_e32 v168, 0xbfb8aa3b, v26
	v_mul_f32_e32 v169, 0xbfb8aa3b, v27
	v_mul_f32_e32 v170, 0xbfb8aa3b, v28
	v_mul_f32_e32 v171, 0xbfb8aa3b, v29
	v_exp_f32_e32 v168, v168
	v_exp_f32_e32 v169, v169
	v_exp_f32_e32 v170, v170
	v_exp_f32_e32 v171, v171
	v_add_f32_e32 v168, 1.0, v168
	v_add_f32_e32 v169, 1.0, v169
	v_add_f32_e32 v170, 1.0, v170
	v_add_f32_e32 v171, 1.0, v171
	v_rcp_f32_e32 v168, v168
	v_rcp_f32_e32 v169, v169
	v_rcp_f32_e32 v170, v170
	v_rcp_f32_e32 v171, v171
	s_nop 0
	v_cvt_pk_bf16_f32 v168, v168, v169
	v_cvt_pk_bf16_f32 v169, v170, v171
	ds_write_b64 v108, v[168:169] offset:0
	v_mul_f32_e32 v176, 0xbfb8aa3b, v30
	v_mul_f32_e32 v177, 0xbfb8aa3b, v31
	v_mul_f32_e32 v178, 0xbfb8aa3b, v32
	v_mul_f32_e32 v179, 0xbfb8aa3b, v33
	v_exp_f32_e32 v176, v176
	v_exp_f32_e32 v177, v177
	v_exp_f32_e32 v178, v178
	v_exp_f32_e32 v179, v179
	v_add_f32_e32 v176, 1.0, v176
	v_add_f32_e32 v177, 1.0, v177
	v_add_f32_e32 v178, 1.0, v178
	v_add_f32_e32 v179, 1.0, v179
	v_rcp_f32_e32 v176, v176
	v_rcp_f32_e32 v177, v177
	v_rcp_f32_e32 v178, v178
	v_rcp_f32_e32 v179, v179
	s_nop 0
	v_cvt_pk_bf16_f32 v176, v176, v177
	v_cvt_pk_bf16_f32 v177, v178, v179
	ds_write_b64 v108, v[176:177] offset:12288
	s_waitcnt vmcnt(12)
	v_mfma_f32_16x16x32_bf16 v[26:29], v[54:57], v[2:5], 0
	v_mfma_f32_16x16x32_bf16 v[26:29], v[58:61], v[6:9], v[26:29]
	v_mfma_f32_16x16x32_bf16 v[30:33], v[54:57], v[10:13], 0
	v_mfma_f32_16x16x32_bf16 v[30:33], v[58:61], v[14:17], v[30:33]
	v_add_u32_e32 v108, 0x1c0, v154
	s_nop 7
	v_pk_add_f32 v[26:27], v[26:27], v[62:63]
	v_pk_add_f32 v[28:29], v[28:29], v[64:65]
	v_pk_add_f32 v[30:31], v[30:31], v[62:63]
	v_pk_add_f32 v[32:33], v[32:33], v[64:65]
	s_add_u32 s16, s0, 0x43000
	s_addc_u32 s17, s1, 0
	global_load_dwordx4 v[54:57], v153, s[16:17] offset:0
	global_load_dwordx4 v[58:61], v153, s[16:17] offset:64
	s_add_u32 s18, s70, 0x4c0
	s_addc_u32 s19, s71, 0
	global_load_dwordx4 v[62:65], v159, s[18:19]
	v_mul_f32_e32 v168, 0xbfb8aa3b, v26
	v_mul_f32_e32 v169, 0xbfb8aa3b, v27
	v_mul_f32_e32 v170, 0xbfb8aa3b, v28
	v_mul_f32_e32 v171, 0xbfb8aa3b, v29
	v_exp_f32_e32 v168, v168
	v_exp_f32_e32 v169, v169
	v_exp_f32_e32 v170, v170
	v_exp_f32_e32 v171, v171
	v_add_f32_e32 v168, 1.0, v168
	v_add_f32_e32 v169, 1.0, v169
	v_add_f32_e32 v170, 1.0, v170
	v_add_f32_e32 v171, 1.0, v171
	v_rcp_f32_e32 v168, v168
	v_rcp_f32_e32 v169, v169
	v_rcp_f32_e32 v170, v170
	v_rcp_f32_e32 v171, v171
	s_nop 0
	v_cvt_pk_bf16_f32 v168, v168, v169
	v_cvt_pk_bf16_f32 v169, v170, v171
	ds_write_b64 v108, v[168:169] offset:0
	v_mul_f32_e32 v176, 0xbfb8aa3b, v30
	v_mul_f32_e32 v177, 0xbfb8aa3b, v31
	v_mul_f32_e32 v178, 0xbfb8aa3b, v32
	v_mul_f32_e32 v179, 0xbfb8aa3b, v33
	v_exp_f32_e32 v176, v176
	v_exp_f32_e32 v177, v177
	v_exp_f32_e32 v178, v178
	v_exp_f32_e32 v179, v179
	v_add_f32_e32 v176, 1.0, v176
	v_add_f32_e32 v177, 1.0, v177
	v_add_f32_e32 v178, 1.0, v178
	v_add_f32_e32 v179, 1.0, v179
	v_rcp_f32_e32 v176, v176
	v_rcp_f32_e32 v177, v177
	v_rcp_f32_e32 v178, v178
	v_rcp_f32_e32 v179, v179
	s_nop 0
	v_cvt_pk_bf16_f32 v176, v176, v177
	v_cvt_pk_bf16_f32 v177, v178, v179
	ds_write_b64 v108, v[176:177] offset:12288
	s_waitcnt vmcnt(12)
	v_mfma_f32_16x16x32_bf16 v[26:29], v[66:69], v[2:5], 0
	v_mfma_f32_16x16x32_bf16 v[26:29], v[70:73], v[6:9], v[26:29]
	v_mfma_f32_16x16x32_bf16 v[30:33], v[66:69], v[10:13], 0
	v_mfma_f32_16x16x32_bf16 v[30:33], v[70:73], v[14:17], v[30:33]
	v_add_u32_e32 v108, 0x1e0, v154
	s_nop 7
	v_pk_add_f32 v[26:27], v[26:27], v[74:75]
	v_pk_add_f32 v[28:29], v[28:29], v[76:77]
	v_pk_add_f32 v[30:31], v[30:31], v[74:75]
	v_pk_add_f32 v[32:33], v[32:33], v[76:77]
	s_add_u32 s16, s0, 0x44000
	s_addc_u32 s17, s1, 0
	global_load_dwordx4 v[66:69], v153, s[16:17] offset:0
	global_load_dwordx4 v[70:73], v153, s[16:17] offset:64
	s_add_u32 s18, s70, 0x500
	s_addc_u32 s19, s71, 0
	global_load_dwordx4 v[74:77], v159, s[18:19]
	v_mul_f32_e32 v168, 0xbfb8aa3b, v26
	v_mul_f32_e32 v169, 0xbfb8aa3b, v27
	v_mul_f32_e32 v170, 0xbfb8aa3b, v28
	v_mul_f32_e32 v171, 0xbfb8aa3b, v29
	v_exp_f32_e32 v168, v168
	v_exp_f32_e32 v169, v169
	v_exp_f32_e32 v170, v170
	v_exp_f32_e32 v171, v171
	v_add_f32_e32 v168, 1.0, v168
	v_add_f32_e32 v169, 1.0, v169
	v_add_f32_e32 v170, 1.0, v170
	v_add_f32_e32 v171, 1.0, v171
	v_rcp_f32_e32 v168, v168
	v_rcp_f32_e32 v169, v169
	v_rcp_f32_e32 v170, v170
	v_rcp_f32_e32 v171, v171
	s_nop 0
	v_cvt_pk_bf16_f32 v168, v168, v169
	v_cvt_pk_bf16_f32 v169, v170, v171
	ds_write_b64 v108, v[168:169] offset:0
	v_mul_f32_e32 v176, 0xbfb8aa3b, v30
	v_mul_f32_e32 v177, 0xbfb8aa3b, v31
	v_mul_f32_e32 v178, 0xbfb8aa3b, v32
	v_mul_f32_e32 v179, 0xbfb8aa3b, v33
	v_exp_f32_e32 v176, v176
	v_exp_f32_e32 v177, v177
	v_exp_f32_e32 v178, v178
	v_exp_f32_e32 v179, v179
	v_add_f32_e32 v176, 1.0, v176
	v_add_f32_e32 v177, 1.0, v177
	v_add_f32_e32 v178, 1.0, v178
	v_add_f32_e32 v179, 1.0, v179
	v_rcp_f32_e32 v176, v176
	v_rcp_f32_e32 v177, v177
	v_rcp_f32_e32 v178, v178
	v_rcp_f32_e32 v179, v179
	s_nop 0
	v_cvt_pk_bf16_f32 v176, v176, v177
	v_cvt_pk_bf16_f32 v177, v178, v179
	ds_write_b64 v108, v[176:177] offset:12288
	s_waitcnt vmcnt(12)
	v_mfma_f32_16x16x32_bf16 v[26:29], v[78:81], v[2:5], 0
	v_mfma_f32_16x16x32_bf16 v[26:29], v[82:85], v[6:9], v[26:29]
	v_mfma_f32_16x16x32_bf16 v[30:33], v[78:81], v[10:13], 0
	v_mfma_f32_16x16x32_bf16 v[30:33], v[82:85], v[14:17], v[30:33]
	v_add_u32_e32 v108, 0x200, v154
	s_nop 7
	v_pk_add_f32 v[26:27], v[26:27], v[86:87]
	v_pk_add_f32 v[28:29], v[28:29], v[88:89]
	v_pk_add_f32 v[30:31], v[30:31], v[86:87]
	v_pk_add_f32 v[32:33], v[32:33], v[88:89]
	s_add_u32 s16, s0, 0x45000
	s_addc_u32 s17, s1, 0
	global_load_dwordx4 v[78:81], v153, s[16:17] offset:0
	global_load_dwordx4 v[82:85], v153, s[16:17] offset:64
	s_add_u32 s18, s70, 0x540
	s_addc_u32 s19, s71, 0
	global_load_dwordx4 v[86:89], v159, s[18:19]
	v_mul_f32_e32 v168, 0xbfb8aa3b, v26
	v_mul_f32_e32 v169, 0xbfb8aa3b, v27
	v_mul_f32_e32 v170, 0xbfb8aa3b, v28
	v_mul_f32_e32 v171, 0xbfb8aa3b, v29
	v_exp_f32_e32 v168, v168
	v_exp_f32_e32 v169, v169
	v_exp_f32_e32 v170, v170
	v_exp_f32_e32 v171, v171
	v_add_f32_e32 v168, 1.0, v168
	v_add_f32_e32 v169, 1.0, v169
	v_add_f32_e32 v170, 1.0, v170
	v_add_f32_e32 v171, 1.0, v171
	v_rcp_f32_e32 v168, v168
	v_rcp_f32_e32 v169, v169
	v_rcp_f32_e32 v170, v170
	v_rcp_f32_e32 v171, v171
	s_nop 0
	v_cvt_pk_bf16_f32 v168, v168, v169
	v_cvt_pk_bf16_f32 v169, v170, v171
	ds_write_b64 v108, v[168:169] offset:0
	v_mul_f32_e32 v176, 0xbfb8aa3b, v30
	v_mul_f32_e32 v177, 0xbfb8aa3b, v31
	v_mul_f32_e32 v178, 0xbfb8aa3b, v32
	v_mul_f32_e32 v179, 0xbfb8aa3b, v33
	v_exp_f32_e32 v176, v176
	v_exp_f32_e32 v177, v177
	v_exp_f32_e32 v178, v178
	v_exp_f32_e32 v179, v179
	v_add_f32_e32 v176, 1.0, v176
	v_add_f32_e32 v177, 1.0, v177
	v_add_f32_e32 v178, 1.0, v178
	v_add_f32_e32 v179, 1.0, v179
	v_rcp_f32_e32 v176, v176
	v_rcp_f32_e32 v177, v177
	v_rcp_f32_e32 v178, v178
	v_rcp_f32_e32 v179, v179
	s_nop 0
	v_cvt_pk_bf16_f32 v176, v176, v177
	v_cvt_pk_bf16_f32 v177, v178, v179
	ds_write_b64 v108, v[176:177] offset:12288
	s_waitcnt vmcnt(12)
	v_mfma_f32_16x16x32_bf16 v[26:29], v[18:21], v[2:5], 0
	v_mfma_f32_16x16x32_bf16 v[26:29], v[22:25], v[6:9], v[26:29]
	v_mfma_f32_16x16x32_bf16 v[30:33], v[18:21], v[10:13], 0
	v_mfma_f32_16x16x32_bf16 v[30:33], v[22:25], v[14:17], v[30:33]
	v_add_u32_e32 v108, 0x220, v154
	s_nop 7
	v_pk_add_f32 v[26:27], v[26:27], v[38:39]
	v_pk_add_f32 v[28:29], v[28:29], v[40:41]
	v_pk_add_f32 v[30:31], v[30:31], v[38:39]
	v_pk_add_f32 v[32:33], v[32:33], v[40:41]
	s_add_u32 s16, s0, 0x46000
	s_addc_u32 s17, s1, 0
	global_load_dwordx4 v[18:21], v153, s[16:17] offset:0
	global_load_dwordx4 v[22:25], v153, s[16:17] offset:64
	s_add_u32 s18, s70, 0x580
	s_addc_u32 s19, s71, 0
	global_load_dwordx4 v[38:41], v159, s[18:19]
	v_mul_f32_e32 v168, 0xbfb8aa3b, v26
	v_mul_f32_e32 v169, 0xbfb8aa3b, v27
	v_mul_f32_e32 v170, 0xbfb8aa3b, v28
	v_mul_f32_e32 v171, 0xbfb8aa3b, v29
	v_exp_f32_e32 v168, v168
	v_exp_f32_e32 v169, v169
	v_exp_f32_e32 v170, v170
	v_exp_f32_e32 v171, v171
	v_add_f32_e32 v168, 1.0, v168
	v_add_f32_e32 v169, 1.0, v169
	v_add_f32_e32 v170, 1.0, v170
	v_add_f32_e32 v171, 1.0, v171
	v_rcp_f32_e32 v168, v168
	v_rcp_f32_e32 v169, v169
	v_rcp_f32_e32 v170, v170
	v_rcp_f32_e32 v171, v171
	s_nop 0
	v_cvt_pk_bf16_f32 v168, v168, v169
	v_cvt_pk_bf16_f32 v169, v170, v171
	ds_write_b64 v108, v[168:169] offset:0
	v_mul_f32_e32 v176, 0xbfb8aa3b, v30
	v_mul_f32_e32 v177, 0xbfb8aa3b, v31
	v_mul_f32_e32 v178, 0xbfb8aa3b, v32
	v_mul_f32_e32 v179, 0xbfb8aa3b, v33
	v_exp_f32_e32 v176, v176
	v_exp_f32_e32 v177, v177
	v_exp_f32_e32 v178, v178
	v_exp_f32_e32 v179, v179
	v_add_f32_e32 v176, 1.0, v176
	v_add_f32_e32 v177, 1.0, v177
	v_add_f32_e32 v178, 1.0, v178
	v_add_f32_e32 v179, 1.0, v179
	v_rcp_f32_e32 v176, v176
	v_rcp_f32_e32 v177, v177
	v_rcp_f32_e32 v178, v178
	v_rcp_f32_e32 v179, v179
	s_nop 0
	v_cvt_pk_bf16_f32 v176, v176, v177
	v_cvt_pk_bf16_f32 v177, v178, v179
	ds_write_b64 v108, v[176:177] offset:12288
	s_waitcnt vmcnt(12)
	v_mfma_f32_16x16x32_bf16 v[26:29], v[42:45], v[2:5], 0
	v_mfma_f32_16x16x32_bf16 v[26:29], v[46:49], v[6:9], v[26:29]
	v_mfma_f32_16x16x32_bf16 v[30:33], v[42:45], v[10:13], 0
	v_mfma_f32_16x16x32_bf16 v[30:33], v[46:49], v[14:17], v[30:33]
	v_add_u32_e32 v108, 0x240, v154
	s_nop 7
	v_pk_add_f32 v[26:27], v[26:27], v[50:51]
	v_pk_add_f32 v[28:29], v[28:29], v[52:53]
	v_pk_add_f32 v[30:31], v[30:31], v[50:51]
	v_pk_add_f32 v[32:33], v[32:33], v[52:53]
	s_add_u32 s16, s0, 0x47000
	s_addc_u32 s17, s1, 0
	global_load_dwordx4 v[42:45], v153, s[16:17] offset:0
	global_load_dwordx4 v[46:49], v153, s[16:17] offset:64
	s_add_u32 s18, s70, 0x5c0
	s_addc_u32 s19, s71, 0
	global_load_dwordx4 v[50:53], v159, s[18:19]
	v_mul_f32_e32 v168, 0xbfb8aa3b, v26
	v_mul_f32_e32 v169, 0xbfb8aa3b, v27
	v_mul_f32_e32 v170, 0xbfb8aa3b, v28
	v_mul_f32_e32 v171, 0xbfb8aa3b, v29
	v_exp_f32_e32 v168, v168
	v_exp_f32_e32 v169, v169
	v_exp_f32_e32 v170, v170
	v_exp_f32_e32 v171, v171
	v_add_f32_e32 v168, 1.0, v168
	v_add_f32_e32 v169, 1.0, v169
	v_add_f32_e32 v170, 1.0, v170
	v_add_f32_e32 v171, 1.0, v171
	v_rcp_f32_e32 v168, v168
	v_rcp_f32_e32 v169, v169
	v_rcp_f32_e32 v170, v170
	v_rcp_f32_e32 v171, v171
	s_nop 0
	v_cvt_pk_bf16_f32 v168, v168, v169
	v_cvt_pk_bf16_f32 v169, v170, v171
	ds_write_b64 v108, v[168:169] offset:0
	v_mul_f32_e32 v176, 0xbfb8aa3b, v30
	v_mul_f32_e32 v177, 0xbfb8aa3b, v31
	v_mul_f32_e32 v178, 0xbfb8aa3b, v32
	v_mul_f32_e32 v179, 0xbfb8aa3b, v33
	v_exp_f32_e32 v176, v176
	v_exp_f32_e32 v177, v177
	v_exp_f32_e32 v178, v178
	v_exp_f32_e32 v179, v179
	v_add_f32_e32 v176, 1.0, v176
	v_add_f32_e32 v177, 1.0, v177
	v_add_f32_e32 v178, 1.0, v178
	v_add_f32_e32 v179, 1.0, v179
	v_rcp_f32_e32 v176, v176
	v_rcp_f32_e32 v177, v177
	v_rcp_f32_e32 v178, v178
	v_rcp_f32_e32 v179, v179
	s_nop 0
	v_cvt_pk_bf16_f32 v176, v176, v177
	v_cvt_pk_bf16_f32 v177, v178, v179
	ds_write_b64 v108, v[176:177] offset:12288
	s_waitcnt vmcnt(12)
	v_mfma_f32_16x16x32_bf16 v[26:29], v[54:57], v[2:5], 0
	v_mfma_f32_16x16x32_bf16 v[26:29], v[58:61], v[6:9], v[26:29]
	v_mfma_f32_16x16x32_bf16 v[30:33], v[54:57], v[10:13], 0
	v_mfma_f32_16x16x32_bf16 v[30:33], v[58:61], v[14:17], v[30:33]
	v_add_u32_e32 v108, 0x260, v154
	s_nop 7
	v_pk_add_f32 v[26:27], v[26:27], v[62:63]
	v_pk_add_f32 v[28:29], v[28:29], v[64:65]
	v_pk_add_f32 v[30:31], v[30:31], v[62:63]
	v_pk_add_f32 v[32:33], v[32:33], v[64:65]
	s_add_u32 s16, s0, 0x48000
	s_addc_u32 s17, s1, 0
	global_load_dwordx4 v[54:57], v153, s[16:17] offset:0
	global_load_dwordx4 v[58:61], v153, s[16:17] offset:64
	s_add_u32 s18, s70, 0x600
	s_addc_u32 s19, s71, 0
	global_load_dwordx4 v[62:65], v159, s[18:19]
	v_mul_f32_e32 v168, 0xbfb8aa3b, v26
	v_mul_f32_e32 v169, 0xbfb8aa3b, v27
	v_mul_f32_e32 v170, 0xbfb8aa3b, v28
	v_mul_f32_e32 v171, 0xbfb8aa3b, v29
	v_exp_f32_e32 v168, v168
	v_exp_f32_e32 v169, v169
	v_exp_f32_e32 v170, v170
	v_exp_f32_e32 v171, v171
	v_add_f32_e32 v168, 1.0, v168
	v_add_f32_e32 v169, 1.0, v169
	v_add_f32_e32 v170, 1.0, v170
	v_add_f32_e32 v171, 1.0, v171
	v_rcp_f32_e32 v168, v168
	v_rcp_f32_e32 v169, v169
	v_rcp_f32_e32 v170, v170
	v_rcp_f32_e32 v171, v171
	s_nop 0
	v_cvt_pk_bf16_f32 v168, v168, v169
	v_cvt_pk_bf16_f32 v169, v170, v171
	ds_write_b64 v108, v[168:169] offset:0
	v_mul_f32_e32 v176, 0xbfb8aa3b, v30
	v_mul_f32_e32 v177, 0xbfb8aa3b, v31
	v_mul_f32_e32 v178, 0xbfb8aa3b, v32
	v_mul_f32_e32 v179, 0xbfb8aa3b, v33
	v_exp_f32_e32 v176, v176
	v_exp_f32_e32 v177, v177
	v_exp_f32_e32 v178, v178
	v_exp_f32_e32 v179, v179
	v_add_f32_e32 v176, 1.0, v176
	v_add_f32_e32 v177, 1.0, v177
	v_add_f32_e32 v178, 1.0, v178
	v_add_f32_e32 v179, 1.0, v179
	v_rcp_f32_e32 v176, v176
	v_rcp_f32_e32 v177, v177
	v_rcp_f32_e32 v178, v178
	v_rcp_f32_e32 v179, v179
	s_nop 0
	v_cvt_pk_bf16_f32 v176, v176, v177
	v_cvt_pk_bf16_f32 v177, v178, v179
	ds_write_b64 v108, v[176:177] offset:12288
	s_waitcnt vmcnt(12)
	v_mfma_f32_16x16x32_bf16 v[26:29], v[66:69], v[2:5], 0
	v_mfma_f32_16x16x32_bf16 v[26:29], v[70:73], v[6:9], v[26:29]
	v_mfma_f32_16x16x32_bf16 v[30:33], v[66:69], v[10:13], 0
	v_mfma_f32_16x16x32_bf16 v[30:33], v[70:73], v[14:17], v[30:33]
	v_add_u32_e32 v108, 0x280, v154
	s_nop 7
	v_pk_add_f32 v[26:27], v[26:27], v[74:75]
	v_pk_add_f32 v[28:29], v[28:29], v[76:77]
	v_pk_add_f32 v[30:31], v[30:31], v[74:75]
	v_pk_add_f32 v[32:33], v[32:33], v[76:77]
	s_add_u32 s16, s0, 0x49000
	s_addc_u32 s17, s1, 0
	global_load_dwordx4 v[66:69], v153, s[16:17] offset:0
	global_load_dwordx4 v[70:73], v153, s[16:17] offset:64
	s_add_u32 s18, s70, 0x640
	s_addc_u32 s19, s71, 0
	global_load_dwordx4 v[74:77], v159, s[18:19]
	v_mul_f32_e32 v168, 0xbfb8aa3b, v26
	v_mul_f32_e32 v169, 0xbfb8aa3b, v27
	v_mul_f32_e32 v170, 0xbfb8aa3b, v28
	v_mul_f32_e32 v171, 0xbfb8aa3b, v29
	v_exp_f32_e32 v168, v168
	v_exp_f32_e32 v169, v169
	v_exp_f32_e32 v170, v170
	v_exp_f32_e32 v171, v171
	v_add_f32_e32 v168, 1.0, v168
	v_add_f32_e32 v169, 1.0, v169
	v_add_f32_e32 v170, 1.0, v170
	v_add_f32_e32 v171, 1.0, v171
	v_rcp_f32_e32 v168, v168
	v_rcp_f32_e32 v169, v169
	v_rcp_f32_e32 v170, v170
	v_rcp_f32_e32 v171, v171
	s_nop 0
	v_cvt_pk_bf16_f32 v168, v168, v169
	v_cvt_pk_bf16_f32 v169, v170, v171
	ds_write_b64 v108, v[168:169] offset:0
	v_mul_f32_e32 v176, 0xbfb8aa3b, v30
	v_mul_f32_e32 v177, 0xbfb8aa3b, v31
	v_mul_f32_e32 v178, 0xbfb8aa3b, v32
	v_mul_f32_e32 v179, 0xbfb8aa3b, v33
	v_exp_f32_e32 v176, v176
	v_exp_f32_e32 v177, v177
	v_exp_f32_e32 v178, v178
	v_exp_f32_e32 v179, v179
	v_add_f32_e32 v176, 1.0, v176
	v_add_f32_e32 v177, 1.0, v177
	v_add_f32_e32 v178, 1.0, v178
	v_add_f32_e32 v179, 1.0, v179
	v_rcp_f32_e32 v176, v176
	v_rcp_f32_e32 v177, v177
	v_rcp_f32_e32 v178, v178
	v_rcp_f32_e32 v179, v179
	s_nop 0
	v_cvt_pk_bf16_f32 v176, v176, v177
	v_cvt_pk_bf16_f32 v177, v178, v179
	ds_write_b64 v108, v[176:177] offset:12288
	s_waitcnt vmcnt(12)
	v_mfma_f32_16x16x32_bf16 v[26:29], v[78:81], v[2:5], 0
	v_mfma_f32_16x16x32_bf16 v[26:29], v[82:85], v[6:9], v[26:29]
	v_mfma_f32_16x16x32_bf16 v[30:33], v[78:81], v[10:13], 0
	v_mfma_f32_16x16x32_bf16 v[30:33], v[82:85], v[14:17], v[30:33]
	v_add_u32_e32 v108, 0x2a0, v154
	s_nop 7
	v_pk_add_f32 v[26:27], v[26:27], v[86:87]
	v_pk_add_f32 v[28:29], v[28:29], v[88:89]
	v_pk_add_f32 v[30:31], v[30:31], v[86:87]
	v_pk_add_f32 v[32:33], v[32:33], v[88:89]
	s_add_u32 s16, s0, 0x4a000
	s_addc_u32 s17, s1, 0
	global_load_dwordx4 v[78:81], v153, s[16:17] offset:0
	global_load_dwordx4 v[82:85], v153, s[16:17] offset:64
	s_add_u32 s18, s70, 0x680
	s_addc_u32 s19, s71, 0
	global_load_dwordx4 v[86:89], v159, s[18:19]
	v_mul_f32_e32 v168, 0xbfb8aa3b, v26
	v_mul_f32_e32 v169, 0xbfb8aa3b, v27
	v_mul_f32_e32 v170, 0xbfb8aa3b, v28
	v_mul_f32_e32 v171, 0xbfb8aa3b, v29
	v_exp_f32_e32 v168, v168
	v_exp_f32_e32 v169, v169
	v_exp_f32_e32 v170, v170
	v_exp_f32_e32 v171, v171
	v_add_f32_e32 v168, 1.0, v168
	v_add_f32_e32 v169, 1.0, v169
	v_add_f32_e32 v170, 1.0, v170
	v_add_f32_e32 v171, 1.0, v171
	v_rcp_f32_e32 v168, v168
	v_rcp_f32_e32 v169, v169
	v_rcp_f32_e32 v170, v170
	v_rcp_f32_e32 v171, v171
	s_nop 0
	v_cvt_pk_bf16_f32 v168, v168, v169
	v_cvt_pk_bf16_f32 v169, v170, v171
	ds_write_b64 v108, v[168:169] offset:0
	v_mul_f32_e32 v176, 0xbfb8aa3b, v30
	v_mul_f32_e32 v177, 0xbfb8aa3b, v31
	v_mul_f32_e32 v178, 0xbfb8aa3b, v32
	v_mul_f32_e32 v179, 0xbfb8aa3b, v33
	v_exp_f32_e32 v176, v176
	v_exp_f32_e32 v177, v177
	v_exp_f32_e32 v178, v178
	v_exp_f32_e32 v179, v179
	v_add_f32_e32 v176, 1.0, v176
	v_add_f32_e32 v177, 1.0, v177
	v_add_f32_e32 v178, 1.0, v178
	v_add_f32_e32 v179, 1.0, v179
	v_rcp_f32_e32 v176, v176
	v_rcp_f32_e32 v177, v177
	v_rcp_f32_e32 v178, v178
	v_rcp_f32_e32 v179, v179
	s_nop 0
	v_cvt_pk_bf16_f32 v176, v176, v177
	v_cvt_pk_bf16_f32 v177, v178, v179
	ds_write_b64 v108, v[176:177] offset:12288
	s_waitcnt vmcnt(12)
	v_mfma_f32_16x16x32_bf16 v[26:29], v[18:21], v[2:5], 0
	v_mfma_f32_16x16x32_bf16 v[26:29], v[22:25], v[6:9], v[26:29]
	v_mfma_f32_16x16x32_bf16 v[30:33], v[18:21], v[10:13], 0
	v_mfma_f32_16x16x32_bf16 v[30:33], v[22:25], v[14:17], v[30:33]
	v_add_u32_e32 v108, 0x2c0, v154
	s_nop 7
	v_pk_add_f32 v[26:27], v[26:27], v[38:39]
	v_pk_add_f32 v[28:29], v[28:29], v[40:41]
	v_pk_add_f32 v[30:31], v[30:31], v[38:39]
	v_pk_add_f32 v[32:33], v[32:33], v[40:41]
	v_mul_f32_e32 v168, 0xbfb8aa3b, v26
	v_mul_f32_e32 v169, 0xbfb8aa3b, v27
	v_mul_f32_e32 v170, 0xbfb8aa3b, v28
	v_mul_f32_e32 v171, 0xbfb8aa3b, v29
	v_exp_f32_e32 v168, v168
	v_exp_f32_e32 v169, v169
	v_exp_f32_e32 v170, v170
	v_exp_f32_e32 v171, v171
	v_add_f32_e32 v168, 1.0, v168
	v_add_f32_e32 v169, 1.0, v169
	v_add_f32_e32 v170, 1.0, v170
	v_add_f32_e32 v171, 1.0, v171
	v_rcp_f32_e32 v168, v168
	v_rcp_f32_e32 v169, v169
	v_rcp_f32_e32 v170, v170
	v_rcp_f32_e32 v171, v171
	s_nop 0
	v_cvt_pk_bf16_f32 v168, v168, v169
	v_cvt_pk_bf16_f32 v169, v170, v171
	ds_write_b64 v108, v[168:169] offset:0
	v_mul_f32_e32 v176, 0xbfb8aa3b, v30
	v_mul_f32_e32 v177, 0xbfb8aa3b, v31
	v_mul_f32_e32 v178, 0xbfb8aa3b, v32
	v_mul_f32_e32 v179, 0xbfb8aa3b, v33
	v_exp_f32_e32 v176, v176
	v_exp_f32_e32 v177, v177
	v_exp_f32_e32 v178, v178
	v_exp_f32_e32 v179, v179
	v_add_f32_e32 v176, 1.0, v176
	v_add_f32_e32 v177, 1.0, v177
	v_add_f32_e32 v178, 1.0, v178
	v_add_f32_e32 v179, 1.0, v179
	v_rcp_f32_e32 v176, v176
	v_rcp_f32_e32 v177, v177
	v_rcp_f32_e32 v178, v178
	v_rcp_f32_e32 v179, v179
	s_nop 0
	v_cvt_pk_bf16_f32 v176, v176, v177
	v_cvt_pk_bf16_f32 v177, v178, v179
	ds_write_b64 v108, v[176:177] offset:12288
	s_waitcnt vmcnt(9)
	v_mfma_f32_16x16x32_bf16 v[26:29], v[42:45], v[2:5], 0
	v_mfma_f32_16x16x32_bf16 v[26:29], v[46:49], v[6:9], v[26:29]
	v_mfma_f32_16x16x32_bf16 v[30:33], v[42:45], v[10:13], 0
	v_mfma_f32_16x16x32_bf16 v[30:33], v[46:49], v[14:17], v[30:33]
	v_add_u32_e32 v108, 0x2e0, v154
	s_nop 7
	v_pk_add_f32 v[26:27], v[26:27], v[50:51]
	v_pk_add_f32 v[28:29], v[28:29], v[52:53]
	v_pk_add_f32 v[30:31], v[30:31], v[50:51]
	v_pk_add_f32 v[32:33], v[32:33], v[52:53]
	v_mul_f32_e32 v168, 0xbfb8aa3b, v26
	v_mul_f32_e32 v169, 0xbfb8aa3b, v27
	v_mul_f32_e32 v170, 0xbfb8aa3b, v28
	v_mul_f32_e32 v171, 0xbfb8aa3b, v29
	v_exp_f32_e32 v168, v168
	v_exp_f32_e32 v169, v169
	v_exp_f32_e32 v170, v170
	v_exp_f32_e32 v171, v171
	v_add_f32_e32 v168, 1.0, v168
	v_add_f32_e32 v169, 1.0, v169
	v_add_f32_e32 v170, 1.0, v170
	v_add_f32_e32 v171, 1.0, v171
	v_rcp_f32_e32 v168, v168
	v_rcp_f32_e32 v169, v169
	v_rcp_f32_e32 v170, v170
	v_rcp_f32_e32 v171, v171
	s_nop 0
	v_cvt_pk_bf16_f32 v168, v168, v169
	v_cvt_pk_bf16_f32 v169, v170, v171
	ds_write_b64 v108, v[168:169] offset:0
	v_mul_f32_e32 v176, 0xbfb8aa3b, v30
	v_mul_f32_e32 v177, 0xbfb8aa3b, v31
	v_mul_f32_e32 v178, 0xbfb8aa3b, v32
	v_mul_f32_e32 v179, 0xbfb8aa3b, v33
	v_exp_f32_e32 v176, v176
	v_exp_f32_e32 v177, v177
	v_exp_f32_e32 v178, v178
	v_exp_f32_e32 v179, v179
	v_add_f32_e32 v176, 1.0, v176
	v_add_f32_e32 v177, 1.0, v177
	v_add_f32_e32 v178, 1.0, v178
	v_add_f32_e32 v179, 1.0, v179
	v_rcp_f32_e32 v176, v176
	v_rcp_f32_e32 v177, v177
	v_rcp_f32_e32 v178, v178
	v_rcp_f32_e32 v179, v179
	s_nop 0
	v_cvt_pk_bf16_f32 v176, v176, v177
	v_cvt_pk_bf16_f32 v177, v178, v179
	ds_write_b64 v108, v[176:177] offset:12288
	s_waitcnt vmcnt(6)
	v_mfma_f32_16x16x32_bf16 v[26:29], v[54:57], v[2:5], 0
	v_mfma_f32_16x16x32_bf16 v[26:29], v[58:61], v[6:9], v[26:29]
	v_mfma_f32_16x16x32_bf16 v[30:33], v[54:57], v[10:13], 0
	v_mfma_f32_16x16x32_bf16 v[30:33], v[58:61], v[14:17], v[30:33]
	v_add_u32_e32 v108, 0x6000, v154
	s_nop 7
	v_pk_add_f32 v[26:27], v[26:27], v[62:63]
	v_pk_add_f32 v[28:29], v[28:29], v[64:65]
	v_pk_add_f32 v[30:31], v[30:31], v[62:63]
	v_pk_add_f32 v[32:33], v[32:33], v[64:65]
	v_mul_f32_e32 v168, 0xbfb8aa3b, v26
	v_mul_f32_e32 v169, 0xbfb8aa3b, v27
	v_mul_f32_e32 v170, 0xbfb8aa3b, v28
	v_mul_f32_e32 v171, 0xbfb8aa3b, v29
	v_exp_f32_e32 v168, v168
	v_exp_f32_e32 v169, v169
	v_exp_f32_e32 v170, v170
	v_exp_f32_e32 v171, v171
	v_add_f32_e32 v168, 1.0, v168
	v_add_f32_e32 v169, 1.0, v169
	v_add_f32_e32 v170, 1.0, v170
	v_add_f32_e32 v171, 1.0, v171
	v_rcp_f32_e32 v168, v168
	v_rcp_f32_e32 v169, v169
	v_rcp_f32_e32 v170, v170
	v_rcp_f32_e32 v171, v171
	s_nop 0
	v_cvt_pk_bf16_f32 v168, v168, v169
	v_cvt_pk_bf16_f32 v169, v170, v171
	ds_write_b64 v108, v[168:169] offset:0
	v_mul_f32_e32 v176, 0xbfb8aa3b, v30
	v_mul_f32_e32 v177, 0xbfb8aa3b, v31
	v_mul_f32_e32 v178, 0xbfb8aa3b, v32
	v_mul_f32_e32 v179, 0xbfb8aa3b, v33
	v_exp_f32_e32 v176, v176
	v_exp_f32_e32 v177, v177
	v_exp_f32_e32 v178, v178
	v_exp_f32_e32 v179, v179
	v_add_f32_e32 v176, 1.0, v176
	v_add_f32_e32 v177, 1.0, v177
	v_add_f32_e32 v178, 1.0, v178
	v_add_f32_e32 v179, 1.0, v179
	v_rcp_f32_e32 v176, v176
	v_rcp_f32_e32 v177, v177
	v_rcp_f32_e32 v178, v178
	v_rcp_f32_e32 v179, v179
	s_nop 0
	v_cvt_pk_bf16_f32 v176, v176, v177
	v_cvt_pk_bf16_f32 v177, v178, v179
	ds_write_b64 v108, v[176:177] offset:12288
	s_waitcnt vmcnt(3)
	v_mfma_f32_16x16x32_bf16 v[26:29], v[66:69], v[2:5], 0
	v_mfma_f32_16x16x32_bf16 v[26:29], v[70:73], v[6:9], v[26:29]
	v_mfma_f32_16x16x32_bf16 v[30:33], v[66:69], v[10:13], 0
	v_mfma_f32_16x16x32_bf16 v[30:33], v[70:73], v[14:17], v[30:33]
	v_add_u32_e32 v108, 0x6020, v154
	s_nop 7
	v_pk_add_f32 v[26:27], v[26:27], v[74:75]
	v_pk_add_f32 v[28:29], v[28:29], v[76:77]
	v_pk_add_f32 v[30:31], v[30:31], v[74:75]
	v_pk_add_f32 v[32:33], v[32:33], v[76:77]
	v_mul_f32_e32 v168, 0xbfb8aa3b, v26
	v_mul_f32_e32 v169, 0xbfb8aa3b, v27
	v_mul_f32_e32 v170, 0xbfb8aa3b, v28
	v_mul_f32_e32 v171, 0xbfb8aa3b, v29
	v_exp_f32_e32 v168, v168
	v_exp_f32_e32 v169, v169
	v_exp_f32_e32 v170, v170
	v_exp_f32_e32 v171, v171
	v_add_f32_e32 v168, 1.0, v168
	v_add_f32_e32 v169, 1.0, v169
	v_add_f32_e32 v170, 1.0, v170
	v_add_f32_e32 v171, 1.0, v171
	v_rcp_f32_e32 v168, v168
	v_rcp_f32_e32 v169, v169
	v_rcp_f32_e32 v170, v170
	v_rcp_f32_e32 v171, v171
	s_nop 0
	v_cvt_pk_bf16_f32 v168, v168, v169
	v_cvt_pk_bf16_f32 v169, v170, v171
	ds_write_b64 v108, v[168:169] offset:0
	v_mul_f32_e32 v176, 0xbfb8aa3b, v30
	v_mul_f32_e32 v177, 0xbfb8aa3b, v31
	v_mul_f32_e32 v178, 0xbfb8aa3b, v32
	v_mul_f32_e32 v179, 0xbfb8aa3b, v33
	v_exp_f32_e32 v176, v176
	v_exp_f32_e32 v177, v177
	v_exp_f32_e32 v178, v178
	v_exp_f32_e32 v179, v179
	v_add_f32_e32 v176, 1.0, v176
	v_add_f32_e32 v177, 1.0, v177
	v_add_f32_e32 v178, 1.0, v178
	v_add_f32_e32 v179, 1.0, v179
	v_rcp_f32_e32 v176, v176
	v_rcp_f32_e32 v177, v177
	v_rcp_f32_e32 v178, v178
	v_rcp_f32_e32 v179, v179
	s_nop 0
	v_cvt_pk_bf16_f32 v176, v176, v177
	v_cvt_pk_bf16_f32 v177, v178, v179
	ds_write_b64 v108, v[176:177] offset:12288
	s_waitcnt vmcnt(0)
	v_mfma_f32_16x16x32_bf16 v[26:29], v[78:81], v[2:5], 0
	v_mfma_f32_16x16x32_bf16 v[26:29], v[82:85], v[6:9], v[26:29]
	v_mfma_f32_16x16x32_bf16 v[30:33], v[78:81], v[10:13], 0
	v_mfma_f32_16x16x32_bf16 v[30:33], v[82:85], v[14:17], v[30:33]
	v_add_u32_e32 v108, 0x6040, v154
	s_nop 7
	v_pk_add_f32 v[26:27], v[26:27], v[86:87]
	v_pk_add_f32 v[28:29], v[28:29], v[88:89]
	v_pk_add_f32 v[30:31], v[30:31], v[86:87]
	v_pk_add_f32 v[32:33], v[32:33], v[88:89]
	v_mul_f32_e32 v168, 0xbfb8aa3b, v26
	v_mul_f32_e32 v169, 0xbfb8aa3b, v27
	v_mul_f32_e32 v170, 0xbfb8aa3b, v28
	v_mul_f32_e32 v171, 0xbfb8aa3b, v29
	v_exp_f32_e32 v168, v168
	v_exp_f32_e32 v169, v169
	v_exp_f32_e32 v170, v170
	v_exp_f32_e32 v171, v171
	v_add_f32_e32 v168, 1.0, v168
	v_add_f32_e32 v169, 1.0, v169
	v_add_f32_e32 v170, 1.0, v170
	v_add_f32_e32 v171, 1.0, v171
	v_rcp_f32_e32 v168, v168
	v_rcp_f32_e32 v169, v169
	v_rcp_f32_e32 v170, v170
	v_rcp_f32_e32 v171, v171
	s_nop 0
	v_cvt_pk_bf16_f32 v168, v168, v169
	v_cvt_pk_bf16_f32 v169, v170, v171
	ds_write_b64 v108, v[168:169] offset:0
	v_mul_f32_e32 v176, 0xbfb8aa3b, v30
	v_mul_f32_e32 v177, 0xbfb8aa3b, v31
	v_mul_f32_e32 v178, 0xbfb8aa3b, v32
	v_mul_f32_e32 v179, 0xbfb8aa3b, v33
	v_exp_f32_e32 v176, v176
	v_exp_f32_e32 v177, v177
	v_exp_f32_e32 v178, v178
	v_exp_f32_e32 v179, v179
	v_add_f32_e32 v176, 1.0, v176
	v_add_f32_e32 v177, 1.0, v177
	v_add_f32_e32 v178, 1.0, v178
	v_add_f32_e32 v179, 1.0, v179
	v_rcp_f32_e32 v176, v176
	v_rcp_f32_e32 v177, v177
	v_rcp_f32_e32 v178, v178
	v_rcp_f32_e32 v179, v179
	s_nop 0
	v_cvt_pk_bf16_f32 v176, v176, v177
	v_cvt_pk_bf16_f32 v177, v178, v179
	ds_write_b64 v108, v[176:177] offset:12288
	s_branch .LBB0_402
.Lb3w_5:
	ds_read_b128 v[2:5], v0 offset:128
	ds_read_b128 v[6:9], v0 offset:192
	ds_read_b128 v[10:13], v0 offset:8576
	ds_read_b128 v[14:17], v0 offset:8640
	s_add_u32 s16, s0, 0x4b000
	s_addc_u32 s17, s1, 0
	global_load_dwordx4 v[18:21], v153, s[16:17] offset:0
	global_load_dwordx4 v[22:25], v153, s[16:17] offset:64
	s_add_u32 s18, s70, 0x6c0
	s_addc_u32 s19, s71, 0
	global_load_dwordx4 v[38:41], v159, s[18:19]
	s_add_u32 s16, s0, 0x4c000
	s_addc_u32 s17, s1, 0
	global_load_dwordx4 v[42:45], v153, s[16:17] offset:0
	global_load_dwordx4 v[46:49], v153, s[16:17] offset:64
	s_add_u32 s18, s70, 0x700
	s_addc_u32 s19, s71, 0
	global_load_dwordx4 v[50:53], v159, s[18:19]
	s_add_u32 s16, s0, 0x4d000
	s_addc_u32 s17, s1, 0
	global_load_dwordx4 v[54:57], v153, s[16:17] offset:0
	global_load_dwordx4 v[58:61], v153, s[16:17] offset:64
	s_add_u32 s18, s70, 0x740
	s_addc_u32 s19, s71, 0
	global_load_dwordx4 v[62:65], v159, s[18:19]
	s_add_u32 s16, s0, 0x4e000
	s_addc_u32 s17, s1, 0
	global_load_dwordx4 v[66:69], v153, s[16:17] offset:0
	global_load_dwordx4 v[70:73], v153, s[16:17] offset:64
	s_add_u32 s18, s70, 0x780
	s_addc_u32 s19, s71, 0
	global_load_dwordx4 v[74:77], v159, s[18:19]
	s_add_u32 s16, s0, 0x4f000
	s_addc_u32 s17, s1, 0
	global_load_dwordx4 v[78:81], v153, s[16:17] offset:0
	global_load_dwordx4 v[82:85], v153, s[16:17] offset:64
	s_add_u32 s18, s70, 0x7c0
	s_addc_u32 s19, s71, 0
	global_load_dwordx4 v[86:89], v159, s[18:19]
	s_waitcnt vmcnt(12) lgkmcnt(0)
	v_mfma_f32_16x16x32_bf16 v[26:29], v[18:21], v[2:5], 0
	v_mfma_f32_16x16x32_bf16 v[26:29], v[22:25], v[6:9], v[26:29]
	v_mfma_f32_16x16x32_bf16 v[30:33], v[18:21], v[10:13], 0
	v_mfma_f32_16x16x32_bf16 v[30:33], v[22:25], v[14:17], v[30:33]
	v_add_u32_e32 v108, 0x6060, v154
	s_nop 7
	v_pk_add_f32 v[26:27], v[26:27], v[38:39]
	v_pk_add_f32 v[28:29], v[28:29], v[40:41]
	v_pk_add_f32 v[30:31], v[30:31], v[38:39]
	v_pk_add_f32 v[32:33], v[32:33], v[40:41]
	s_add_u32 s16, s0, 0x50000
	s_addc_u32 s17, s1, 0
	global_load_dwordx4 v[18:21], v153, s[16:17] offset:0
	global_load_dwordx4 v[22:25], v153, s[16:17] offset:64
	s_add_u32 s18, s70, 0x800
	s_addc_u32 s19, s71, 0
	global_load_dwordx4 v[38:41], v159, s[18:19]
	v_mul_f32_e32 v168, 0xbfb8aa3b, v26
	v_mul_f32_e32 v169, 0xbfb8aa3b, v27
	v_mul_f32_e32 v170, 0xbfb8aa3b, v28
	v_mul_f32_e32 v171, 0xbfb8aa3b, v29
	v_exp_f32_e32 v168, v168
	v_exp_f32_e32 v169, v169
	v_exp_f32_e32 v170, v170
	v_exp_f32_e32 v171, v171
	v_add_f32_e32 v168, 1.0, v168
	v_add_f32_e32 v169, 1.0, v169
	v_add_f32_e32 v170, 1.0, v170
	v_add_f32_e32 v171, 1.0, v171
	v_rcp_f32_e32 v168, v168
	v_rcp_f32_e32 v169, v169
	v_rcp_f32_e32 v170, v170
	v_rcp_f32_e32 v171, v171
	s_nop 0
	v_cvt_pk_bf16_f32 v168, v168, v169
	v_cvt_pk_bf16_f32 v169, v170, v171
	ds_write_b64 v108, v[168:169] offset:0
	v_mul_f32_e32 v176, 0xbfb8aa3b, v30
	v_mul_f32_e32 v177, 0xbfb8aa3b, v31
	v_mul_f32_e32 v178, 0xbfb8aa3b, v32
	v_mul_f32_e32 v179, 0xbfb8aa3b, v33
	v_exp_f32_e32 v176, v176
	v_exp_f32_e32 v177, v177
	v_exp_f32_e32 v178, v178
	v_exp_f32_e32 v179, v179
	v_add_f32_e32 v176, 1.0, v176
	v_add_f32_e32 v177, 1.0, v177
	v_add_f32_e32 v178, 1.0, v178
	v_add_f32_e32 v179, 1.0, v179
	v_rcp_f32_e32 v176, v176
	v_rcp_f32_e32 v177, v177
	v_rcp_f32_e32 v178, v178
	v_rcp_f32_e32 v179, v179
	s_nop 0
	v_cvt_pk_bf16_f32 v176, v176, v177
	v_cvt_pk_bf16_f32 v177, v178, v179
	ds_write_b64 v108, v[176:177] offset:12288
	s_waitcnt vmcnt(12)
	v_mfma_f32_16x16x32_bf16 v[26:29], v[42:45], v[2:5], 0
	v_mfma_f32_16x16x32_bf16 v[26:29], v[46:49], v[6:9], v[26:29]
	v_mfma_f32_16x16x32_bf16 v[30:33], v[42:45], v[10:13], 0
	v_mfma_f32_16x16x32_bf16 v[30:33], v[46:49], v[14:17], v[30:33]
	v_add_u32_e32 v108, 0x6080, v154
	s_nop 7
	v_pk_add_f32 v[26:27], v[26:27], v[50:51]
	v_pk_add_f32 v[28:29], v[28:29], v[52:53]
	v_pk_add_f32 v[30:31], v[30:31], v[50:51]
	v_pk_add_f32 v[32:33], v[32:33], v[52:53]
	s_add_u32 s16, s0, 0x51000
	s_addc_u32 s17, s1, 0
	global_load_dwordx4 v[42:45], v153, s[16:17] offset:0
	global_load_dwordx4 v[46:49], v153, s[16:17] offset:64
	s_add_u32 s18, s70, 0x840
	s_addc_u32 s19, s71, 0
	global_load_dwordx4 v[50:53], v159, s[18:19]
	v_mul_f32_e32 v168, 0xbfb8aa3b, v26
	v_mul_f32_e32 v169, 0xbfb8aa3b, v27
	v_mul_f32_e32 v170, 0xbfb8aa3b, v28
	v_mul_f32_e32 v171, 0xbfb8aa3b, v29
	v_exp_f32_e32 v168, v168
	v_exp_f32_e32 v169, v169
	v_exp_f32_e32 v170, v170
	v_exp_f32_e32 v171, v171
	v_add_f32_e32 v168, 1.0, v168
	v_add_f32_e32 v169, 1.0, v169
	v_add_f32_e32 v170, 1.0, v170
	v_add_f32_e32 v171, 1.0, v171
	v_rcp_f32_e32 v168, v168
	v_rcp_f32_e32 v169, v169
	v_rcp_f32_e32 v170, v170
	v_rcp_f32_e32 v171, v171
	s_nop 0
	v_cvt_pk_bf16_f32 v168, v168, v169
	v_cvt_pk_bf16_f32 v169, v170, v171
	ds_write_b64 v108, v[168:169] offset:0
	v_mul_f32_e32 v176, 0xbfb8aa3b, v30
	v_mul_f32_e32 v177, 0xbfb8aa3b, v31
	v_mul_f32_e32 v178, 0xbfb8aa3b, v32
	v_mul_f32_e32 v179, 0xbfb8aa3b, v33
	v_exp_f32_e32 v176, v176
	v_exp_f32_e32 v177, v177
	v_exp_f32_e32 v178, v178
	v_exp_f32_e32 v179, v179
	v_add_f32_e32 v176, 1.0, v176
	v_add_f32_e32 v177, 1.0, v177
	v_add_f32_e32 v178, 1.0, v178
	v_add_f32_e32 v179, 1.0, v179
	v_rcp_f32_e32 v176, v176
	v_rcp_f32_e32 v177, v177
	v_rcp_f32_e32 v178, v178
	v_rcp_f32_e32 v179, v179
	s_nop 0
	v_cvt_pk_bf16_f32 v176, v176, v177
	v_cvt_pk_bf16_f32 v177, v178, v179
	ds_write_b64 v108, v[176:177] offset:12288
	s_waitcnt vmcnt(12)
	v_mfma_f32_16x16x32_bf16 v[26:29], v[54:57], v[2:5], 0
	v_mfma_f32_16x16x32_bf16 v[26:29], v[58:61], v[6:9], v[26:29]
	v_mfma_f32_16x16x32_bf16 v[30:33], v[54:57], v[10:13], 0
	v_mfma_f32_16x16x32_bf16 v[30:33], v[58:61], v[14:17], v[30:33]
	v_add_u32_e32 v108, 0x60a0, v154
	s_nop 7
	v_pk_add_f32 v[26:27], v[26:27], v[62:63]
	v_pk_add_f32 v[28:29], v[28:29], v[64:65]
	v_pk_add_f32 v[30:31], v[30:31], v[62:63]
	v_pk_add_f32 v[32:33], v[32:33], v[64:65]
	s_add_u32 s16, s0, 0x52000
	s_addc_u32 s17, s1, 0
	global_load_dwordx4 v[54:57], v153, s[16:17] offset:0
	global_load_dwordx4 v[58:61], v153, s[16:17] offset:64
	s_add_u32 s18, s70, 0x880
	s_addc_u32 s19, s71, 0
	global_load_dwordx4 v[62:65], v159, s[18:19]
	v_mul_f32_e32 v168, 0xbfb8aa3b, v26
	v_mul_f32_e32 v169, 0xbfb8aa3b, v27
	v_mul_f32_e32 v170, 0xbfb8aa3b, v28
	v_mul_f32_e32 v171, 0xbfb8aa3b, v29
	v_exp_f32_e32 v168, v168
	v_exp_f32_e32 v169, v169
	v_exp_f32_e32 v170, v170
	v_exp_f32_e32 v171, v171
	v_add_f32_e32 v168, 1.0, v168
	v_add_f32_e32 v169, 1.0, v169
	v_add_f32_e32 v170, 1.0, v170
	v_add_f32_e32 v171, 1.0, v171
	v_rcp_f32_e32 v168, v168
	v_rcp_f32_e32 v169, v169
	v_rcp_f32_e32 v170, v170
	v_rcp_f32_e32 v171, v171
	s_nop 0
	v_cvt_pk_bf16_f32 v168, v168, v169
	v_cvt_pk_bf16_f32 v169, v170, v171
	ds_write_b64 v108, v[168:169] offset:0
	v_mul_f32_e32 v176, 0xbfb8aa3b, v30
	v_mul_f32_e32 v177, 0xbfb8aa3b, v31
	v_mul_f32_e32 v178, 0xbfb8aa3b, v32
	v_mul_f32_e32 v179, 0xbfb8aa3b, v33
	v_exp_f32_e32 v176, v176
	v_exp_f32_e32 v177, v177
	v_exp_f32_e32 v178, v178
	v_exp_f32_e32 v179, v179
	v_add_f32_e32 v176, 1.0, v176
	v_add_f32_e32 v177, 1.0, v177
	v_add_f32_e32 v178, 1.0, v178
	v_add_f32_e32 v179, 1.0, v179
	v_rcp_f32_e32 v176, v176
	v_rcp_f32_e32 v177, v177
	v_rcp_f32_e32 v178, v178
	v_rcp_f32_e32 v179, v179
	s_nop 0
	v_cvt_pk_bf16_f32 v176, v176, v177
	v_cvt_pk_bf16_f32 v177, v178, v179
	ds_write_b64 v108, v[176:177] offset:12288
	s_waitcnt vmcnt(12)
	v_mfma_f32_16x16x32_bf16 v[26:29], v[66:69], v[2:5], 0
	v_mfma_f32_16x16x32_bf16 v[26:29], v[70:73], v[6:9], v[26:29]
	v_mfma_f32_16x16x32_bf16 v[30:33], v[66:69], v[10:13], 0
	v_mfma_f32_16x16x32_bf16 v[30:33], v[70:73], v[14:17], v[30:33]
	v_add_u32_e32 v108, 0x60c0, v154
	s_nop 7
	v_pk_add_f32 v[26:27], v[26:27], v[74:75]
	v_pk_add_f32 v[28:29], v[28:29], v[76:77]
	v_pk_add_f32 v[30:31], v[30:31], v[74:75]
	v_pk_add_f32 v[32:33], v[32:33], v[76:77]
	s_add_u32 s16, s0, 0x53000
	s_addc_u32 s17, s1, 0
	global_load_dwordx4 v[66:69], v153, s[16:17] offset:0
	global_load_dwordx4 v[70:73], v153, s[16:17] offset:64
	s_add_u32 s18, s70, 0x8c0
	s_addc_u32 s19, s71, 0
	global_load_dwordx4 v[74:77], v159, s[18:19]
	v_mul_f32_e32 v168, 0xbfb8aa3b, v26
	v_mul_f32_e32 v169, 0xbfb8aa3b, v27
	v_mul_f32_e32 v170, 0xbfb8aa3b, v28
	v_mul_f32_e32 v171, 0xbfb8aa3b, v29
	v_exp_f32_e32 v168, v168
	v_exp_f32_e32 v169, v169
	v_exp_f32_e32 v170, v170
	v_exp_f32_e32 v171, v171
	v_add_f32_e32 v168, 1.0, v168
	v_add_f32_e32 v169, 1.0, v169
	v_add_f32_e32 v170, 1.0, v170
	v_add_f32_e32 v171, 1.0, v171
	v_rcp_f32_e32 v168, v168
	v_rcp_f32_e32 v169, v169
	v_rcp_f32_e32 v170, v170
	v_rcp_f32_e32 v171, v171
	s_nop 0
	v_cvt_pk_bf16_f32 v168, v168, v169
	v_cvt_pk_bf16_f32 v169, v170, v171
	ds_write_b64 v108, v[168:169] offset:0
	v_mul_f32_e32 v176, 0xbfb8aa3b, v30
	v_mul_f32_e32 v177, 0xbfb8aa3b, v31
	v_mul_f32_e32 v178, 0xbfb8aa3b, v32
	v_mul_f32_e32 v179, 0xbfb8aa3b, v33
	v_exp_f32_e32 v176, v176
	v_exp_f32_e32 v177, v177
	v_exp_f32_e32 v178, v178
	v_exp_f32_e32 v179, v179
	v_add_f32_e32 v176, 1.0, v176
	v_add_f32_e32 v177, 1.0, v177
	v_add_f32_e32 v178, 1.0, v178
	v_add_f32_e32 v179, 1.0, v179
	v_rcp_f32_e32 v176, v176
	v_rcp_f32_e32 v177, v177
	v_rcp_f32_e32 v178, v178
	v_rcp_f32_e32 v179, v179
	s_nop 0
	v_cvt_pk_bf16_f32 v176, v176, v177
	v_cvt_pk_bf16_f32 v177, v178, v179
	ds_write_b64 v108, v[176:177] offset:12288
	s_waitcnt vmcnt(12)
	v_mfma_f32_16x16x32_bf16 v[26:29], v[78:81], v[2:5], 0
	v_mfma_f32_16x16x32_bf16 v[26:29], v[82:85], v[6:9], v[26:29]
	v_mfma_f32_16x16x32_bf16 v[30:33], v[78:81], v[10:13], 0
	v_mfma_f32_16x16x32_bf16 v[30:33], v[82:85], v[14:17], v[30:33]
	v_add_u32_e32 v108, 0x60e0, v154
	s_nop 7
	v_pk_add_f32 v[26:27], v[26:27], v[86:87]
	v_pk_add_f32 v[28:29], v[28:29], v[88:89]
	v_pk_add_f32 v[30:31], v[30:31], v[86:87]
	v_pk_add_f32 v[32:33], v[32:33], v[88:89]
	s_add_u32 s16, s0, 0x54000
	s_addc_u32 s17, s1, 0
	global_load_dwordx4 v[78:81], v153, s[16:17] offset:0
	global_load_dwordx4 v[82:85], v153, s[16:17] offset:64
	s_add_u32 s18, s70, 0x900
	s_addc_u32 s19, s71, 0
	global_load_dwordx4 v[86:89], v159, s[18:19]
	v_mul_f32_e32 v168, 0xbfb8aa3b, v26
	v_mul_f32_e32 v169, 0xbfb8aa3b, v27
	v_mul_f32_e32 v170, 0xbfb8aa3b, v28
	v_mul_f32_e32 v171, 0xbfb8aa3b, v29
	v_exp_f32_e32 v168, v168
	v_exp_f32_e32 v169, v169
	v_exp_f32_e32 v170, v170
	v_exp_f32_e32 v171, v171
	v_add_f32_e32 v168, 1.0, v168
	v_add_f32_e32 v169, 1.0, v169
	v_add_f32_e32 v170, 1.0, v170
	v_add_f32_e32 v171, 1.0, v171
	v_rcp_f32_e32 v168, v168
	v_rcp_f32_e32 v169, v169
	v_rcp_f32_e32 v170, v170
	v_rcp_f32_e32 v171, v171
	s_nop 0
	v_cvt_pk_bf16_f32 v168, v168, v169
	v_cvt_pk_bf16_f32 v169, v170, v171
	ds_write_b64 v108, v[168:169] offset:0
	v_mul_f32_e32 v176, 0xbfb8aa3b, v30
	v_mul_f32_e32 v177, 0xbfb8aa3b, v31
	v_mul_f32_e32 v178, 0xbfb8aa3b, v32
	v_mul_f32_e32 v179, 0xbfb8aa3b, v33
	v_exp_f32_e32 v176, v176
	v_exp_f32_e32 v177, v177
	v_exp_f32_e32 v178, v178
	v_exp_f32_e32 v179, v179
	v_add_f32_e32 v176, 1.0, v176
	v_add_f32_e32 v177, 1.0, v177
	v_add_f32_e32 v178, 1.0, v178
	v_add_f32_e32 v179, 1.0, v179
	v_rcp_f32_e32 v176, v176
	v_rcp_f32_e32 v177, v177
	v_rcp_f32_e32 v178, v178
	v_rcp_f32_e32 v179, v179
	s_nop 0
	v_cvt_pk_bf16_f32 v176, v176, v177
	v_cvt_pk_bf16_f32 v177, v178, v179
	ds_write_b64 v108, v[176:177] offset:12288
	s_waitcnt vmcnt(12)
	v_mfma_f32_16x16x32_bf16 v[26:29], v[18:21], v[2:5], 0
	v_mfma_f32_16x16x32_bf16 v[26:29], v[22:25], v[6:9], v[26:29]
	v_mfma_f32_16x16x32_bf16 v[30:33], v[18:21], v[10:13], 0
	v_mfma_f32_16x16x32_bf16 v[30:33], v[22:25], v[14:17], v[30:33]
	v_add_u32_e32 v108, 0x6100, v154
	s_nop 7
	v_pk_add_f32 v[26:27], v[26:27], v[38:39]
	v_pk_add_f32 v[28:29], v[28:29], v[40:41]
	v_pk_add_f32 v[30:31], v[30:31], v[38:39]
	v_pk_add_f32 v[32:33], v[32:33], v[40:41]
	s_add_u32 s16, s0, 0x55000
	s_addc_u32 s17, s1, 0
	global_load_dwordx4 v[18:21], v153, s[16:17] offset:0
	global_load_dwordx4 v[22:25], v153, s[16:17] offset:64
	s_add_u32 s18, s70, 0x940
	s_addc_u32 s19, s71, 0
	global_load_dwordx4 v[38:41], v159, s[18:19]
	v_mul_f32_e32 v168, 0xbfb8aa3b, v26
	v_mul_f32_e32 v169, 0xbfb8aa3b, v27
	v_mul_f32_e32 v170, 0xbfb8aa3b, v28
	v_mul_f32_e32 v171, 0xbfb8aa3b, v29
	v_exp_f32_e32 v168, v168
	v_exp_f32_e32 v169, v169
	v_exp_f32_e32 v170, v170
	v_exp_f32_e32 v171, v171
	v_add_f32_e32 v168, 1.0, v168
	v_add_f32_e32 v169, 1.0, v169
	v_add_f32_e32 v170, 1.0, v170
	v_add_f32_e32 v171, 1.0, v171
	v_rcp_f32_e32 v168, v168
	v_rcp_f32_e32 v169, v169
	v_rcp_f32_e32 v170, v170
	v_rcp_f32_e32 v171, v171
	s_nop 0
	v_cvt_pk_bf16_f32 v168, v168, v169
	v_cvt_pk_bf16_f32 v169, v170, v171
	ds_write_b64 v108, v[168:169] offset:0
	v_mul_f32_e32 v176, 0xbfb8aa3b, v30
	v_mul_f32_e32 v177, 0xbfb8aa3b, v31
	v_mul_f32_e32 v178, 0xbfb8aa3b, v32
	v_mul_f32_e32 v179, 0xbfb8aa3b, v33
	v_exp_f32_e32 v176, v176
	v_exp_f32_e32 v177, v177
	v_exp_f32_e32 v178, v178
	v_exp_f32_e32 v179, v179
	v_add_f32_e32 v176, 1.0, v176
	v_add_f32_e32 v177, 1.0, v177
	v_add_f32_e32 v178, 1.0, v178
	v_add_f32_e32 v179, 1.0, v179
	v_rcp_f32_e32 v176, v176
	v_rcp_f32_e32 v177, v177
	v_rcp_f32_e32 v178, v178
	v_rcp_f32_e32 v179, v179
	s_nop 0
	v_cvt_pk_bf16_f32 v176, v176, v177
	v_cvt_pk_bf16_f32 v177, v178, v179
	ds_write_b64 v108, v[176:177] offset:12288
	s_waitcnt vmcnt(12)
	v_mfma_f32_16x16x32_bf16 v[26:29], v[42:45], v[2:5], 0
	v_mfma_f32_16x16x32_bf16 v[26:29], v[46:49], v[6:9], v[26:29]
	v_mfma_f32_16x16x32_bf16 v[30:33], v[42:45], v[10:13], 0
	v_mfma_f32_16x16x32_bf16 v[30:33], v[46:49], v[14:17], v[30:33]
	v_add_u32_e32 v108, 0x6120, v154
	s_nop 7
	v_pk_add_f32 v[26:27], v[26:27], v[50:51]
	v_pk_add_f32 v[28:29], v[28:29], v[52:53]
	v_pk_add_f32 v[30:31], v[30:31], v[50:51]
	v_pk_add_f32 v[32:33], v[32:33], v[52:53]
	s_add_u32 s16, s0, 0x56000
	s_addc_u32 s17, s1, 0
	global_load_dwordx4 v[42:45], v153, s[16:17] offset:0
	global_load_dwordx4 v[46:49], v153, s[16:17] offset:64
	s_add_u32 s18, s70, 0x980
	s_addc_u32 s19, s71, 0
	global_load_dwordx4 v[50:53], v159, s[18:19]
	v_mul_f32_e32 v168, 0xbfb8aa3b, v26
	v_mul_f32_e32 v169, 0xbfb8aa3b, v27
	v_mul_f32_e32 v170, 0xbfb8aa3b, v28
	v_mul_f32_e32 v171, 0xbfb8aa3b, v29
	v_exp_f32_e32 v168, v168
	v_exp_f32_e32 v169, v169
	v_exp_f32_e32 v170, v170
	v_exp_f32_e32 v171, v171
	v_add_f32_e32 v168, 1.0, v168
	v_add_f32_e32 v169, 1.0, v169
	v_add_f32_e32 v170, 1.0, v170
	v_add_f32_e32 v171, 1.0, v171
	v_rcp_f32_e32 v168, v168
	v_rcp_f32_e32 v169, v169
	v_rcp_f32_e32 v170, v170
	v_rcp_f32_e32 v171, v171
	s_nop 0
	v_cvt_pk_bf16_f32 v168, v168, v169
	v_cvt_pk_bf16_f32 v169, v170, v171
	ds_write_b64 v108, v[168:169] offset:0
	v_mul_f32_e32 v176, 0xbfb8aa3b, v30
	v_mul_f32_e32 v177, 0xbfb8aa3b, v31
	v_mul_f32_e32 v178, 0xbfb8aa3b, v32
	v_mul_f32_e32 v179, 0xbfb8aa3b, v33
	v_exp_f32_e32 v176, v176
	v_exp_f32_e32 v177, v177
	v_exp_f32_e32 v178, v178
	v_exp_f32_e32 v179, v179
	v_add_f32_e32 v176, 1.0, v176
	v_add_f32_e32 v177, 1.0, v177
	v_add_f32_e32 v178, 1.0, v178
	v_add_f32_e32 v179, 1.0, v179
	v_rcp_f32_e32 v176, v176
	v_rcp_f32_e32 v177, v177
	v_rcp_f32_e32 v178, v178
	v_rcp_f32_e32 v179, v179
	s_nop 0
	v_cvt_pk_bf16_f32 v176, v176, v177
	v_cvt_pk_bf16_f32 v177, v178, v179
	ds_write_b64 v108, v[176:177] offset:12288
	s_waitcnt vmcnt(12)
	v_mfma_f32_16x16x32_bf16 v[26:29], v[54:57], v[2:5], 0
	v_mfma_f32_16x16x32_bf16 v[26:29], v[58:61], v[6:9], v[26:29]
	v_mfma_f32_16x16x32_bf16 v[30:33], v[54:57], v[10:13], 0
	v_mfma_f32_16x16x32_bf16 v[30:33], v[58:61], v[14:17], v[30:33]
	v_add_u32_e32 v108, 0x6140, v154
	s_nop 7
	v_pk_add_f32 v[26:27], v[26:27], v[62:63]
	v_pk_add_f32 v[28:29], v[28:29], v[64:65]
	v_pk_add_f32 v[30:31], v[30:31], v[62:63]
	v_pk_add_f32 v[32:33], v[32:33], v[64:65]
	s_add_u32 s16, s0, 0x57000
	s_addc_u32 s17, s1, 0
	global_load_dwordx4 v[54:57], v153, s[16:17] offset:0
	global_load_dwordx4 v[58:61], v153, s[16:17] offset:64
	s_add_u32 s18, s70, 0x9c0
	s_addc_u32 s19, s71, 0
	global_load_dwordx4 v[62:65], v159, s[18:19]
	v_mul_f32_e32 v168, 0xbfb8aa3b, v26
	v_mul_f32_e32 v169, 0xbfb8aa3b, v27
	v_mul_f32_e32 v170, 0xbfb8aa3b, v28
	v_mul_f32_e32 v171, 0xbfb8aa3b, v29
	v_exp_f32_e32 v168, v168
	v_exp_f32_e32 v169, v169
	v_exp_f32_e32 v170, v170
	v_exp_f32_e32 v171, v171
	v_add_f32_e32 v168, 1.0, v168
	v_add_f32_e32 v169, 1.0, v169
	v_add_f32_e32 v170, 1.0, v170
	v_add_f32_e32 v171, 1.0, v171
	v_rcp_f32_e32 v168, v168
	v_rcp_f32_e32 v169, v169
	v_rcp_f32_e32 v170, v170
	v_rcp_f32_e32 v171, v171
	s_nop 0
	v_cvt_pk_bf16_f32 v168, v168, v169
	v_cvt_pk_bf16_f32 v169, v170, v171
	ds_write_b64 v108, v[168:169] offset:0
	v_mul_f32_e32 v176, 0xbfb8aa3b, v30
	v_mul_f32_e32 v177, 0xbfb8aa3b, v31
	v_mul_f32_e32 v178, 0xbfb8aa3b, v32
	v_mul_f32_e32 v179, 0xbfb8aa3b, v33
	v_exp_f32_e32 v176, v176
	v_exp_f32_e32 v177, v177
	v_exp_f32_e32 v178, v178
	v_exp_f32_e32 v179, v179
	v_add_f32_e32 v176, 1.0, v176
	v_add_f32_e32 v177, 1.0, v177
	v_add_f32_e32 v178, 1.0, v178
	v_add_f32_e32 v179, 1.0, v179
	v_rcp_f32_e32 v176, v176
	v_rcp_f32_e32 v177, v177
	v_rcp_f32_e32 v178, v178
	v_rcp_f32_e32 v179, v179
	s_nop 0
	v_cvt_pk_bf16_f32 v176, v176, v177
	v_cvt_pk_bf16_f32 v177, v178, v179
	ds_write_b64 v108, v[176:177] offset:12288
	s_waitcnt vmcnt(12)
	v_mfma_f32_16x16x32_bf16 v[26:29], v[66:69], v[2:5], 0
	v_mfma_f32_16x16x32_bf16 v[26:29], v[70:73], v[6:9], v[26:29]
	v_mfma_f32_16x16x32_bf16 v[30:33], v[66:69], v[10:13], 0
	v_mfma_f32_16x16x32_bf16 v[30:33], v[70:73], v[14:17], v[30:33]
	v_add_u32_e32 v108, 0x6160, v154
	s_nop 7
	v_pk_add_f32 v[26:27], v[26:27], v[74:75]
	v_pk_add_f32 v[28:29], v[28:29], v[76:77]
	v_pk_add_f32 v[30:31], v[30:31], v[74:75]
	v_pk_add_f32 v[32:33], v[32:33], v[76:77]
	s_add_u32 s16, s0, 0x58000
	s_addc_u32 s17, s1, 0
	global_load_dwordx4 v[66:69], v153, s[16:17] offset:0
	global_load_dwordx4 v[70:73], v153, s[16:17] offset:64
	s_add_u32 s18, s70, 0xa00
	s_addc_u32 s19, s71, 0
	global_load_dwordx4 v[74:77], v159, s[18:19]
	v_mul_f32_e32 v168, 0xbfb8aa3b, v26
	v_mul_f32_e32 v169, 0xbfb8aa3b, v27
	v_mul_f32_e32 v170, 0xbfb8aa3b, v28
	v_mul_f32_e32 v171, 0xbfb8aa3b, v29
	v_exp_f32_e32 v168, v168
	v_exp_f32_e32 v169, v169
	v_exp_f32_e32 v170, v170
	v_exp_f32_e32 v171, v171
	v_add_f32_e32 v168, 1.0, v168
	v_add_f32_e32 v169, 1.0, v169
	v_add_f32_e32 v170, 1.0, v170
	v_add_f32_e32 v171, 1.0, v171
	v_rcp_f32_e32 v168, v168
	v_rcp_f32_e32 v169, v169
	v_rcp_f32_e32 v170, v170
	v_rcp_f32_e32 v171, v171
	s_nop 0
	v_cvt_pk_bf16_f32 v168, v168, v169
	v_cvt_pk_bf16_f32 v169, v170, v171
	ds_write_b64 v108, v[168:169] offset:0
	v_mul_f32_e32 v176, 0xbfb8aa3b, v30
	v_mul_f32_e32 v177, 0xbfb8aa3b, v31
	v_mul_f32_e32 v178, 0xbfb8aa3b, v32
	v_mul_f32_e32 v179, 0xbfb8aa3b, v33
	v_exp_f32_e32 v176, v176
	v_exp_f32_e32 v177, v177
	v_exp_f32_e32 v178, v178
	v_exp_f32_e32 v179, v179
	v_add_f32_e32 v176, 1.0, v176
	v_add_f32_e32 v177, 1.0, v177
	v_add_f32_e32 v178, 1.0, v178
	v_add_f32_e32 v179, 1.0, v179
	v_rcp_f32_e32 v176, v176
	v_rcp_f32_e32 v177, v177
	v_rcp_f32_e32 v178, v178
	v_rcp_f32_e32 v179, v179
	s_nop 0
	v_cvt_pk_bf16_f32 v176, v176, v177
	v_cvt_pk_bf16_f32 v177, v178, v179
	ds_write_b64 v108, v[176:177] offset:12288
	s_waitcnt vmcnt(12)
	v_mfma_f32_16x16x32_bf16 v[26:29], v[78:81], v[2:5], 0
	v_mfma_f32_16x16x32_bf16 v[26:29], v[82:85], v[6:9], v[26:29]
	v_mfma_f32_16x16x32_bf16 v[30:33], v[78:81], v[10:13], 0
	v_mfma_f32_16x16x32_bf16 v[30:33], v[82:85], v[14:17], v[30:33]
	v_add_u32_e32 v108, 0x6180, v154
	s_nop 7
	v_pk_add_f32 v[26:27], v[26:27], v[86:87]
	v_pk_add_f32 v[28:29], v[28:29], v[88:89]
	v_pk_add_f32 v[30:31], v[30:31], v[86:87]
	v_pk_add_f32 v[32:33], v[32:33], v[88:89]
	s_add_u32 s16, s0, 0x59000
	s_addc_u32 s17, s1, 0
	global_load_dwordx4 v[78:81], v153, s[16:17] offset:0
	global_load_dwordx4 v[82:85], v153, s[16:17] offset:64
	s_add_u32 s18, s70, 0xa40
	s_addc_u32 s19, s71, 0
	global_load_dwordx4 v[86:89], v159, s[18:19]
	v_mul_f32_e32 v168, 0xbfb8aa3b, v26
	v_mul_f32_e32 v169, 0xbfb8aa3b, v27
	v_mul_f32_e32 v170, 0xbfb8aa3b, v28
	v_mul_f32_e32 v171, 0xbfb8aa3b, v29
	v_exp_f32_e32 v168, v168
	v_exp_f32_e32 v169, v169
	v_exp_f32_e32 v170, v170
	v_exp_f32_e32 v171, v171
	v_add_f32_e32 v168, 1.0, v168
	v_add_f32_e32 v169, 1.0, v169
	v_add_f32_e32 v170, 1.0, v170
	v_add_f32_e32 v171, 1.0, v171
	v_rcp_f32_e32 v168, v168
	v_rcp_f32_e32 v169, v169
	v_rcp_f32_e32 v170, v170
	v_rcp_f32_e32 v171, v171
	s_nop 0
	v_cvt_pk_bf16_f32 v168, v168, v169
	v_cvt_pk_bf16_f32 v169, v170, v171
	ds_write_b64 v108, v[168:169] offset:0
	v_mul_f32_e32 v176, 0xbfb8aa3b, v30
	v_mul_f32_e32 v177, 0xbfb8aa3b, v31
	v_mul_f32_e32 v178, 0xbfb8aa3b, v32
	v_mul_f32_e32 v179, 0xbfb8aa3b, v33
	v_exp_f32_e32 v176, v176
	v_exp_f32_e32 v177, v177
	v_exp_f32_e32 v178, v178
	v_exp_f32_e32 v179, v179
	v_add_f32_e32 v176, 1.0, v176
	v_add_f32_e32 v177, 1.0, v177
	v_add_f32_e32 v178, 1.0, v178
	v_add_f32_e32 v179, 1.0, v179
	v_rcp_f32_e32 v176, v176
	v_rcp_f32_e32 v177, v177
	v_rcp_f32_e32 v178, v178
	v_rcp_f32_e32 v179, v179
	s_nop 0
	v_cvt_pk_bf16_f32 v176, v176, v177
	v_cvt_pk_bf16_f32 v177, v178, v179
	ds_write_b64 v108, v[176:177] offset:12288
	s_waitcnt vmcnt(12)
	v_mfma_f32_16x16x32_bf16 v[26:29], v[18:21], v[2:5], 0
	v_mfma_f32_16x16x32_bf16 v[26:29], v[22:25], v[6:9], v[26:29]
	v_mfma_f32_16x16x32_bf16 v[30:33], v[18:21], v[10:13], 0
	v_mfma_f32_16x16x32_bf16 v[30:33], v[22:25], v[14:17], v[30:33]
	v_add_u32_e32 v108, 0x61a0, v154
	s_nop 7
	v_pk_add_f32 v[26:27], v[26:27], v[38:39]
	v_pk_add_f32 v[28:29], v[28:29], v[40:41]
	v_pk_add_f32 v[30:31], v[30:31], v[38:39]
	v_pk_add_f32 v[32:33], v[32:33], v[40:41]
	v_mul_f32_e32 v168, 0xbfb8aa3b, v26
	v_mul_f32_e32 v169, 0xbfb8aa3b, v27
	v_mul_f32_e32 v170, 0xbfb8aa3b, v28
	v_mul_f32_e32 v171, 0xbfb8aa3b, v29
	v_exp_f32_e32 v168, v168
	v_exp_f32_e32 v169, v169
	v_exp_f32_e32 v170, v170
	v_exp_f32_e32 v171, v171
	v_add_f32_e32 v168, 1.0, v168
	v_add_f32_e32 v169, 1.0, v169
	v_add_f32_e32 v170, 1.0, v170
	v_add_f32_e32 v171, 1.0, v171
	v_rcp_f32_e32 v168, v168
	v_rcp_f32_e32 v169, v169
	v_rcp_f32_e32 v170, v170
	v_rcp_f32_e32 v171, v171
	s_nop 0
	v_cvt_pk_bf16_f32 v168, v168, v169
	v_cvt_pk_bf16_f32 v169, v170, v171
	ds_write_b64 v108, v[168:169] offset:0
	v_mul_f32_e32 v176, 0xbfb8aa3b, v30
	v_mul_f32_e32 v177, 0xbfb8aa3b, v31
	v_mul_f32_e32 v178, 0xbfb8aa3b, v32
	v_mul_f32_e32 v179, 0xbfb8aa3b, v33
	v_exp_f32_e32 v176, v176
	v_exp_f32_e32 v177, v177
	v_exp_f32_e32 v178, v178
	v_exp_f32_e32 v179, v179
	v_add_f32_e32 v176, 1.0, v176
	v_add_f32_e32 v177, 1.0, v177
	v_add_f32_e32 v178, 1.0, v178
	v_add_f32_e32 v179, 1.0, v179
	v_rcp_f32_e32 v176, v176
	v_rcp_f32_e32 v177, v177
	v_rcp_f32_e32 v178, v178
	v_rcp_f32_e32 v179, v179
	s_nop 0
	v_cvt_pk_bf16_f32 v176, v176, v177
	v_cvt_pk_bf16_f32 v177, v178, v179
	ds_write_b64 v108, v[176:177] offset:12288
	s_waitcnt vmcnt(9)
	v_mfma_f32_16x16x32_bf16 v[26:29], v[42:45], v[2:5], 0
	v_mfma_f32_16x16x32_bf16 v[26:29], v[46:49], v[6:9], v[26:29]
	v_mfma_f32_16x16x32_bf16 v[30:33], v[42:45], v[10:13], 0
	v_mfma_f32_16x16x32_bf16 v[30:33], v[46:49], v[14:17], v[30:33]
	v_add_u32_e32 v108, 0x61c0, v154
	s_nop 7
	v_pk_add_f32 v[26:27], v[26:27], v[50:51]
	v_pk_add_f32 v[28:29], v[28:29], v[52:53]
	v_pk_add_f32 v[30:31], v[30:31], v[50:51]
	v_pk_add_f32 v[32:33], v[32:33], v[52:53]
	v_mul_f32_e32 v168, 0xbfb8aa3b, v26
	v_mul_f32_e32 v169, 0xbfb8aa3b, v27
	v_mul_f32_e32 v170, 0xbfb8aa3b, v28
	v_mul_f32_e32 v171, 0xbfb8aa3b, v29
	v_exp_f32_e32 v168, v168
	v_exp_f32_e32 v169, v169
	v_exp_f32_e32 v170, v170
	v_exp_f32_e32 v171, v171
	v_add_f32_e32 v168, 1.0, v168
	v_add_f32_e32 v169, 1.0, v169
	v_add_f32_e32 v170, 1.0, v170
	v_add_f32_e32 v171, 1.0, v171
	v_rcp_f32_e32 v168, v168
	v_rcp_f32_e32 v169, v169
	v_rcp_f32_e32 v170, v170
	v_rcp_f32_e32 v171, v171
	s_nop 0
	v_cvt_pk_bf16_f32 v168, v168, v169
	v_cvt_pk_bf16_f32 v169, v170, v171
	ds_write_b64 v108, v[168:169] offset:0
	v_mul_f32_e32 v176, 0xbfb8aa3b, v30
	v_mul_f32_e32 v177, 0xbfb8aa3b, v31
	v_mul_f32_e32 v178, 0xbfb8aa3b, v32
	v_mul_f32_e32 v179, 0xbfb8aa3b, v33
	v_exp_f32_e32 v176, v176
	v_exp_f32_e32 v177, v177
	v_exp_f32_e32 v178, v178
	v_exp_f32_e32 v179, v179
	v_add_f32_e32 v176, 1.0, v176
	v_add_f32_e32 v177, 1.0, v177
	v_add_f32_e32 v178, 1.0, v178
	v_add_f32_e32 v179, 1.0, v179
	v_rcp_f32_e32 v176, v176
	v_rcp_f32_e32 v177, v177
	v_rcp_f32_e32 v178, v178
	v_rcp_f32_e32 v179, v179
	s_nop 0
	v_cvt_pk_bf16_f32 v176, v176, v177
	v_cvt_pk_bf16_f32 v177, v178, v179
	ds_write_b64 v108, v[176:177] offset:12288
	s_waitcnt vmcnt(6)
	v_mfma_f32_16x16x32_bf16 v[26:29], v[54:57], v[2:5], 0
	v_mfma_f32_16x16x32_bf16 v[26:29], v[58:61], v[6:9], v[26:29]
	v_mfma_f32_16x16x32_bf16 v[30:33], v[54:57], v[10:13], 0
	v_mfma_f32_16x16x32_bf16 v[30:33], v[58:61], v[14:17], v[30:33]
	v_add_u32_e32 v108, 0x61e0, v154
	s_nop 7
	v_pk_add_f32 v[26:27], v[26:27], v[62:63]
	v_pk_add_f32 v[28:29], v[28:29], v[64:65]
	v_pk_add_f32 v[30:31], v[30:31], v[62:63]
	v_pk_add_f32 v[32:33], v[32:33], v[64:65]
	v_mul_f32_e32 v168, 0xbfb8aa3b, v26
	v_mul_f32_e32 v169, 0xbfb8aa3b, v27
	v_mul_f32_e32 v170, 0xbfb8aa3b, v28
	v_mul_f32_e32 v171, 0xbfb8aa3b, v29
	v_exp_f32_e32 v168, v168
	v_exp_f32_e32 v169, v169
	v_exp_f32_e32 v170, v170
	v_exp_f32_e32 v171, v171
	v_add_f32_e32 v168, 1.0, v168
	v_add_f32_e32 v169, 1.0, v169
	v_add_f32_e32 v170, 1.0, v170
	v_add_f32_e32 v171, 1.0, v171
	v_rcp_f32_e32 v168, v168
	v_rcp_f32_e32 v169, v169
	v_rcp_f32_e32 v170, v170
	v_rcp_f32_e32 v171, v171
	s_nop 0
	v_cvt_pk_bf16_f32 v168, v168, v169
	v_cvt_pk_bf16_f32 v169, v170, v171
	ds_write_b64 v108, v[168:169] offset:0
	v_mul_f32_e32 v176, 0xbfb8aa3b, v30
	v_mul_f32_e32 v177, 0xbfb8aa3b, v31
	v_mul_f32_e32 v178, 0xbfb8aa3b, v32
	v_mul_f32_e32 v179, 0xbfb8aa3b, v33
	v_exp_f32_e32 v176, v176
	v_exp_f32_e32 v177, v177
	v_exp_f32_e32 v178, v178
	v_exp_f32_e32 v179, v179
	v_add_f32_e32 v176, 1.0, v176
	v_add_f32_e32 v177, 1.0, v177
	v_add_f32_e32 v178, 1.0, v178
	v_add_f32_e32 v179, 1.0, v179
	v_rcp_f32_e32 v176, v176
	v_rcp_f32_e32 v177, v177
	v_rcp_f32_e32 v178, v178
	v_rcp_f32_e32 v179, v179
	s_nop 0
	v_cvt_pk_bf16_f32 v176, v176, v177
	v_cvt_pk_bf16_f32 v177, v178, v179
	ds_write_b64 v108, v[176:177] offset:12288
	s_waitcnt vmcnt(3)
	v_mfma_f32_16x16x32_bf16 v[26:29], v[66:69], v[2:5], 0
	v_mfma_f32_16x16x32_bf16 v[26:29], v[70:73], v[6:9], v[26:29]
	v_mfma_f32_16x16x32_bf16 v[30:33], v[66:69], v[10:13], 0
	v_mfma_f32_16x16x32_bf16 v[30:33], v[70:73], v[14:17], v[30:33]
	v_add_u32_e32 v108, 0x6200, v154
	s_nop 7
	v_pk_add_f32 v[26:27], v[26:27], v[74:75]
	v_pk_add_f32 v[28:29], v[28:29], v[76:77]
	v_pk_add_f32 v[30:31], v[30:31], v[74:75]
	v_pk_add_f32 v[32:33], v[32:33], v[76:77]
	v_mul_f32_e32 v168, 0xbfb8aa3b, v26
	v_mul_f32_e32 v169, 0xbfb8aa3b, v27
	v_mul_f32_e32 v170, 0xbfb8aa3b, v28
	v_mul_f32_e32 v171, 0xbfb8aa3b, v29
	v_exp_f32_e32 v168, v168
	v_exp_f32_e32 v169, v169
	v_exp_f32_e32 v170, v170
	v_exp_f32_e32 v171, v171
	v_add_f32_e32 v168, 1.0, v168
	v_add_f32_e32 v169, 1.0, v169
	v_add_f32_e32 v170, 1.0, v170
	v_add_f32_e32 v171, 1.0, v171
	v_rcp_f32_e32 v168, v168
	v_rcp_f32_e32 v169, v169
	v_rcp_f32_e32 v170, v170
	v_rcp_f32_e32 v171, v171
	s_nop 0
	v_cvt_pk_bf16_f32 v168, v168, v169
	v_cvt_pk_bf16_f32 v169, v170, v171
	ds_write_b64 v108, v[168:169] offset:0
	v_mul_f32_e32 v176, 0xbfb8aa3b, v30
	v_mul_f32_e32 v177, 0xbfb8aa3b, v31
	v_mul_f32_e32 v178, 0xbfb8aa3b, v32
	v_mul_f32_e32 v179, 0xbfb8aa3b, v33
	v_exp_f32_e32 v176, v176
	v_exp_f32_e32 v177, v177
	v_exp_f32_e32 v178, v178
	v_exp_f32_e32 v179, v179
	v_add_f32_e32 v176, 1.0, v176
	v_add_f32_e32 v177, 1.0, v177
	v_add_f32_e32 v178, 1.0, v178
	v_add_f32_e32 v179, 1.0, v179
	v_rcp_f32_e32 v176, v176
	v_rcp_f32_e32 v177, v177
	v_rcp_f32_e32 v178, v178
	v_rcp_f32_e32 v179, v179
	s_nop 0
	v_cvt_pk_bf16_f32 v176, v176, v177
	v_cvt_pk_bf16_f32 v177, v178, v179
	ds_write_b64 v108, v[176:177] offset:12288
	s_waitcnt vmcnt(0)
	v_mfma_f32_16x16x32_bf16 v[26:29], v[78:81], v[2:5], 0
	v_mfma_f32_16x16x32_bf16 v[26:29], v[82:85], v[6:9], v[26:29]
	v_mfma_f32_16x16x32_bf16 v[30:33], v[78:81], v[10:13], 0
	v_mfma_f32_16x16x32_bf16 v[30:33], v[82:85], v[14:17], v[30:33]
	v_add_u32_e32 v108, 0x6220, v154
	s_nop 7
	v_pk_add_f32 v[26:27], v[26:27], v[86:87]
	v_pk_add_f32 v[28:29], v[28:29], v[88:89]
	v_pk_add_f32 v[30:31], v[30:31], v[86:87]
	v_pk_add_f32 v[32:33], v[32:33], v[88:89]
	v_mul_f32_e32 v168, 0xbfb8aa3b, v26
	v_mul_f32_e32 v169, 0xbfb8aa3b, v27
	v_mul_f32_e32 v170, 0xbfb8aa3b, v28
	v_mul_f32_e32 v171, 0xbfb8aa3b, v29
	v_exp_f32_e32 v168, v168
	v_exp_f32_e32 v169, v169
	v_exp_f32_e32 v170, v170
	v_exp_f32_e32 v171, v171
	v_add_f32_e32 v168, 1.0, v168
	v_add_f32_e32 v169, 1.0, v169
	v_add_f32_e32 v170, 1.0, v170
	v_add_f32_e32 v171, 1.0, v171
	v_rcp_f32_e32 v168, v168
	v_rcp_f32_e32 v169, v169
	v_rcp_f32_e32 v170, v170
	v_rcp_f32_e32 v171, v171
	s_nop 0
	v_cvt_pk_bf16_f32 v168, v168, v169
	v_cvt_pk_bf16_f32 v169, v170, v171
	ds_write_b64 v108, v[168:169] offset:0
	v_mul_f32_e32 v176, 0xbfb8aa3b, v30
	v_mul_f32_e32 v177, 0xbfb8aa3b, v31
	v_mul_f32_e32 v178, 0xbfb8aa3b, v32
	v_mul_f32_e32 v179, 0xbfb8aa3b, v33
	v_exp_f32_e32 v176, v176
	v_exp_f32_e32 v177, v177
	v_exp_f32_e32 v178, v178
	v_exp_f32_e32 v179, v179
	v_add_f32_e32 v176, 1.0, v176
	v_add_f32_e32 v177, 1.0, v177
	v_add_f32_e32 v178, 1.0, v178
	v_add_f32_e32 v179, 1.0, v179
	v_rcp_f32_e32 v176, v176
	v_rcp_f32_e32 v177, v177
	v_rcp_f32_e32 v178, v178
	v_rcp_f32_e32 v179, v179
	s_nop 0
	v_cvt_pk_bf16_f32 v176, v176, v177
	v_cvt_pk_bf16_f32 v177, v178, v179
	ds_write_b64 v108, v[176:177] offset:12288
	s_branch .LBB0_402
.Lb3w_6:
	ds_read_b128 v[2:5], v0 offset:128
	ds_read_b128 v[6:9], v0 offset:192
	ds_read_b128 v[10:13], v0 offset:8576
	ds_read_b128 v[14:17], v0 offset:8640
	ds_read_b128 v[18:21], v0 offset:256
	ds_read_b128 v[22:25], v0 offset:320
	ds_read_b128 v[38:41], v0 offset:384
	ds_read_b128 v[42:45], v0 offset:448
	ds_read_b128 v[46:49], v0 offset:8704
	ds_read_b128 v[50:53], v0 offset:8768
	ds_read_b128 v[54:57], v0 offset:8832
	ds_read_b128 v[58:61], v0 offset:8896
	s_add_u32 s16, s0, 0x5a000
	s_addc_u32 s17, s1, 0
	global_load_dwordx4 v[62:65], v153, s[16:17] offset:0
	global_load_dwordx4 v[66:69], v153, s[16:17] offset:64
	s_add_u32 s18, s70, 0xa80
	s_addc_u32 s19, s71, 0
	global_load_dwordx4 v[70:73], v159, s[18:19]
	s_add_u32 s16, s0, 0x5b000
	s_addc_u32 s17, s1, 0
	global_load_dwordx4 v[78:81], v153, s[16:17] offset:0
	global_load_dwordx4 v[82:85], v153, s[16:17] offset:64
	s_add_u32 s18, s70, 0xac0
	s_addc_u32 s19, s71, 0
	global_load_dwordx4 v[86:89], v159, s[18:19]
	s_add_u32 s16, s0, 0x5c000
	s_addc_u32 s17, s1, 0
	global_load_dwordx4 v[94:97], v153, s[16:17] offset:0
	global_load_dwordx4 v[160:163], v153, s[16:17] offset:64
	s_add_u32 s18, s70, 0xb00
	s_addc_u32 s19, s71, 0
	global_load_dwordx4 v[164:167], v159, s[18:19]
	s_add_u32 s16, s0, 0x5d000
	s_addc_u32 s17, s1, 0
	global_load_dwordx4 v[218:221], v153, s[16:17] offset:0
	global_load_dwordx4 v[234:237], v153, s[16:17] offset:64
	s_add_u32 s18, s70, 0xb40
	s_addc_u32 s19, s71, 0
	global_load_dwordx4 v[238:241], v159, s[18:19]
	s_waitcnt vmcnt(9) lgkmcnt(0)
	v_mfma_f32_16x16x32_bf16 v[26:29], v[62:65], v[2:5], 0
	v_mfma_f32_16x16x32_bf16 v[26:29], v[66:69], v[6:9], v[26:29]
	v_mfma_f32_16x16x32_bf16 v[30:33], v[62:65], v[10:13], 0
	v_mfma_f32_16x16x32_bf16 v[30:33], v[66:69], v[14:17], v[30:33]
	v_add_u32_e32 v108, 0x6240, v154
	s_nop 7
	v_pk_add_f32 v[26:27], v[26:27], v[70:71]
	v_pk_add_f32 v[28:29], v[28:29], v[72:73]
	v_pk_add_f32 v[30:31], v[30:31], v[70:71]
	v_pk_add_f32 v[32:33], v[32:33], v[72:73]
	s_add_u32 s16, s0, 0x5e000
	s_addc_u32 s17, s1, 0
	global_load_dwordx4 v[62:65], v153, s[16:17] offset:0
	global_load_dwordx4 v[66:69], v153, s[16:17] offset:64
	s_add_u32 s18, s70, 0xb80
	s_addc_u32 s19, s71, 0
	global_load_dwordx4 v[70:73], v159, s[18:19]
	v_mul_f32_e32 v168, 0xbfb8aa3b, v26
	v_mul_f32_e32 v169, 0xbfb8aa3b, v27
	v_mul_f32_e32 v170, 0xbfb8aa3b, v28
	v_mul_f32_e32 v171, 0xbfb8aa3b, v29
	v_exp_f32_e32 v168, v168
	v_exp_f32_e32 v169, v169
	v_exp_f32_e32 v170, v170
	v_exp_f32_e32 v171, v171
	v_add_f32_e32 v168, 1.0, v168
	v_add_f32_e32 v169, 1.0, v169
	v_add_f32_e32 v170, 1.0, v170
	v_add_f32_e32 v171, 1.0, v171
	v_rcp_f32_e32 v168, v168
	v_rcp_f32_e32 v169, v169
	v_rcp_f32_e32 v170, v170
	v_rcp_f32_e32 v171, v171
	s_nop 0
	v_cvt_pk_bf16_f32 v168, v168, v169
	v_cvt_pk_bf16_f32 v169, v170, v171
	ds_write_b64 v108, v[168:169] offset:0
	v_mul_f32_e32 v176, 0xbfb8aa3b, v30
	v_mul_f32_e32 v177, 0xbfb8aa3b, v31
	v_mul_f32_e32 v178, 0xbfb8aa3b, v32
	v_mul_f32_e32 v179, 0xbfb8aa3b, v33
	v_exp_f32_e32 v176, v176
	v_exp_f32_e32 v177, v177
	v_exp_f32_e32 v178, v178
	v_exp_f32_e32 v179, v179
	v_add_f32_e32 v176, 1.0, v176
	v_add_f32_e32 v177, 1.0, v177
	v_add_f32_e32 v178, 1.0, v178
	v_add_f32_e32 v179, 1.0, v179
	v_rcp_f32_e32 v176, v176
	v_rcp_f32_e32 v177, v177
	v_rcp_f32_e32 v178, v178
	v_rcp_f32_e32 v179, v179
	s_nop 0
	v_cvt_pk_bf16_f32 v176, v176, v177
	v_cvt_pk_bf16_f32 v177, v178, v179
	ds_write_b64 v108, v[176:177] offset:12288
	s_waitcnt vmcnt(9)
	v_mfma_f32_16x16x32_bf16 v[26:29], v[78:81], v[2:5], 0
	v_mfma_f32_16x16x32_bf16 v[26:29], v[82:85], v[6:9], v[26:29]
	v_mfma_f32_16x16x32_bf16 v[30:33], v[78:81], v[10:13], 0
	v_mfma_f32_16x16x32_bf16 v[30:33], v[82:85], v[14:17], v[30:33]
	v_add_u32_e32 v108, 0x6260, v154
	s_nop 7
	v_pk_add_f32 v[26:27], v[26:27], v[86:87]
	v_pk_add_f32 v[28:29], v[28:29], v[88:89]
	v_pk_add_f32 v[30:31], v[30:31], v[86:87]
	v_pk_add_f32 v[32:33], v[32:33], v[88:89]
	s_add_u32 s16, s0, 0x5f000
	s_addc_u32 s17, s1, 0
	global_load_dwordx4 v[78:81], v153, s[16:17] offset:0
	global_load_dwordx4 v[82:85], v153, s[16:17] offset:64
	s_add_u32 s18, s70, 0xbc0
	s_addc_u32 s19, s71, 0
	global_load_dwordx4 v[86:89], v159, s[18:19]
	v_mul_f32_e32 v168, 0xbfb8aa3b, v26
	v_mul_f32_e32 v169, 0xbfb8aa3b, v27
	v_mul_f32_e32 v170, 0xbfb8aa3b, v28
	v_mul_f32_e32 v171, 0xbfb8aa3b, v29
	v_exp_f32_e32 v168, v168
	v_exp_f32_e32 v169, v169
	v_exp_f32_e32 v170, v170
	v_exp_f32_e32 v171, v171
	v_add_f32_e32 v168, 1.0, v168
	v_add_f32_e32 v169, 1.0, v169
	v_add_f32_e32 v170, 1.0, v170
	v_add_f32_e32 v171, 1.0, v171
	v_rcp_f32_e32 v168, v168
	v_rcp_f32_e32 v169, v169
	v_rcp_f32_e32 v170, v170
	v_rcp_f32_e32 v171, v171
	s_nop 0
	v_cvt_pk_bf16_f32 v168, v168, v169
	v_cvt_pk_bf16_f32 v169, v170, v171
	ds_write_b64 v108, v[168:169] offset:0
	v_mul_f32_e32 v176, 0xbfb8aa3b, v30
	v_mul_f32_e32 v177, 0xbfb8aa3b, v31
	v_mul_f32_e32 v178, 0xbfb8aa3b, v32
	v_mul_f32_e32 v179, 0xbfb8aa3b, v33
	v_exp_f32_e32 v176, v176
	v_exp_f32_e32 v177, v177
	v_exp_f32_e32 v178, v178
	v_exp_f32_e32 v179, v179
	v_add_f32_e32 v176, 1.0, v176
	v_add_f32_e32 v177, 1.0, v177
	v_add_f32_e32 v178, 1.0, v178
	v_add_f32_e32 v179, 1.0, v179
	v_rcp_f32_e32 v176, v176
	v_rcp_f32_e32 v177, v177
	v_rcp_f32_e32 v178, v178
	v_rcp_f32_e32 v179, v179
	s_nop 0
	v_cvt_pk_bf16_f32 v176, v176, v177
	v_cvt_pk_bf16_f32 v177, v178, v179
	ds_write_b64 v108, v[176:177] offset:12288
	s_waitcnt vmcnt(9)
	v_mfma_f32_16x16x32_bf16 v[26:29], v[94:97], v[2:5], 0
	v_mfma_f32_16x16x32_bf16 v[26:29], v[160:163], v[6:9], v[26:29]
	v_mfma_f32_16x16x32_bf16 v[30:33], v[94:97], v[10:13], 0
	v_mfma_f32_16x16x32_bf16 v[30:33], v[160:163], v[14:17], v[30:33]
	v_add_u32_e32 v108, 0x6280, v154
	s_nop 7
	v_pk_add_f32 v[26:27], v[26:27], v[164:165]
	v_pk_add_f32 v[28:29], v[28:29], v[166:167]
	v_pk_add_f32 v[30:31], v[30:31], v[164:165]
	v_pk_add_f32 v[32:33], v[32:33], v[166:167]
	s_add_u32 s16, s0, 0x60000
	s_addc_u32 s17, s1, 0
	global_load_dwordx4 v[94:97], v153, s[16:17] offset:0
	global_load_dwordx4 v[160:163], v153, s[16:17] offset:64
	global_load_dwordx4 v[164:167], v153, s[16:17] offset:128
	global_load_dwordx4 v[182:185], v153, s[16:17] offset:192
	v_mul_f32_e32 v168, 0xbfb8aa3b, v26
	v_mul_f32_e32 v169, 0xbfb8aa3b, v27
	v_mul_f32_e32 v170, 0xbfb8aa3b, v28
	v_mul_f32_e32 v171, 0xbfb8aa3b, v29
	v_exp_f32_e32 v168, v168
	v_exp_f32_e32 v169, v169
	v_exp_f32_e32 v170, v170
	v_exp_f32_e32 v171, v171
	v_add_f32_e32 v168, 1.0, v168
	v_add_f32_e32 v169, 1.0, v169
	v_add_f32_e32 v170, 1.0, v170
	v_add_f32_e32 v171, 1.0, v171
	v_rcp_f32_e32 v168, v168
	v_rcp_f32_e32 v169, v169
	v_rcp_f32_e32 v170, v170
	v_rcp_f32_e32 v171, v171
	s_nop 0
	v_cvt_pk_bf16_f32 v168, v168, v169
	v_cvt_pk_bf16_f32 v169, v170, v171
	ds_write_b64 v108, v[168:169] offset:0
	v_mul_f32_e32 v176, 0xbfb8aa3b, v30
	v_mul_f32_e32 v177, 0xbfb8aa3b, v31
	v_mul_f32_e32 v178, 0xbfb8aa3b, v32
	v_mul_f32_e32 v179, 0xbfb8aa3b, v33
	v_exp_f32_e32 v176, v176
	v_exp_f32_e32 v177, v177
	v_exp_f32_e32 v178, v178
	v_exp_f32_e32 v179, v179
	v_add_f32_e32 v176, 1.0, v176
	v_add_f32_e32 v177, 1.0, v177
	v_add_f32_e32 v178, 1.0, v178
	v_add_f32_e32 v179, 1.0, v179
	v_rcp_f32_e32 v176, v176
	v_rcp_f32_e32 v177, v177
	v_rcp_f32_e32 v178, v178
	v_rcp_f32_e32 v179, v179
	s_nop 0
	v_cvt_pk_bf16_f32 v176, v176, v177
	v_cvt_pk_bf16_f32 v177, v178, v179
	ds_write_b64 v108, v[176:177] offset:12288
	s_waitcnt vmcnt(10)
	v_mfma_f32_16x16x32_bf16 v[26:29], v[218:221], v[2:5], 0
	v_mfma_f32_16x16x32_bf16 v[26:29], v[234:237], v[6:9], v[26:29]
	v_mfma_f32_16x16x32_bf16 v[30:33], v[218:221], v[10:13], 0
	v_mfma_f32_16x16x32_bf16 v[30:33], v[234:237], v[14:17], v[30:33]
	v_add_u32_e32 v108, 0x62a0, v154
	s_nop 7
	v_pk_add_f32 v[26:27], v[26:27], v[238:239]
	v_pk_add_f32 v[28:29], v[28:29], v[240:241]
	v_pk_add_f32 v[30:31], v[30:31], v[238:239]
	v_pk_add_f32 v[32:33], v[32:33], v[240:241]
	s_add_u32 s16, s0, 0x61000
	s_addc_u32 s17, s1, 0
	global_load_dwordx4 v[218:221], v153, s[16:17] offset:0
	global_load_dwordx4 v[234:237], v153, s[16:17] offset:64
	global_load_dwordx4 v[238:241], v153, s[16:17] offset:128
	global_load_dwordx4 v[242:245], v153, s[16:17] offset:192
	v_mul_f32_e32 v168, 0xbfb8aa3b, v26
	v_mul_f32_e32 v169, 0xbfb8aa3b, v27
	v_mul_f32_e32 v170, 0xbfb8aa3b, v28
	v_mul_f32_e32 v171, 0xbfb8aa3b, v29
	v_exp_f32_e32 v168, v168
	v_exp_f32_e32 v169, v169
	v_exp_f32_e32 v170, v170
	v_exp_f32_e32 v171, v171
	v_add_f32_e32 v168, 1.0, v168
	v_add_f32_e32 v169, 1.0, v169
	v_add_f32_e32 v170, 1.0, v170
	v_add_f32_e32 v171, 1.0, v171
	v_rcp_f32_e32 v168, v168
	v_rcp_f32_e32 v169, v169
	v_rcp_f32_e32 v170, v170
	v_rcp_f32_e32 v171, v171
	s_nop 0
	v_cvt_pk_bf16_f32 v168, v168, v169
	v_cvt_pk_bf16_f32 v169, v170, v171
	ds_write_b64 v108, v[168:169] offset:0
	v_mul_f32_e32 v176, 0xbfb8aa3b, v30
	v_mul_f32_e32 v177, 0xbfb8aa3b, v31
	v_mul_f32_e32 v178, 0xbfb8aa3b, v32
	v_mul_f32_e32 v179, 0xbfb8aa3b, v33
	v_exp_f32_e32 v176, v176
	v_exp_f32_e32 v177, v177
	v_exp_f32_e32 v178, v178
	v_exp_f32_e32 v179, v179
	v_add_f32_e32 v176, 1.0, v176
	v_add_f32_e32 v177, 1.0, v177
	v_add_f32_e32 v178, 1.0, v178
	v_add_f32_e32 v179, 1.0, v179
	v_rcp_f32_e32 v176, v176
	v_rcp_f32_e32 v177, v177
	v_rcp_f32_e32 v178, v178
	v_rcp_f32_e32 v179, v179
	s_nop 0
	v_cvt_pk_bf16_f32 v176, v176, v177
	v_cvt_pk_bf16_f32 v177, v178, v179
	ds_write_b64 v108, v[176:177] offset:12288
	s_waitcnt vmcnt(11)
	v_mfma_f32_16x16x32_bf16 v[26:29], v[62:65], v[2:5], 0
	v_mfma_f32_16x16x32_bf16 v[26:29], v[66:69], v[6:9], v[26:29]
	v_mfma_f32_16x16x32_bf16 v[30:33], v[62:65], v[10:13], 0
	v_mfma_f32_16x16x32_bf16 v[30:33], v[66:69], v[14:17], v[30:33]
	v_add_u32_e32 v108, 0x62c0, v154
	s_nop 7
	v_pk_add_f32 v[26:27], v[26:27], v[70:71]
	v_pk_add_f32 v[28:29], v[28:29], v[72:73]
	v_pk_add_f32 v[30:31], v[30:31], v[70:71]
	v_pk_add_f32 v[32:33], v[32:33], v[72:73]
	s_add_u32 s16, s0, 0x62000
	s_addc_u32 s17, s1, 0
	global_load_dwordx4 v[62:65], v153, s[16:17] offset:0
	global_load_dwordx4 v[66:69], v153, s[16:17] offset:64
	global_load_dwordx4 v[70:73], v153, s[16:17] offset:128
	global_load_dwordx4 v[74:77], v153, s[16:17] offset:192
	v_mul_f32_e32 v168, 0xbfb8aa3b, v26
	v_mul_f32_e32 v169, 0xbfb8aa3b, v27
	v_mul_f32_e32 v170, 0xbfb8aa3b, v28
	v_mul_f32_e32 v171, 0xbfb8aa3b, v29
	v_exp_f32_e32 v168, v168
	v_exp_f32_e32 v169, v169
	v_exp_f32_e32 v170, v170
	v_exp_f32_e32 v171, v171
	v_add_f32_e32 v168, 1.0, v168
	v_add_f32_e32 v169, 1.0, v169
	v_add_f32_e32 v170, 1.0, v170
	v_add_f32_e32 v171, 1.0, v171
	v_rcp_f32_e32 v168, v168
	v_rcp_f32_e32 v169, v169
	v_rcp_f32_e32 v170, v170
	v_rcp_f32_e32 v171, v171
	s_nop 0
	v_cvt_pk_bf16_f32 v168, v168, v169
	v_cvt_pk_bf16_f32 v169, v170, v171
	ds_write_b64 v108, v[168:169] offset:0
	v_mul_f32_e32 v176, 0xbfb8aa3b, v30
	v_mul_f32_e32 v177, 0xbfb8aa3b, v31
	v_mul_f32_e32 v178, 0xbfb8aa3b, v32
	v_mul_f32_e32 v179, 0xbfb8aa3b, v33
	v_exp_f32_e32 v176, v176
	v_exp_f32_e32 v177, v177
	v_exp_f32_e32 v178, v178
	v_exp_f32_e32 v179, v179
	v_add_f32_e32 v176, 1.0, v176
	v_add_f32_e32 v177, 1.0, v177
	v_add_f32_e32 v178, 1.0, v178
	v_add_f32_e32 v179, 1.0, v179
	v_rcp_f32_e32 v176, v176
	v_rcp_f32_e32 v177, v177
	v_rcp_f32_e32 v178, v178
	v_rcp_f32_e32 v179, v179
	s_nop 0
	v_cvt_pk_bf16_f32 v176, v176, v177
	v_cvt_pk_bf16_f32 v177, v178, v179
	ds_write_b64 v108, v[176:177] offset:12288
	s_waitcnt vmcnt(12)
	v_mfma_f32_16x16x32_bf16 v[26:29], v[78:81], v[2:5], 0
	v_mfma_f32_16x16x32_bf16 v[26:29], v[82:85], v[6:9], v[26:29]
	v_mfma_f32_16x16x32_bf16 v[30:33], v[78:81], v[10:13], 0
	v_mfma_f32_16x16x32_bf16 v[30:33], v[82:85], v[14:17], v[30:33]
	v_add_u32_e32 v108, 0x62e0, v154
	s_nop 7
	v_pk_add_f32 v[26:27], v[26:27], v[86:87]
	v_pk_add_f32 v[28:29], v[28:29], v[88:89]
	v_pk_add_f32 v[30:31], v[30:31], v[86:87]
	v_pk_add_f32 v[32:33], v[32:33], v[88:89]
	s_add_u32 s16, s0, 0x63000
	s_addc_u32 s17, s1, 0
	global_load_dwordx4 v[78:81], v153, s[16:17] offset:0
	global_load_dwordx4 v[82:85], v153, s[16:17] offset:64
	global_load_dwordx4 v[86:89], v153, s[16:17] offset:128
	global_load_dwordx4 v[90:93], v153, s[16:17] offset:192
	v_mul_f32_e32 v168, 0xbfb8aa3b, v26
	v_mul_f32_e32 v169, 0xbfb8aa3b, v27
	v_mul_f32_e32 v170, 0xbfb8aa3b, v28
	v_mul_f32_e32 v171, 0xbfb8aa3b, v29
	v_exp_f32_e32 v168, v168
	v_exp_f32_e32 v169, v169
	v_exp_f32_e32 v170, v170
	v_exp_f32_e32 v171, v171
	v_add_f32_e32 v168, 1.0, v168
	v_add_f32_e32 v169, 1.0, v169
	v_add_f32_e32 v170, 1.0, v170
	v_add_f32_e32 v171, 1.0, v171
	v_rcp_f32_e32 v168, v168
	v_rcp_f32_e32 v169, v169
	v_rcp_f32_e32 v170, v170
	v_rcp_f32_e32 v171, v171
	s_nop 0
	v_cvt_pk_bf16_f32 v168, v168, v169
	v_cvt_pk_bf16_f32 v169, v170, v171
	ds_write_b64 v108, v[168:169] offset:0
	v_mul_f32_e32 v176, 0xbfb8aa3b, v30
	v_mul_f32_e32 v177, 0xbfb8aa3b, v31
	v_mul_f32_e32 v178, 0xbfb8aa3b, v32
	v_mul_f32_e32 v179, 0xbfb8aa3b, v33
	v_exp_f32_e32 v176, v176
	v_exp_f32_e32 v177, v177
	v_exp_f32_e32 v178, v178
	v_exp_f32_e32 v179, v179
	v_add_f32_e32 v176, 1.0, v176
	v_add_f32_e32 v177, 1.0, v177
	v_add_f32_e32 v178, 1.0, v178
	v_add_f32_e32 v179, 1.0, v179
	v_rcp_f32_e32 v176, v176
	v_rcp_f32_e32 v177, v177
	v_rcp_f32_e32 v178, v178
	v_rcp_f32_e32 v179, v179
	s_nop 0
	v_cvt_pk_bf16_f32 v176, v176, v177
	v_cvt_pk_bf16_f32 v177, v178, v179
	ds_write_b64 v108, v[176:177] offset:12288
	s_waitcnt vmcnt(12)
	v_mfma_f32_16x16x32_bf16 v[26:29], v[94:97], v[18:21], 0
	v_mfma_f32_16x16x32_bf16 v[26:29], v[160:163], v[22:25], v[26:29]
	v_mfma_f32_16x16x32_bf16 v[26:29], v[164:167], v[38:41], v[26:29]
	v_mfma_f32_16x16x32_bf16 v[26:29], v[182:185], v[42:45], v[26:29]
	v_mfma_f32_16x16x32_bf16 v[30:33], v[94:97], v[46:49], 0
	v_mfma_f32_16x16x32_bf16 v[30:33], v[160:163], v[50:53], v[30:33]
	v_mfma_f32_16x16x32_bf16 v[30:33], v[164:167], v[54:57], v[30:33]
	v_mfma_f32_16x16x32_bf16 v[30:33], v[182:185], v[58:61], v[30:33]
	s_add_u32 s20, s54, 0x0
	s_addc_u32 s21, s55, 0
	s_nop 7
	s_add_u32 s16, s0, 0x64000
	s_addc_u32 s17, s1, 0
	global_load_dwordx4 v[94:97], v153, s[16:17] offset:0
	global_load_dwordx4 v[160:163], v153, s[16:17] offset:64
	global_load_dwordx4 v[164:167], v153, s[16:17] offset:128
	global_load_dwordx4 v[182:185], v153, s[16:17] offset:192
	v_cvt_pk_bf16_f32 v168, v26, v27
	v_cvt_pk_bf16_f32 v169, v28, v29
	global_store_dwordx2 v157, v[168:169], s[20:21]
	v_cvt_pk_bf16_f32 v176, v30, v31
	v_cvt_pk_bf16_f32 v177, v32, v33
	global_store_dwordx2 v158, v[176:177], s[20:21]
	s_waitcnt vmcnt(14)
	v_mfma_f32_16x16x32_bf16 v[26:29], v[218:221], v[18:21], 0
	v_mfma_f32_16x16x32_bf16 v[26:29], v[234:237], v[22:25], v[26:29]
	v_mfma_f32_16x16x32_bf16 v[26:29], v[238:241], v[38:41], v[26:29]
	v_mfma_f32_16x16x32_bf16 v[26:29], v[242:245], v[42:45], v[26:29]
	v_mfma_f32_16x16x32_bf16 v[30:33], v[218:221], v[46:49], 0
	v_mfma_f32_16x16x32_bf16 v[30:33], v[234:237], v[50:53], v[30:33]
	v_mfma_f32_16x16x32_bf16 v[30:33], v[238:241], v[54:57], v[30:33]
	v_mfma_f32_16x16x32_bf16 v[30:33], v[242:245], v[58:61], v[30:33]
	s_add_u32 s20, s54, 0x20
	s_addc_u32 s21, s55, 0
	s_nop 7
	s_add_u32 s16, s0, 0x65000
	s_addc_u32 s17, s1, 0
	global_load_dwordx4 v[218:221], v153, s[16:17] offset:0
	global_load_dwordx4 v[234:237], v153, s[16:17] offset:64
	global_load_dwordx4 v[238:241], v153, s[16:17] offset:128
	global_load_dwordx4 v[242:245], v153, s[16:17] offset:192
	v_cvt_pk_bf16_f32 v168, v26, v27
	v_cvt_pk_bf16_f32 v169, v28, v29
	global_store_dwordx2 v157, v[168:169], s[20:21]
	v_cvt_pk_bf16_f32 v176, v30, v31
	v_cvt_pk_bf16_f32 v177, v32, v33
	global_store_dwordx2 v158, v[176:177], s[20:21]
	s_waitcnt vmcnt(16)
	v_mfma_f32_16x16x32_bf16 v[26:29], v[62:65], v[18:21], 0
	v_mfma_f32_16x16x32_bf16 v[26:29], v[66:69], v[22:25], v[26:29]
	v_mfma_f32_16x16x32_bf16 v[26:29], v[70:73], v[38:41], v[26:29]
	v_mfma_f32_16x16x32_bf16 v[26:29], v[74:77], v[42:45], v[26:29]
	v_mfma_f32_16x16x32_bf16 v[30:33], v[62:65], v[46:49], 0
	v_mfma_f32_16x16x32_bf16 v[30:33], v[66:69], v[50:53], v[30:33]
	v_mfma_f32_16x16x32_bf16 v[30:33], v[70:73], v[54:57], v[30:33]
	v_mfma_f32_16x16x32_bf16 v[30:33], v[74:77], v[58:61], v[30:33]
	s_add_u32 s20, s54, 0x40
	s_addc_u32 s21, s55, 0
	s_nop 7
	s_add_u32 s16, s0, 0x66000
	s_addc_u32 s17, s1, 0
	global_load_dwordx4 v[62:65], v153, s[16:17] offset:0
	global_load_dwordx4 v[66:69], v153, s[16:17] offset:64
	global_load_dwordx4 v[70:73], v153, s[16:17] offset:128
	global_load_dwordx4 v[74:77], v153, s[16:17] offset:192
	v_cvt_pk_bf16_f32 v168, v26, v27
	v_cvt_pk_bf16_f32 v169, v28, v29
	global_store_dwordx2 v157, v[168:169], s[20:21]
	v_cvt_pk_bf16_f32 v176, v30, v31
	v_cvt_pk_bf16_f32 v177, v32, v33
	global_store_dwordx2 v158, v[176:177], s[20:21]
	s_waitcnt vmcnt(18)
	v_mfma_f32_16x16x32_bf16 v[26:29], v[78:81], v[18:21], 0
	v_mfma_f32_16x16x32_bf16 v[26:29], v[82:85], v[22:25], v[26:29]
	v_mfma_f32_16x16x32_bf16 v[26:29], v[86:89], v[38:41], v[26:29]
	v_mfma_f32_16x16x32_bf16 v[26:29], v[90:93], v[42:45], v[26:29]
	v_mfma_f32_16x16x32_bf16 v[30:33], v[78:81], v[46:49], 0
	v_mfma_f32_16x16x32_bf16 v[30:33], v[82:85], v[50:53], v[30:33]
	v_mfma_f32_16x16x32_bf16 v[30:33], v[86:89], v[54:57], v[30:33]
	v_mfma_f32_16x16x32_bf16 v[30:33], v[90:93], v[58:61], v[30:33]
	s_add_u32 s20, s54, 0x60
	s_addc_u32 s21, s55, 0
	s_nop 7
	s_add_u32 s16, s0, 0x67000
	s_addc_u32 s17, s1, 0
	global_load_dwordx4 v[78:81], v153, s[16:17] offset:0
	global_load_dwordx4 v[82:85], v153, s[16:17] offset:64
	global_load_dwordx4 v[86:89], v153, s[16:17] offset:128
	global_load_dwordx4 v[90:93], v153, s[16:17] offset:192
	v_cvt_pk_bf16_f32 v168, v26, v27
	v_cvt_pk_bf16_f32 v169, v28, v29
	global_store_dwordx2 v157, v[168:169], s[20:21]
	v_cvt_pk_bf16_f32 v176, v30, v31
	v_cvt_pk_bf16_f32 v177, v32, v33
	global_store_dwordx2 v158, v[176:177], s[20:21]
	s_waitcnt vmcnt(20)
	v_mfma_f32_16x16x32_bf16 v[26:29], v[94:97], v[18:21], 0
	v_mfma_f32_16x16x32_bf16 v[26:29], v[160:163], v[22:25], v[26:29]
	v_mfma_f32_16x16x32_bf16 v[26:29], v[164:167], v[38:41], v[26:29]
	v_mfma_f32_16x16x32_bf16 v[26:29], v[182:185], v[42:45], v[26:29]
	v_mfma_f32_16x16x32_bf16 v[30:33], v[94:97], v[46:49], 0
	v_mfma_f32_16x16x32_bf16 v[30:33], v[160:163], v[50:53], v[30:33]
	v_mfma_f32_16x16x32_bf16 v[30:33], v[164:167], v[54:57], v[30:33]
	v_mfma_f32_16x16x32_bf16 v[30:33], v[182:185], v[58:61], v[30:33]
	s_add_u32 s20, s54, 0x80
	s_addc_u32 s21, s55, 0
	s_nop 7
	s_add_u32 s16, s0, 0x68000
	s_addc_u32 s17, s1, 0
	global_load_dwordx4 v[94:97], v153, s[16:17] offset:0
	global_load_dwordx4 v[160:163], v153, s[16:17] offset:64
	global_load_dwordx4 v[164:167], v153, s[16:17] offset:128
	global_load_dwordx4 v[182:185], v153, s[16:17] offset:192
	v_cvt_pk_bf16_f32 v168, v26, v27
	v_cvt_pk_bf16_f32 v169, v28, v29
	global_store_dwordx2 v157, v[168:169], s[20:21]
	v_cvt_pk_bf16_f32 v176, v30, v31
	v_cvt_pk_bf16_f32 v177, v32, v33
	global_store_dwordx2 v158, v[176:177], s[20:21]
	s_waitcnt vmcnt(20)
	v_mfma_f32_16x16x32_bf16 v[26:29], v[218:221], v[18:21], 0
	v_mfma_f32_16x16x32_bf16 v[26:29], v[234:237], v[22:25], v[26:29]
	v_mfma_f32_16x16x32_bf16 v[26:29], v[238:241], v[38:41], v[26:29]
	v_mfma_f32_16x16x32_bf16 v[26:29], v[242:245], v[42:45], v[26:29]
	v_mfma_f32_16x16x32_bf16 v[30:33], v[218:221], v[46:49], 0
	v_mfma_f32_16x16x32_bf16 v[30:33], v[234:237], v[50:53], v[30:33]
	v_mfma_f32_16x16x32_bf16 v[30:33], v[238:241], v[54:57], v[30:33]
	v_mfma_f32_16x16x32_bf16 v[30:33], v[242:245], v[58:61], v[30:33]
	s_add_u32 s20, s54, 0xa0
	s_addc_u32 s21, s55, 0
	s_nop 7
	v_cvt_pk_bf16_f32 v168, v26, v27
	v_cvt_pk_bf16_f32 v169, v28, v29
	global_store_dwordx2 v157, v[168:169], s[20:21]
	v_cvt_pk_bf16_f32 v176, v30, v31
	v_cvt_pk_bf16_f32 v177, v32, v33
	global_store_dwordx2 v158, v[176:177], s[20:21]
	s_waitcnt vmcnt(16)
	v_mfma_f32_16x16x32_bf16 v[26:29], v[62:65], v[18:21], 0
	v_mfma_f32_16x16x32_bf16 v[26:29], v[66:69], v[22:25], v[26:29]
	v_mfma_f32_16x16x32_bf16 v[26:29], v[70:73], v[38:41], v[26:29]
	v_mfma_f32_16x16x32_bf16 v[26:29], v[74:77], v[42:45], v[26:29]
	v_mfma_f32_16x16x32_bf16 v[30:33], v[62:65], v[46:49], 0
	v_mfma_f32_16x16x32_bf16 v[30:33], v[66:69], v[50:53], v[30:33]
	v_mfma_f32_16x16x32_bf16 v[30:33], v[70:73], v[54:57], v[30:33]
	v_mfma_f32_16x16x32_bf16 v[30:33], v[74:77], v[58:61], v[30:33]
	s_add_u32 s20, s54, 0xc0
	s_addc_u32 s21, s55, 0
	s_nop 7
	v_cvt_pk_bf16_f32 v168, v26, v27
	v_cvt_pk_bf16_f32 v169, v28, v29
	global_store_dwordx2 v157, v[168:169], s[20:21]
	v_cvt_pk_bf16_f32 v176, v30, v31
	v_cvt_pk_bf16_f32 v177, v32, v33
	global_store_dwordx2 v158, v[176:177], s[20:21]
	s_waitcnt vmcnt(12)
	v_mfma_f32_16x16x32_bf16 v[26:29], v[78:81], v[18:21], 0
	v_mfma_f32_16x16x32_bf16 v[26:29], v[82:85], v[22:25], v[26:29]
	v_mfma_f32_16x16x32_bf16 v[26:29], v[86:89], v[38:41], v[26:29]
	v_mfma_f32_16x16x32_bf16 v[26:29], v[90:93], v[42:45], v[26:29]
	v_mfma_f32_16x16x32_bf16 v[30:33], v[78:81], v[46:49], 0
	v_mfma_f32_16x16x32_bf16 v[30:33], v[82:85], v[50:53], v[30:33]
	v_mfma_f32_16x16x32_bf16 v[30:33], v[86:89], v[54:57], v[30:33]
	v_mfma_f32_16x16x32_bf16 v[30:33], v[90:93], v[58:61], v[30:33]
	s_add_u32 s20, s54, 0xe0
	s_addc_u32 s21, s55, 0
	s_nop 7
	v_cvt_pk_bf16_f32 v168, v26, v27
	v_cvt_pk_bf16_f32 v169, v28, v29
	global_store_dwordx2 v157, v[168:169], s[20:21]
	v_cvt_pk_bf16_f32 v176, v30, v31
	v_cvt_pk_bf16_f32 v177, v32, v33
	global_store_dwordx2 v158, v[176:177], s[20:21]
	s_waitcnt vmcnt(8)
	v_mfma_f32_16x16x32_bf16 v[26:29], v[94:97], v[18:21], 0
	v_mfma_f32_16x16x32_bf16 v[26:29], v[160:163], v[22:25], v[26:29]
	v_mfma_f32_16x16x32_bf16 v[26:29], v[164:167], v[38:41], v[26:29]
	v_mfma_f32_16x16x32_bf16 v[26:29], v[182:185], v[42:45], v[26:29]
	v_mfma_f32_16x16x32_bf16 v[30:33], v[94:97], v[46:49], 0
	v_mfma_f32_16x16x32_bf16 v[30:33], v[160:163], v[50:53], v[30:33]
	v_mfma_f32_16x16x32_bf16 v[30:33], v[164:167], v[54:57], v[30:33]
	v_mfma_f32_16x16x32_bf16 v[30:33], v[182:185], v[58:61], v[30:33]
	s_add_u32 s20, s54, 0x100
	s_addc_u32 s21, s55, 0
	s_nop 7
	v_cvt_pk_bf16_f32 v168, v26, v27
	v_cvt_pk_bf16_f32 v169, v28, v29
	global_store_dwordx2 v157, v[168:169], s[20:21]
	v_cvt_pk_bf16_f32 v176, v30, v31
	v_cvt_pk_bf16_f32 v177, v32, v33
	global_store_dwordx2 v158, v[176:177], s[20:21]
	s_branch .LBB0_402
.Lb3w_7:
	ds_read_b128 v[2:5], v0 offset:256
	ds_read_b128 v[6:9], v0 offset:320
	ds_read_b128 v[10:13], v0 offset:384
	ds_read_b128 v[14:17], v0 offset:448
	ds_read_b128 v[18:21], v0 offset:8704
	ds_read_b128 v[22:25], v0 offset:8768
	ds_read_b128 v[38:41], v0 offset:8832
	ds_read_b128 v[42:45], v0 offset:8896
	s_add_u32 s16, s0, 0x69000
	s_addc_u32 s17, s1, 0
	global_load_dwordx4 v[46:49], v153, s[16:17] offset:0
	global_load_dwordx4 v[50:53], v153, s[16:17] offset:64
	global_load_dwordx4 v[54:57], v153, s[16:17] offset:128
	global_load_dwordx4 v[58:61], v153, s[16:17] offset:192
	s_add_u32 s16, s0, 0x6a000
	s_addc_u32 s17, s1, 0
	global_load_dwordx4 v[62:65], v153, s[16:17] offset:0
	global_load_dwordx4 v[66:69], v153, s[16:17] offset:64
	global_load_dwordx4 v[70:73], v153, s[16:17] offset:128
	global_load_dwordx4 v[74:77], v153, s[16:17] offset:192
	s_add_u32 s16, s0, 0x6b000
	s_addc_u32 s17, s1, 0
	global_load_dwordx4 v[78:81], v153, s[16:17] offset:0
	global_load_dwordx4 v[82:85], v153, s[16:17] offset:64
	global_load_dwordx4 v[86:89], v153, s[16:17] offset:128
	global_load_dwordx4 v[90:93], v153, s[16:17] offset:192
	s_add_u32 s16, s0, 0x6c000
	s_addc_u32 s17, s1, 0
	global_load_dwordx4 v[94:97], v153, s[16:17] offset:0
	global_load_dwordx4 v[160:163], v153, s[16:17] offset:64
	global_load_dwordx4 v[164:167], v153, s[16:17] offset:128
	global_load_dwordx4 v[182:185], v153, s[16:17] offset:192
	s_add_u32 s16, s0, 0x6d000
	s_addc_u32 s17, s1, 0
	global_load_dwordx4 v[218:221], v153, s[16:17] offset:0
	global_load_dwordx4 v[234:237], v153, s[16:17] offset:64
	global_load_dwordx4 v[238:241], v153, s[16:17] offset:128
	global_load_dwordx4 v[242:245], v153, s[16:17] offset:192
	s_waitcnt vmcnt(16) lgkmcnt(0)
	v_mfma_f32_16x16x32_bf16 v[26:29], v[46:49], v[2:5], 0
	v_mfma_f32_16x16x32_bf16 v[26:29], v[50:53], v[6:9], v[26:29]
	v_mfma_f32_16x16x32_bf16 v[26:29], v[54:57], v[10:13], v[26:29]
	v_mfma_f32_16x16x32_bf16 v[26:29], v[58:61], v[14:17], v[26:29]
	v_mfma_f32_16x16x32_bf16 v[30:33], v[46:49], v[18:21], 0
	v_mfma_f32_16x16x32_bf16 v[30:33], v[50:53], v[22:25], v[30:33]
	v_mfma_f32_16x16x32_bf16 v[30:33], v[54:57], v[38:41], v[30:33]
	v_mfma_f32_16x16x32_bf16 v[30:33], v[58:61], v[42:45], v[30:33]
	s_add_u32 s20, s54, 0x120
	s_addc_u32 s21, s55, 0
	s_nop 7
	s_add_u32 s16, s0, 0x6e000
	s_addc_u32 s17, s1, 0
	global_load_dwordx4 v[46:49], v153, s[16:17] offset:0
	global_load_dwordx4 v[50:53], v153, s[16:17] offset:64
	global_load_dwordx4 v[54:57], v153, s[16:17] offset:128
	global_load_dwordx4 v[58:61], v153, s[16:17] offset:192
	v_cvt_pk_bf16_f32 v168, v26, v27
	v_cvt_pk_bf16_f32 v169, v28, v29
	global_store_dwordx2 v157, v[168:169], s[20:21]
	v_cvt_pk_bf16_f32 v176, v30, v31
	v_cvt_pk_bf16_f32 v177, v32, v33
	global_store_dwordx2 v158, v[176:177], s[20:21]
	s_waitcnt vmcnt(18)
	v_mfma_f32_16x16x32_bf16 v[26:29], v[62:65], v[2:5], 0
	v_mfma_f32_16x16x32_bf16 v[26:29], v[66:69], v[6:9], v[26:29]
	v_mfma_f32_16x16x32_bf16 v[26:29], v[70:73], v[10:13], v[26:29]
	v_mfma_f32_16x16x32_bf16 v[26:29], v[74:77], v[14:17], v[26:29]
	v_mfma_f32_16x16x32_bf16 v[30:33], v[62:65], v[18:21], 0
	v_mfma_f32_16x16x32_bf16 v[30:33], v[66:69], v[22:25], v[30:33]
	v_mfma_f32_16x16x32_bf16 v[30:33], v[70:73], v[38:41], v[30:33]
	v_mfma_f32_16x16x32_bf16 v[30:33], v[74:77], v[42:45], v[30:33]
	s_add_u32 s20, s54, 0x140
	s_addc_u32 s21, s55, 0
	s_nop 7
	s_add_u32 s16, s0, 0x6f000
	s_addc_u32 s17, s1, 0
	global_load_dwordx4 v[62:65], v153, s[16:17] offset:0
	global_load_dwordx4 v[66:69], v153, s[16:17] offset:64
	global_load_dwordx4 v[70:73], v153, s[16:17] offset:128
	global_load_dwordx4 v[74:77], v153, s[16:17] offset:192
	v_cvt_pk_bf16_f32 v168, v26, v27
	v_cvt_pk_bf16_f32 v169, v28, v29
	global_store_dwordx2 v157, v[168:169], s[20:21]
	v_cvt_pk_bf16_f32 v176, v30, v31
	v_cvt_pk_bf16_f32 v177, v32, v33
	global_store_dwordx2 v158, v[176:177], s[20:21]
	s_waitcnt vmcnt(20)
	v_mfma_f32_16x16x32_bf16 v[26:29], v[78:81], v[2:5], 0
	v_mfma_f32_16x16x32_bf16 v[26:29], v[82:85], v[6:9], v[26:29]
	v_mfma_f32_16x16x32_bf16 v[26:29], v[86:89], v[10:13], v[26:29]
	v_mfma_f32_16x16x32_bf16 v[26:29], v[90:93], v[14:17], v[26:29]
	v_mfma_f32_16x16x32_bf16 v[30:33], v[78:81], v[18:21], 0
	v_mfma_f32_16x16x32_bf16 v[30:33], v[82:85], v[22:25], v[30:33]
	v_mfma_f32_16x16x32_bf16 v[30:33], v[86:89], v[38:41], v[30:33]
	v_mfma_f32_16x16x32_bf16 v[30:33], v[90:93], v[42:45], v[30:33]
	s_add_u32 s20, s54, 0x160
	s_addc_u32 s21, s55, 0
	s_nop 7
	s_add_u32 s16, s0, 0x70000
	s_addc_u32 s17, s1, 0
	global_load_dwordx4 v[78:81], v153, s[16:17] offset:0
	global_load_dwordx4 v[82:85], v153, s[16:17] offset:64
	global_load_dwordx4 v[86:89], v153, s[16:17] offset:128
	global_load_dwordx4 v[90:93], v153, s[16:17] offset:192
	v_cvt_pk_bf16_f32 v168, v26, v27
	v_cvt_pk_bf16_f32 v169, v28, v29
	global_store_dwordx2 v157, v[168:169], s[20:21]
	v_cvt_pk_bf16_f32 v176, v30, v31
	v_cvt_pk_bf16_f32 v177, v32, v33
	global_store_dwordx2 v158, v[176:177], s[20:21]
	s_waitcnt vmcnt(22)
	v_mfma_f32_16x16x32_bf16 v[26:29], v[94:97], v[2:5], 0
	v_mfma_f32_16x16x32_bf16 v[26:29], v[160:163], v[6:9], v[26:29]
	v_mfma_f32_16x16x32_bf16 v[26:29], v[164:167], v[10:13], v[26:29]
	v_mfma_f32_16x16x32_bf16 v[26:29], v[182:185], v[14:17], v[26:29]
	v_mfma_f32_16x16x32_bf16 v[30:33], v[94:97], v[18:21], 0
	v_mfma_f32_16x16x32_bf16 v[30:33], v[160:163], v[22:25], v[30:33]
	v_mfma_f32_16x16x32_bf16 v[30:33], v[164:167], v[38:41], v[30:33]
	v_mfma_f32_16x16x32_bf16 v[30:33], v[182:185], v[42:45], v[30:33]
	s_add_u32 s20, s54, 0x180
	s_addc_u32 s21, s55, 0
	s_nop 7
	s_add_u32 s16, s0, 0x71000
	s_addc_u32 s17, s1, 0
	global_load_dwordx4 v[94:97], v153, s[16:17] offset:0
	global_load_dwordx4 v[160:163], v153, s[16:17] offset:64
	global_load_dwordx4 v[164:167], v153, s[16:17] offset:128
	global_load_dwordx4 v[182:185], v153, s[16:17] offset:192
	v_cvt_pk_bf16_f32 v168, v26, v27
	v_cvt_pk_bf16_f32 v169, v28, v29
	global_store_dwordx2 v157, v[168:169], s[20:21]
	v_cvt_pk_bf16_f32 v176, v30, v31
	v_cvt_pk_bf16_f32 v177, v32, v33
	global_store_dwordx2 v158, v[176:177], s[20:21]
	s_waitcnt vmcnt(24)
	v_mfma_f32_16x16x32_bf16 v[26:29], v[218:221], v[2:5], 0
	v_mfma_f32_16x16x32_bf16 v[26:29], v[234:237], v[6:9], v[26:29]
	v_mfma_f32_16x16x32_bf16 v[26:29], v[238:241], v[10:13], v[26:29]
	v_mfma_f32_16x16x32_bf16 v[26:29], v[242:245], v[14:17], v[26:29]
	v_mfma_f32_16x16x32_bf16 v[30:33], v[218:221], v[18:21], 0
	v_mfma_f32_16x16x32_bf16 v[30:33], v[234:237], v[22:25], v[30:33]
	v_mfma_f32_16x16x32_bf16 v[30:33], v[238:241], v[38:41], v[30:33]
	v_mfma_f32_16x16x32_bf16 v[30:33], v[242:245], v[42:45], v[30:33]
	s_add_u32 s20, s54, 0x1a0
	s_addc_u32 s21, s55, 0
	s_nop 7
	s_add_u32 s16, s0, 0x72000
	s_addc_u32 s17, s1, 0
	global_load_dwordx4 v[218:221], v153, s[16:17] offset:0
	global_load_dwordx4 v[234:237], v153, s[16:17] offset:64
	global_load_dwordx4 v[238:241], v153, s[16:17] offset:128
	global_load_dwordx4 v[242:245], v153, s[16:17] offset:192
	v_cvt_pk_bf16_f32 v168, v26, v27
	v_cvt_pk_bf16_f32 v169, v28, v29
	global_store_dwordx2 v157, v[168:169], s[20:21]
	v_cvt_pk_bf16_f32 v176, v30, v31
	v_cvt_pk_bf16_f32 v177, v32, v33
	global_store_dwordx2 v158, v[176:177], s[20:21]
	s_waitcnt vmcnt(26)
	v_mfma_f32_16x16x32_bf16 v[26:29], v[46:49], v[2:5], 0
	v_mfma_f32_16x16x32_bf16 v[26:29], v[50:53], v[6:9], v[26:29]
	v_mfma_f32_16x16x32_bf16 v[26:29], v[54:57], v[10:13], v[26:29]
	v_mfma_f32_16x16x32_bf16 v[26:29], v[58:61], v[14:17], v[26:29]
	v_mfma_f32_16x16x32_bf16 v[30:33], v[46:49], v[18:21], 0
	v_mfma_f32_16x16x32_bf16 v[30:33], v[50:53], v[22:25], v[30:33]
	v_mfma_f32_16x16x32_bf16 v[30:33], v[54:57], v[38:41], v[30:33]
	v_mfma_f32_16x16x32_bf16 v[30:33], v[58:61], v[42:45], v[30:33]
	s_add_u32 s20, s54, 0x1c0
	s_addc_u32 s21, s55, 0
	s_nop 7
	s_add_u32 s16, s0, 0x73000
	s_addc_u32 s17, s1, 0
	global_load_dwordx4 v[46:49], v153, s[16:17] offset:0
	global_load_dwordx4 v[50:53], v153, s[16:17] offset:64
	global_load_dwordx4 v[54:57], v153, s[16:17] offset:128
	global_load_dwordx4 v[58:61], v153, s[16:17] offset:192
	v_cvt_pk_bf16_f32 v168, v26, v27
	v_cvt_pk_bf16_f32 v169, v28, v29
	global_store_dwordx2 v157, v[168:169], s[20:21]
	v_cvt_pk_bf16_f32 v176, v30, v31
	v_cvt_pk_bf16_f32 v177, v32, v33
	global_store_dwordx2 v158, v[176:177], s[20:21]
	s_waitcnt vmcnt(26)
	v_mfma_f32_16x16x32_bf16 v[26:29], v[62:65], v[2:5], 0
	v_mfma_f32_16x16x32_bf16 v[26:29], v[66:69], v[6:9], v[26:29]
	v_mfma_f32_16x16x32_bf16 v[26:29], v[70:73], v[10:13], v[26:29]
	v_mfma_f32_16x16x32_bf16 v[26:29], v[74:77], v[14:17], v[26:29]
	v_mfma_f32_16x16x32_bf16 v[30:33], v[62:65], v[18:21], 0
	v_mfma_f32_16x16x32_bf16 v[30:33], v[66:69], v[22:25], v[30:33]
	v_mfma_f32_16x16x32_bf16 v[30:33], v[70:73], v[38:41], v[30:33]
	v_mfma_f32_16x16x32_bf16 v[30:33], v[74:77], v[42:45], v[30:33]
	s_add_u32 s20, s54, 0x1e0
	s_addc_u32 s21, s55, 0
	s_nop 7
	s_add_u32 s16, s0, 0x74000
	s_addc_u32 s17, s1, 0
	global_load_dwordx4 v[62:65], v153, s[16:17] offset:0
	global_load_dwordx4 v[66:69], v153, s[16:17] offset:64
	global_load_dwordx4 v[70:73], v153, s[16:17] offset:128
	global_load_dwordx4 v[74:77], v153, s[16:17] offset:192
	v_cvt_pk_bf16_f32 v168, v26, v27
	v_cvt_pk_bf16_f32 v169, v28, v29
	global_store_dwordx2 v157, v[168:169], s[20:21]
	v_cvt_pk_bf16_f32 v176, v30, v31
	v_cvt_pk_bf16_f32 v177, v32, v33
	global_store_dwordx2 v158, v[176:177], s[20:21]
	s_waitcnt vmcnt(26)
	v_mfma_f32_16x16x32_bf16 v[26:29], v[78:81], v[2:5], 0
	v_mfma_f32_16x16x32_bf16 v[26:29], v[82:85], v[6:9], v[26:29]
	v_mfma_f32_16x16x32_bf16 v[26:29], v[86:89], v[10:13], v[26:29]
	v_mfma_f32_16x16x32_bf16 v[26:29], v[90:93], v[14:17], v[26:29]
	v_mfma_f32_16x16x32_bf16 v[30:33], v[78:81], v[18:21], 0
	v_mfma_f32_16x16x32_bf16 v[30:33], v[82:85], v[22:25], v[30:33]
	v_mfma_f32_16x16x32_bf16 v[30:33], v[86:89], v[38:41], v[30:33]
	v_mfma_f32_16x16x32_bf16 v[30:33], v[90:93], v[42:45], v[30:33]
	s_add_u32 s20, s54, 0x200
	s_addc_u32 s21, s55, 0
	s_nop 7
	s_add_u32 s16, s0, 0x75000
	s_addc_u32 s17, s1, 0
	global_load_dwordx4 v[78:81], v153, s[16:17] offset:0
	global_load_dwordx4 v[82:85], v153, s[16:17] offset:64
	global_load_dwordx4 v[86:89], v153, s[16:17] offset:128
	global_load_dwordx4 v[90:93], v153, s[16:17] offset:192
	v_cvt_pk_bf16_f32 v168, v26, v27
	v_cvt_pk_bf16_f32 v169, v28, v29
	global_store_dwordx2 v157, v[168:169], s[20:21]
	v_cvt_pk_bf16_f32 v176, v30, v31
	v_cvt_pk_bf16_f32 v177, v32, v33
	global_store_dwordx2 v158, v[176:177], s[20:21]
	s_waitcnt vmcnt(26)
	v_mfma_f32_16x16x32_bf16 v[26:29], v[94:97], v[2:5], 0
	v_mfma_f32_16x16x32_bf16 v[26:29], v[160:163], v[6:9], v[26:29]
	v_mfma_f32_16x16x32_bf16 v[26:29], v[164:167], v[10:13], v[26:29]
	v_mfma_f32_16x16x32_bf16 v[26:29], v[182:185], v[14:17], v[26:29]
	v_mfma_f32_16x16x32_bf16 v[30:33], v[94:97], v[18:21], 0
	v_mfma_f32_16x16x32_bf16 v[30:33], v[160:163], v[22:25], v[30:33]
	v_mfma_f32_16x16x32_bf16 v[30:33], v[164:167], v[38:41], v[30:33]
	v_mfma_f32_16x16x32_bf16 v[30:33], v[182:185], v[42:45], v[30:33]
	s_add_u32 s20, s54, 0x220
	s_addc_u32 s21, s55, 0
	s_nop 7
	s_add_u32 s16, s0, 0x76000
	s_addc_u32 s17, s1, 0
	global_load_dwordx4 v[94:97], v153, s[16:17] offset:0
	global_load_dwordx4 v[160:163], v153, s[16:17] offset:64
	global_load_dwordx4 v[164:167], v153, s[16:17] offset:128
	global_load_dwordx4 v[182:185], v153, s[16:17] offset:192
	v_cvt_pk_bf16_f32 v168, v26, v27
	v_cvt_pk_bf16_f32 v169, v28, v29
	global_store_dwordx2 v157, v[168:169], s[20:21]
	v_cvt_pk_bf16_f32 v176, v30, v31
	v_cvt_pk_bf16_f32 v177, v32, v33
	global_store_dwordx2 v158, v[176:177], s[20:21]
	s_waitcnt vmcnt(26)
	v_mfma_f32_16x16x32_bf16 v[26:29], v[218:221], v[2:5], 0
	v_mfma_f32_16x16x32_bf16 v[26:29], v[234:237], v[6:9], v[26:29]
	v_mfma_f32_16x16x32_bf16 v[26:29], v[238:241], v[10:13], v[26:29]
	v_mfma_f32_16x16x32_bf16 v[26:29], v[242:245], v[14:17], v[26:29]
	v_mfma_f32_16x16x32_bf16 v[30:33], v[218:221], v[18:21], 0
	v_mfma_f32_16x16x32_bf16 v[30:33], v[234:237], v[22:25], v[30:33]
	v_mfma_f32_16x16x32_bf16 v[30:33], v[238:241], v[38:41], v[30:33]
	v_mfma_f32_16x16x32_bf16 v[30:33], v[242:245], v[42:45], v[30:33]
	s_add_u32 s20, s54, 0x240
	s_addc_u32 s21, s55, 0
	s_nop 7
	s_add_u32 s16, s0, 0x77000
	s_addc_u32 s17, s1, 0
	global_load_dwordx4 v[218:221], v153, s[16:17] offset:0
	global_load_dwordx4 v[234:237], v153, s[16:17] offset:64
	global_load_dwordx4 v[238:241], v153, s[16:17] offset:128
	global_load_dwordx4 v[242:245], v153, s[16:17] offset:192
	v_cvt_pk_bf16_f32 v168, v26, v27
	v_cvt_pk_bf16_f32 v169, v28, v29
	global_store_dwordx2 v157, v[168:169], s[20:21]
	v_cvt_pk_bf16_f32 v176, v30, v31
	v_cvt_pk_bf16_f32 v177, v32, v33
	global_store_dwordx2 v158, v[176:177], s[20:21]
	s_waitcnt vmcnt(26)
	v_mfma_f32_16x16x32_bf16 v[26:29], v[46:49], v[2:5], 0
	v_mfma_f32_16x16x32_bf16 v[26:29], v[50:53], v[6:9], v[26:29]
	v_mfma_f32_16x16x32_bf16 v[26:29], v[54:57], v[10:13], v[26:29]
	v_mfma_f32_16x16x32_bf16 v[26:29], v[58:61], v[14:17], v[26:29]
	v_mfma_f32_16x16x32_bf16 v[30:33], v[46:49], v[18:21], 0
	v_mfma_f32_16x16x32_bf16 v[30:33], v[50:53], v[22:25], v[30:33]
	v_mfma_f32_16x16x32_bf16 v[30:33], v[54:57], v[38:41], v[30:33]
	v_mfma_f32_16x16x32_bf16 v[30:33], v[58:61], v[42:45], v[30:33]
	s_add_u32 s20, s54, 0x260
	s_addc_u32 s21, s55, 0
	s_nop 7
	v_cvt_pk_bf16_f32 v168, v26, v27
	v_cvt_pk_bf16_f32 v169, v28, v29
	global_store_dwordx2 v157, v[168:169], s[20:21]
	v_cvt_pk_bf16_f32 v176, v30, v31
	v_cvt_pk_bf16_f32 v177, v32, v33
	global_store_dwordx2 v158, v[176:177], s[20:21]
	s_waitcnt vmcnt(22)
	v_mfma_f32_16x16x32_bf16 v[26:29], v[62:65], v[2:5], 0
	v_mfma_f32_16x16x32_bf16 v[26:29], v[66:69], v[6:9], v[26:29]
	v_mfma_f32_16x16x32_bf16 v[26:29], v[70:73], v[10:13], v[26:29]
	v_mfma_f32_16x16x32_bf16 v[26:29], v[74:77], v[14:17], v[26:29]
	v_mfma_f32_16x16x32_bf16 v[30:33], v[62:65], v[18:21], 0
	v_mfma_f32_16x16x32_bf16 v[30:33], v[66:69], v[22:25], v[30:33]
	v_mfma_f32_16x16x32_bf16 v[30:33], v[70:73], v[38:41], v[30:33]
	v_mfma_f32_16x16x32_bf16 v[30:33], v[74:77], v[42:45], v[30:33]
	s_add_u32 s20, s54, 0x280
	s_addc_u32 s21, s55, 0
	s_nop 7
	v_cvt_pk_bf16_f32 v168, v26, v27
	v_cvt_pk_bf16_f32 v169, v28, v29
	global_store_dwordx2 v157, v[168:169], s[20:21]
	v_cvt_pk_bf16_f32 v176, v30, v31
	v_cvt_pk_bf16_f32 v177, v32, v33
	global_store_dwordx2 v158, v[176:177], s[20:21]
	s_waitcnt vmcnt(18)
	v_mfma_f32_16x16x32_bf16 v[26:29], v[78:81], v[2:5], 0
	v_mfma_f32_16x16x32_bf16 v[26:29], v[82:85], v[6:9], v[26:29]
	v_mfma_f32_16x16x32_bf16 v[26:29], v[86:89], v[10:13], v[26:29]
	v_mfma_f32_16x16x32_bf16 v[26:29], v[90:93], v[14:17], v[26:29]
	v_mfma_f32_16x16x32_bf16 v[30:33], v[78:81], v[18:21], 0
	v_mfma_f32_16x16x32_bf16 v[30:33], v[82:85], v[22:25], v[30:33]
	v_mfma_f32_16x16x32_bf16 v[30:33], v[86:89], v[38:41], v[30:33]
	v_mfma_f32_16x16x32_bf16 v[30:33], v[90:93], v[42:45], v[30:33]
	s_add_u32 s20, s54, 0x2a0
	s_addc_u32 s21, s55, 0
	s_nop 7
	v_cvt_pk_bf16_f32 v168, v26, v27
	v_cvt_pk_bf16_f32 v169, v28, v29
	global_store_dwordx2 v157, v[168:169], s[20:21]
	v_cvt_pk_bf16_f32 v176, v30, v31
	v_cvt_pk_bf16_f32 v177, v32, v33
	global_store_dwordx2 v158, v[176:177], s[20:21]
	s_waitcnt vmcnt(14)
	v_mfma_f32_16x16x32_bf16 v[26:29], v[94:97], v[2:5], 0
	v_mfma_f32_16x16x32_bf16 v[26:29], v[160:163], v[6:9], v[26:29]
	v_mfma_f32_16x16x32_bf16 v[26:29], v[164:167], v[10:13], v[26:29]
	v_mfma_f32_16x16x32_bf16 v[26:29], v[182:185], v[14:17], v[26:29]
	v_mfma_f32_16x16x32_bf16 v[30:33], v[94:97], v[18:21], 0
	v_mfma_f32_16x16x32_bf16 v[30:33], v[160:163], v[22:25], v[30:33]
	v_mfma_f32_16x16x32_bf16 v[30:33], v[164:167], v[38:41], v[30:33]
	v_mfma_f32_16x16x32_bf16 v[30:33], v[182:185], v[42:45], v[30:33]
	s_add_u32 s20, s54, 0x2c0
	s_addc_u32 s21, s55, 0
	s_nop 7
	v_cvt_pk_bf16_f32 v168, v26, v27
	v_cvt_pk_bf16_f32 v169, v28, v29
	global_store_dwordx2 v157, v[168:169], s[20:21]
	v_cvt_pk_bf16_f32 v176, v30, v31
	v_cvt_pk_bf16_f32 v177, v32, v33
	global_store_dwordx2 v158, v[176:177], s[20:21]
	s_waitcnt vmcnt(10)
	v_mfma_f32_16x16x32_bf16 v[26:29], v[218:221], v[2:5], 0
	v_mfma_f32_16x16x32_bf16 v[26:29], v[234:237], v[6:9], v[26:29]
	v_mfma_f32_16x16x32_bf16 v[26:29], v[238:241], v[10:13], v[26:29]
	v_mfma_f32_16x16x32_bf16 v[26:29], v[242:245], v[14:17], v[26:29]
	v_mfma_f32_16x16x32_bf16 v[30:33], v[218:221], v[18:21], 0
	v_mfma_f32_16x16x32_bf16 v[30:33], v[234:237], v[22:25], v[30:33]
	v_mfma_f32_16x16x32_bf16 v[30:33], v[238:241], v[38:41], v[30:33]
	v_mfma_f32_16x16x32_bf16 v[30:33], v[242:245], v[42:45], v[30:33]
	s_add_u32 s20, s54, 0x2e0
	s_addc_u32 s21, s55, 0
	s_nop 7
	v_cvt_pk_bf16_f32 v168, v26, v27
	v_cvt_pk_bf16_f32 v169, v28, v29
	global_store_dwordx2 v157, v[168:169], s[20:21]
	v_cvt_pk_bf16_f32 v176, v30, v31
	v_cvt_pk_bf16_f32 v177, v32, v33
	global_store_dwordx2 v158, v[176:177], s[20:21]
